# hg passes: dead denormal-prescale and inf-select of logf removed (argument clamped to [1e-30,1]); redundant s_nop before DPP scan blocks removed; router AB loads hoisted
# speedup vs baseline: 1.1321x; 1.0078x over previous
; #define LAS __attribute__((address_space(3)))
; __device__ __forceinline__ void lru_conv(const Frame& F, const LruRaw& R, const LAS float* CT, LAS float* ucb) {
;     const int tk = F.lane & 15, g = F.lane >> 4;
;     float acc[16];
; #pragma unroll
;     for (int q = 0; q < 4; ++q) { const f32x4 c4 = *(const LAS f32x4*)(CT + 4 * 64 + g * 16 + q * 4); acc[q * 4] = c4[0]; acc[q * 4 + 1] = c4[1]; acc[q * 4 + 2] = c4[2]; acc[q * 4 + 3] = c4[3]; }
; #pragma unroll
;     for (int tap = 0; tap < 4; ++tap) { float t0[8], t1[8]; const bool ok = (R.ok >> tap) & 1u; const u32x4 z4 = (u32x4){0u, 0u, 0u, 0u};
;         unpack8(ok ? R.a[tap] : z4, t0); unpack8(ok ? R.b[tap] : z4, t1);
; #pragma unroll
;         for (int q = 0; q < 2; ++q) { const f32x4 w0 = *(const LAS f32x4*)(CT + tap * 64 + g * 16 + q * 4), w1 = *(const LAS f32x4*)(CT + tap * 64 + g * 16 + 8 + q * 4);
; #pragma unroll
;             for (int i = 0; i < 4; ++i) { acc[q * 4 + i] = fmaf(w0[i], t0[q * 4 + i], acc[q * 4 + i]); acc[8 + q * 4 + i] = fmaf(w1[i], t1[q * 4 + i], acc[8 + q * 4 + i]); } } }
; #pragma unroll
;     for (int q = 0; q < 4; ++q) *(LAS f32x4*)(ucb + tk * 68 + g * 16 + q * 4) = (f32x4){acc[q * 4], acc[q * 4 + 1], acc[q * 4 + 2], acc[q * 4 + 3]};
.LBB0_466:
	v_bfe_i32 v145, v36, 0, 1
	ds_read_b128 v[38:41], v107
	ds_read_b128 v[42:45], v107 offset:16
	ds_read_b128 v[46:49], v107 offset:32
	ds_read_b128 v[50:53], v107 offset:48
	s_waitcnt vmcnt(0)
	v_and_b32_e32 v37, v145, v24
	v_and_b32_e32 v103, v145, v12
	ds_read_b128 v[54:57], v108
	ds_read_b128 v[58:61], v108 offset:16
	ds_read_b128 v[62:65], v108 offset:32
	ds_read_b128 v[66:69], v108 offset:48
	v_bfe_i32 v182, v36, 1, 1
	v_bfe_i32 v184, v36, 3, 1
	v_and_b32_sdwa v102, v145, v25 dst_sel:WORD_1 dst_unused:UNUSED_PAD src0_sel:DWORD src1_sel:DWORD
	v_and_b32_e32 v134, v182, v32
	ds_read_b128 v[70:73], v108 offset:256
	ds_read_b128 v[74:77], v108 offset:272
	ds_read_b128 v[78:81], v108 offset:288
	ds_read_b128 v[82:85], v108 offset:304
	v_bfe_i32 v183, v36, 2, 1
	v_and_b32_e32 v6, v184, v6
	v_and_b32_e32 v4, v184, v4
	v_lshlrev_b32_e32 v168, 16, v37
	v_and_b32_e32 v169, 0xffff0000, v37
	v_lshlrev_b32_e32 v190, 16, v103
	v_and_b32_e32 v191, 0xffff0000, v103
	v_bitop3_b32 v103, v145, s91, v25 bitop3:0x80
	v_and_b32_sdwa v154, v182, v33 dst_sel:WORD_1 dst_unused:UNUSED_PAD src0_sel:DWORD src1_sel:DWORD
	v_and_b32_e32 v135, v182, v20
	v_and_b32_e32 v136, v183, v28
	v_and_b32_e32 v137, v183, v16
	ds_read_b128 v[86:89], v108 offset:512
	ds_read_b128 v[122:125], v108 offset:528
	ds_read_b128 v[126:129], v108 offset:544
	ds_read_b128 v[130:133], v108 offset:560
	v_and_b32_sdwa v36, v184, v9 dst_sel:WORD_1 dst_unused:UNUSED_PAD src0_sel:DWORD src1_sel:DWORD
	v_and_b32_e32 v138, v184, v8
	v_and_b32_sdwa v8, v184, v7 dst_sel:WORD_1 dst_unused:UNUSED_PAD src0_sel:DWORD src1_sel:DWORD
	v_and_b32_sdwa v160, v184, v5 dst_sel:WORD_1 dst_unused:UNUSED_PAD src0_sel:DWORD src1_sel:DWORD
	v_lshlrev_b32_e32 v166, 16, v134
	v_and_b32_e32 v167, 0xffff0000, v134
	v_lshlrev_b32_e32 v192, 16, v4
	v_and_b32_e32 v193, 0xffff0000, v4
	v_bitop3_b32 v37, v184, s91, v9 bitop3:0x80
	v_bitop3_b32 v155, v182, s91, v33 bitop3:0x80
	v_bitop3_b32 v161, v184, s91, v5 bitop3:0x80
	v_lshlrev_b32_e32 v208, 16, v6
	v_and_b32_e32 v209, 0xffff0000, v6
	v_bitop3_b32 v9, v184, s91, v7 bitop3:0x80
	s_waitcnt lgkmcnt(11)
	v_pk_fma_f32 v[4:5], v[54:55], v[168:169], v[38:39]
	v_pk_fma_f32 v[6:7], v[56:57], v[102:103], v[40:41]
	v_and_b32_sdwa v156, v183, v29 dst_sel:WORD_1 dst_unused:UNUSED_PAD src0_sel:DWORD src1_sel:DWORD
	v_lshlrev_b32_e32 v162, 16, v138
	v_and_b32_e32 v163, 0xffff0000, v138
	v_lshlrev_b32_e32 v164, 16, v136
	v_and_b32_e32 v165, 0xffff0000, v136
	v_lshlrev_b32_e32 v170, 16, v137
	v_and_b32_e32 v171, 0xffff0000, v137
	v_lshlrev_b32_e32 v172, 16, v135
	v_and_b32_e32 v173, 0xffff0000, v135
	v_bitop3_b32 v157, v183, s91, v29 bitop3:0x80
	ds_read_b128 v[134:137], v108 offset:768
	ds_read_b128 v[138:141], v108 offset:784
	ds_read_b128 v[146:149], v108 offset:800
	ds_read_b128 v[150:153], v108 offset:816
	s_waitcnt lgkmcnt(11)
	v_pk_fma_f32 v[4:5], v[70:71], v[166:167], v[4:5]
	v_pk_fma_f32 v[6:7], v[72:73], v[154:155], v[6:7]
	v_and_b32_e32 v91, v145, v26
	s_waitcnt lgkmcnt(7)
	v_pk_fma_f32 v[4:5], v[86:87], v[164:165], v[4:5]
	v_pk_fma_f32 v[6:7], v[88:89], v[156:157], v[6:7]
	v_and_b32_sdwa v90, v145, v27 dst_sel:WORD_1 dst_unused:UNUSED_PAD src0_sel:DWORD src1_sel:DWORD
	v_and_b32_e32 v34, v182, v34
	v_lshlrev_b32_e32 v200, 16, v91
	v_and_b32_e32 v201, 0xffff0000, v91
	v_bitop3_b32 v91, v145, s91, v27 bitop3:0x80
	s_waitcnt lgkmcnt(3)
	v_pk_fma_f32 v[4:5], v[134:135], v[162:163], v[4:5]
	v_pk_fma_f32 v[6:7], v[136:137], v[36:37], v[6:7]
	v_and_b32_sdwa v142, v145, v13 dst_sel:WORD_1 dst_unused:UNUSED_PAD src0_sel:DWORD src1_sel:DWORD
	v_and_b32_sdwa v12, v182, v35 dst_sel:WORD_1 dst_unused:UNUSED_PAD src0_sel:DWORD src1_sel:DWORD
	v_and_b32_e32 v30, v183, v30
	v_bitop3_b32 v143, v145, s91, v13 bitop3:0x80
	v_lshlrev_b32_e32 v198, 16, v34
	v_and_b32_e32 v199, 0xffff0000, v34
	v_bitop3_b32 v13, v182, s91, v35 bitop3:0x80
	ds_write_b128 v109, v[4:7] offset:36864
	v_pk_fma_f32 v[4:5], v[58:59], v[200:201], v[42:43]
	v_pk_fma_f32 v[6:7], v[60:61], v[90:91], v[44:45]
	v_and_b32_sdwa v32, v182, v21 dst_sel:WORD_1 dst_unused:UNUSED_PAD src0_sel:DWORD src1_sel:DWORD
	v_and_b32_sdwa v20, v183, v31 dst_sel:WORD_1 dst_unused:UNUSED_PAD src0_sel:DWORD src1_sel:DWORD
	v_and_b32_e32 v10, v184, v10
	v_bitop3_b32 v33, v182, s91, v21 bitop3:0x80
	v_lshlrev_b32_e32 v196, 16, v30
	v_and_b32_e32 v197, 0xffff0000, v30
	v_bitop3_b32 v21, v183, s91, v31 bitop3:0x80
	v_pk_fma_f32 v[4:5], v[74:75], v[198:199], v[4:5]
	v_pk_fma_f32 v[6:7], v[76:77], v[12:13], v[6:7]
	v_and_b32_sdwa v158, v183, v17 dst_sel:WORD_1 dst_unused:UNUSED_PAD src0_sel:DWORD src1_sel:DWORD
	v_and_b32_sdwa v16, v184, v11 dst_sel:WORD_1 dst_unused:UNUSED_PAD src0_sel:DWORD src1_sel:DWORD
	v_bitop3_b32 v159, v183, s91, v17 bitop3:0x80
	v_lshlrev_b32_e32 v194, 16, v10
	v_and_b32_e32 v195, 0xffff0000, v10
	v_bitop3_b32 v17, v184, s91, v11 bitop3:0x80
	v_pk_fma_f32 v[4:5], v[122:123], v[196:197], v[4:5]
	v_pk_fma_f32 v[6:7], v[124:125], v[20:21], v[6:7]
	s_waitcnt lgkmcnt(3)
	v_pk_fma_f32 v[4:5], v[138:139], v[194:195], v[4:5]
	v_pk_fma_f32 v[6:7], v[140:141], v[16:17], v[6:7]
	s_mov_b32 s28, s30
	s_add_i32 s29, s2, s30
	ds_write_b128 v109, v[4:7] offset:36880
	v_pk_fma_f32 v[4:5], v[62:63], v[190:191], v[46:47]
	v_pk_fma_f32 v[6:7], v[64:65], v[142:143], v[48:49]
	s_add_i32 s30, s30, 8
	v_pk_fma_f32 v[4:5], v[78:79], v[172:173], v[4:5]
	v_pk_fma_f32 v[6:7], v[80:81], v[32:33], v[6:7]
	s_min_i32 s8, s30, s33
	v_and_b32_e32 v14, v145, v14
	v_pk_fma_f32 v[4:5], v[126:127], v[170:171], v[4:5]
	v_pk_fma_f32 v[6:7], v[128:129], v[158:159], v[6:7]
	s_add_i32 s8, s8, s2
	v_and_b32_sdwa v24, v145, v15 dst_sel:WORD_1 dst_unused:UNUSED_PAD src0_sel:DWORD src1_sel:DWORD
	v_and_b32_e32 v22, v182, v22
	v_lshlrev_b32_e32 v206, 16, v14
	v_and_b32_e32 v207, 0xffff0000, v14
	v_bitop3_b32 v25, v145, s91, v15 bitop3:0x80
	s_waitcnt lgkmcnt(3)
; #define LAS __attribute__((address_space(3)))
; __device__ __forceinline__ void lru_load(const Frame& F, int b, int kb, int nt, LruRaw& R) {
;     ...
;     for (int tap = 0; tap < 4; ++tap) { const int tp = tpos + tap - 2; const bool ok = (tp >= 0 && tp < len); const bf16_t* pr = pbase + (size_t)(ok ? tp : tpos) * 2048;
;         okm |= ok ? (1u << tap) : 0u;
;         R.a[tap] = *(const u32x4*)pr; R.b[tap] = *(const u32x4*)(pr + 8); }
; __device__ __forceinline__ void lru_gates(const Frame& F, LAS bf16_t* Wl, const LAS float* CT, LAS float* ucb, float (&av)[2][4][4], unsigned (&pw)[2][4][4]) {
;     ...
;     for (int ks = 0; ks < 2; ++ks) { const f32x4 u0 = *(const LAS f32x4*)(ucb + tk * 68 + ks * 32 + g * 8), u1 = *(const LAS f32x4*)(ucb + tk * 68 + ks * 32 + g * 8 + 4);
;         u32x4 w; w.x = cvt_pk_bf16(u0[0], u0[1]); w.y = cvt_pk_bf16(u0[2], u0[3]); w.z = cvt_pk_bf16(u1[0], u1[1]); w.w = cvt_pk_bf16(u1[2], u1[3]); __builtin_memcpy(&bfr[ks], &w, 16); }
; #pragma unroll
;     for (int d = 0; d < 2; ++d)
; #pragma unroll
;         for (int et = 0; et < 4; ++et) {
;             f32x4 ra = (f32x4){0.f, 0.f, 0.f, 0.f}, ri = (f32x4){0.f, 0.f, 0.f, 0.f};
; #pragma unroll
;             for (int ks = 0; ks < 2; ++ks) {
;                 const bf16x8 wa = *(const LAS bf16x8*)(Wl + ((d * 2 + 0) * 64 + et * 16 + tk) * 72 + ks * 32 + g * 8);
;                 const bf16x8 wx = *(const LAS bf16x8*)(Wl + ((d * 2 + 1) * 64 + et * 16 + tk) * 72 + ks * 32 + g * 8);
;                 ra = __builtin_amdgcn_mfma_f32_16x16x32_bf16(wa, bfr[ks], ra, 0, 0, 0);
;                 ri = __builtin_amdgcn_mfma_f32_16x16x32_bf16(wx, bfr[ks], ri, 0, 0, 0);
;             }
;             const f32x4 ba4 = *(const LAS f32x4*)(CT + (5 + 3 * d) * 64 + et * 16 + 4 * g), bx4 = *(const LAS f32x4*)(CT + (6 + 3 * d) * 64 + et * 16 + 4 * g), cs4 = *(const LAS f32x4*)(CT + (7 + 3 * d) * 64 + et * 16 + 4 * g);
;             const f32x4 u4 = *(const LAS f32x4*)(ucb + tk * 68 + et * 16 + 4 * g);
; #pragma unroll
;             for (int i = 0; i < 4; ++i) {
;                 const float r = sigmoidf_(ra[i] + ba4[i]), ig = sigmoidf_(ri[i] + bx4[i]);
;                 const float la = __uint_as_float(cvt_pk_bf16(cs4[i] * r, 0.f) << 16), a = __expf(la);
;                 av[d][et][i] = a; pw[d][et][i] = cvt_pk_bf16(la, __builtin_amdgcn_sqrtf(fmaxf(1.0f - a * a, 0.f)) * ig * u4[i]); }
	v_pk_fma_f32 v[4:5], v[146:147], v[192:193], v[4:5]
	v_pk_fma_f32 v[6:7], v[148:149], v[160:161], v[6:7]
	s_lshl_b32 s9, s8, 4
	v_and_b32_sdwa v26, v182, v23 dst_sel:WORD_1 dst_unused:UNUSED_PAD src0_sel:DWORD src1_sel:DWORD
	v_and_b32_e32 v18, v183, v18
	v_lshlrev_b32_e32 v204, 16, v22
	v_and_b32_e32 v205, 0xffff0000, v22
	v_bitop3_b32 v27, v182, s91, v23 bitop3:0x80
	ds_write_b128 v109, v[4:7] offset:36896
	v_pk_fma_f32 v[4:5], v[66:67], v[206:207], v[50:51]
	v_pk_fma_f32 v[6:7], v[68:69], v[24:25], v[52:53]
	s_add_i32 s10, s9, 0xffffff00
	v_and_b32_sdwa v28, v183, v19 dst_sel:WORD_1 dst_unused:UNUSED_PAD src0_sel:DWORD src1_sel:DWORD
	v_lshlrev_b32_e32 v202, 16, v18
	v_and_b32_e32 v203, 0xffff0000, v18
	v_bitop3_b32 v29, v183, s91, v19 bitop3:0x80
	v_pk_fma_f32 v[4:5], v[82:83], v[204:205], v[4:5]
	v_pk_fma_f32 v[6:7], v[84:85], v[26:27], v[6:7]
	s_cmp_lt_i32 s8, 16
	v_pk_fma_f32 v[4:5], v[130:131], v[202:203], v[4:5]
	v_pk_fma_f32 v[6:7], v[132:133], v[28:29], v[6:7]
	s_cselect_b32 s54, s9, s10
	s_waitcnt lgkmcnt(3)
	v_pk_fma_f32 v[4:5], v[150:151], v[208:209], v[4:5]
	v_pk_fma_f32 v[6:7], v[152:153], v[8:9], v[6:7]
	v_or_b32_e32 v102, s54, v104
	ds_write_b128 v109, v[4:7] offset:36912
	s_cselect_b32 s31, 0x100, s88
	v_add_u32_e32 v6, -2, v102
	v_cmp_lt_i32_e32 vcc, 1, v102
	v_cmp_gt_i32_e64 s[46:47], s31, v6
	s_cselect_b32 s8, s13, s16
	s_and_b64 s[46:47], vcc, s[46:47]
	s_ashr_i32 s9, s8, 31
	v_cndmask_b32_e64 v6, v102, v6, s[46:47]
	s_lshl_b64 s[8:9], s[8:9], 12
	v_ashrrev_i32_e32 v7, 31, v6
	v_lshl_add_u64 v[4:5], v[100:101], 0, s[8:9]
	v_lshlrev_b64 v[6:7], 12, v[6:7]
	v_cmp_lt_i32_e32 vcc, 0, v102
	v_cmp_ge_i32_e64 s[48:49], s31, v102
	v_lshl_add_u64 v[6:7], v[4:5], 0, v[6:7]
	s_and_b64 s[48:49], vcc, s[48:49]
	global_load_dwordx4 v[12:15], v[6:7], off offset:2064
	global_load_dwordx4 v[24:27], v[6:7], off offset:2048
	v_subbrev_co_u32_e64 v6, vcc, 0, v102, s[48:49]
	v_ashrrev_i32_e32 v7, 31, v6
	v_lshlrev_b64 v[6:7], 12, v[6:7]
	v_lshl_add_u64 v[6:7], v[4:5], 0, v[6:7]
	v_ashrrev_i32_e32 v103, 31, v102
	global_load_dwordx4 v[20:23], v[6:7], off offset:2064
	global_load_dwordx4 v[32:35], v[6:7], off offset:2048
	v_lshlrev_b64 v[6:7], 12, v[102:103]
	v_lshl_add_u64 v[6:7], v[4:5], 0, v[6:7]
	global_load_dwordx4 v[16:19], v[6:7], off offset:2064
	global_load_dwordx4 v[28:31], v[6:7], off offset:2048
	v_add_u32_e32 v6, 1, v102
	v_cmp_lt_i32_e32 vcc, -2, v102
	v_cmp_gt_i32_e64 s[50:51], s31, v6
	s_and_b64 s[50:51], vcc, s[50:51]
	ds_read_b128 v[36:39], v110 offset:36864
	ds_read_b128 v[40:43], v110 offset:36880
	v_cndmask_b32_e64 v6, v102, v6, s[50:51]
	v_ashrrev_i32_e32 v7, 31, v6
	v_lshlrev_b64 v[6:7], 12, v[6:7]
	v_lshl_add_u64 v[8:9], v[4:5], 0, v[6:7]
	global_load_dwordx4 v[4:7], v[8:9], off offset:2064
	s_nop 0
	global_load_dwordx4 v[8:11], v[8:9], off offset:2048
	s_waitcnt lgkmcnt(1)
	v_cvt_pk_bf16_f32 v56, v36, v37
	v_cvt_pk_bf16_f32 v57, v38, v39
	s_waitcnt lgkmcnt(0)
	v_cvt_pk_bf16_f32 v58, v40, v41
	v_cvt_pk_bf16_f32 v59, v42, v43
	ds_read_b128 v[36:39], v110 offset:36992
	ds_read_b128 v[40:43], v110 offset:37008
	s_waitcnt lgkmcnt(1)
	v_cvt_pk_bf16_f32 v60, v36, v37
	v_cvt_pk_bf16_f32 v61, v38, v39
	s_waitcnt lgkmcnt(0)
	v_cvt_pk_bf16_f32 v62, v40, v41
	v_cvt_pk_bf16_f32 v63, v42, v43
	ds_read_b128 v[36:39], v114
	ds_read_b128 v[40:43], v114 offset:9216
	ds_read_b128 v[44:47], v113
	ds_read_b128 v[48:51], v114 offset:64
	s_waitcnt lgkmcnt(3)
	v_mfma_f32_16x16x32_bf16 v[36:39], v[36:39], v[56:59], 0
	ds_read_b128 v[52:55], v114 offset:9280
	ds_read_b128 v[64:67], v111
	ds_read_b128 v[68:71], v120 offset:36864
	s_cmp_lt_i32 s29, 16
	s_waitcnt lgkmcnt(3)
	v_mfma_f32_16x16x32_bf16 v[36:39], v[48:51], v[60:63], v[36:39]
	ds_read_b128 v[48:51], v112
	s_cselect_b32 s8, s13, s17
	s_waitcnt lgkmcnt(2)
	s_nop 4
	v_add_f32_e32 v36, v36, v64
	v_mul_f32_e32 v36, 0xbfb8aa3b, v36
	v_exp_f32_e32 v36, v36
	v_mfma_f32_16x16x32_bf16 v[40:43], v[40:43], v[56:59], 0
	v_add_f32_e32 v37, v37, v65
	v_mul_f32_e32 v37, 0xbfb8aa3b, v37
	v_add_f32_e32 v36, 1.0, v36
	v_rcp_f32_e32 v36, v36
	v_mfma_f32_16x16x32_bf16 v[40:43], v[52:55], v[60:63], v[40:43]
	v_exp_f32_e32 v37, v37
	v_add_f32_e32 v38, v38, v66
	v_mul_f32_e32 v36, v44, v36
	v_cvt_pk_bf16_f32 v36, v36, v2
	v_add_f32_e32 v37, 1.0, v37
	v_lshlrev_b32_e32 v44, 16, v36
	s_waitcnt lgkmcnt(0)
	s_nop 1
	v_add_f32_e32 v40, v40, v48
	v_mul_f32_e32 v36, 0x3fb8aa3b, v44
	v_mul_f32_e32 v40, 0xbfb8aa3b, v40
	v_exp_f32_e32 v36, v36
	v_exp_f32_e32 v40, v40
	v_rcp_f32_e32 v37, v37
	v_mul_f32_e32 v38, 0xbfb8aa3b, v38
	v_fma_f32 v48, -v36, v36, 1.0
	v_add_f32_e32 v40, 1.0, v40
	v_max_f32_e32 v48, 0, v48
	v_rcp_f32_e32 v40, v40
	v_sqrt_f32_e32 v48, v48
	v_mul_f32_e32 v37, v45, v37
	v_exp_f32_e32 v38, v38
	v_add_f32_e32 v39, v39, v67
	v_mul_f32_e32 v40, v40, v48
	v_mul_f32_e32 v40, v68, v40
	v_cvt_pk_bf16_f32 v52, v44, v40
	v_add_f32_e32 v40, v41, v49
	v_cvt_pk_bf16_f32 v37, v37, v2
	v_mul_f32_e32 v40, 0xbfb8aa3b, v40
	v_lshlrev_b32_e32 v41, 16, v37
	v_mul_f32_e32 v37, 0x3fb8aa3b, v41
	v_exp_f32_e32 v37, v37
	v_exp_f32_e32 v40, v40
	v_add_f32_e32 v38, 1.0, v38
	v_rcp_f32_e32 v38, v38
	v_fma_f32 v44, -v37, v37, 1.0
	v_add_f32_e32 v40, 1.0, v40
	v_max_f32_e32 v44, 0, v44
	v_rcp_f32_e32 v40, v40
	v_sqrt_f32_e32 v44, v44
	v_mul_f32_e32 v38, v46, v38
	v_mul_f32_e32 v39, 0xbfb8aa3b, v39
	v_exp_f32_e32 v39, v39
	v_mul_f32_e32 v40, v40, v44
	v_mul_f32_e32 v40, v69, v40
	v_cvt_pk_bf16_f32 v53, v41, v40
	v_cvt_pk_bf16_f32 v38, v38, v2
	v_add_f32_e32 v40, v42, v50
	v_lshlrev_b32_e32 v41, 16, v38
	v_mul_f32_e32 v38, 0x3fb8aa3b, v41
	v_mul_f32_e32 v40, 0xbfb8aa3b, v40
	v_exp_f32_e32 v38, v38
	v_exp_f32_e32 v40, v40
	v_add_f32_e32 v39, 1.0, v39
	v_rcp_f32_e32 v39, v39
	v_fma_f32 v42, -v38, v38, 1.0
	v_add_f32_e32 v40, 1.0, v40
	v_max_f32_e32 v42, 0, v42
	v_rcp_f32_e32 v40, v40
	v_sqrt_f32_e32 v42, v42
	v_mul_f32_e32 v39, v47, v39
	v_mul_f32_e32 v40, v40, v42
	v_mul_f32_e32 v40, v70, v40
	v_cvt_pk_bf16_f32 v54, v41, v40
	v_cvt_pk_bf16_f32 v39, v39, v2
	v_add_f32_e32 v40, v43, v51
	v_lshlrev_b32_e32 v41, 16, v39
	v_mul_f32_e32 v39, 0x3fb8aa3b, v41
	v_mul_f32_e32 v40, 0xbfb8aa3b, v40
	v_exp_f32_e32 v39, v39
	v_exp_f32_e32 v40, v40
	v_fma_f32 v42, -v39, v39, 1.0
	v_add_f32_e32 v40, 1.0, v40
	v_max_f32_e32 v42, 0, v42
	v_rcp_f32_e32 v40, v40
	v_sqrt_f32_e32 v42, v42
	s_nop 0
	v_mul_f32_e32 v40, v40, v42
	v_mul_f32_e32 v40, v71, v40
	v_cvt_pk_bf16_f32 v55, v41, v40
	ds_read_b128 v[40:43], v114 offset:2304
	ds_read_b128 v[44:47], v114 offset:11520
	ds_read_b128 v[48:51], v113 offset:64
	ds_read_b128 v[64:67], v114 offset:2368
	s_waitcnt lgkmcnt(3)
; #define LAS __attribute__((address_space(3)))
; __device__ __forceinline__ unsigned cvt_pk_bf16(float lo, float hi) { unsigned r; asm volatile("v_cvt_pk_bf16_f32 %0, %1, %2" : "=v"(r) : "v"(lo), "v"(hi)); return r; }
; __device__ __forceinline__ float sigmoidf_(float x) { return __builtin_amdgcn_rcpf(1.0f + __expf(-x)); }
; __device__ __forceinline__ void lru_gates(const Frame& F, LAS bf16_t* Wl, const LAS float* CT, LAS float* ucb, float (&av)[2][4][4], unsigned (&pw)[2][4][4]) {
;     ...
;                 const bf16x8 wa = *(const LAS bf16x8*)(Wl + ((d * 2 + 0) * 64 + et * 16 + tk) * 72 + ks * 32 + g * 8);
;                 const bf16x8 wx = *(const LAS bf16x8*)(Wl + ((d * 2 + 1) * 64 + et * 16 + tk) * 72 + ks * 32 + g * 8);
;                 ra = __builtin_amdgcn_mfma_f32_16x16x32_bf16(wa, bfr[ks], ra, 0, 0, 0);
;                 ri = __builtin_amdgcn_mfma_f32_16x16x32_bf16(wx, bfr[ks], ri, 0, 0, 0);
;             }
;             const f32x4 ba4 = *(const LAS f32x4*)(CT + (5 + 3 * d) * 64 + et * 16 + 4 * g), bx4 = *(const LAS f32x4*)(CT + (6 + 3 * d) * 64 + et * 16 + 4 * g), cs4 = *(const LAS f32x4*)(CT + (7 + 3 * d) * 64 + et * 16 + 4 * g);
;             const f32x4 u4 = *(const LAS f32x4*)(ucb + tk * 68 + et * 16 + 4 * g);
; #pragma unroll
;             for (int i = 0; i < 4; ++i) {
;                 const float r = sigmoidf_(ra[i] + ba4[i]), ig = sigmoidf_(ri[i] + bx4[i]);
;                 const float la = __uint_as_float(cvt_pk_bf16(cs4[i] * r, 0.f) << 16), a = __expf(la);
;                 av[d][et][i] = a; pw[d][et][i] = cvt_pk_bf16(la, __builtin_amdgcn_sqrtf(fmaxf(1.0f - a * a, 0.f)) * ig * u4[i]); }
	v_mfma_f32_16x16x32_bf16 v[40:43], v[40:43], v[56:59], 0
	ds_read_b128 v[68:71], v114 offset:11584
	ds_read_b128 v[72:75], v111 offset:64
	ds_read_b128 v[76:79], v120 offset:36928
	s_waitcnt lgkmcnt(3)
	v_mfma_f32_16x16x32_bf16 v[40:43], v[64:67], v[60:63], v[40:43]
	ds_read_b128 v[64:67], v112 offset:64
	v_mfma_f32_16x16x32_bf16 v[44:47], v[44:47], v[56:59], 0
	s_waitcnt lgkmcnt(2)
	s_nop 4
	v_add_f32_e32 v40, v40, v72
	v_mul_f32_e32 v40, 0xbfb8aa3b, v40
	v_exp_f32_e32 v40, v40
	v_mfma_f32_16x16x32_bf16 v[44:47], v[68:71], v[60:63], v[44:47]
	v_add_f32_e32 v41, v41, v73
	v_mul_f32_e32 v41, 0xbfb8aa3b, v41
	v_add_f32_e32 v40, 1.0, v40
	v_rcp_f32_e32 v40, v40
	v_exp_f32_e32 v41, v41
	s_waitcnt lgkmcnt(0)
	s_nop 1
	v_add_f32_e32 v44, v44, v64
	v_mul_f32_e32 v44, 0xbfb8aa3b, v44
	v_mul_f32_e32 v40, v48, v40
	v_cvt_pk_bf16_f32 v40, v40, v2
	v_exp_f32_e32 v44, v44
	v_lshlrev_b32_e32 v48, 16, v40
	v_mul_f32_e32 v40, 0x3fb8aa3b, v48
	v_exp_f32_e32 v40, v40
	v_add_f32_e32 v44, 1.0, v44
	v_rcp_f32_e32 v44, v44
	v_add_f32_e32 v41, 1.0, v41
	v_fma_f32 v64, -v40, v40, 1.0
	v_max_f32_e32 v64, 0, v64
	v_sqrt_f32_e32 v64, v64
	v_rcp_f32_e32 v41, v41
	v_add_f32_e32 v42, v42, v74
	v_mul_f32_e32 v42, 0xbfb8aa3b, v42
	v_mul_f32_e32 v44, v44, v64
	v_mul_f32_e32 v44, v76, v44
	v_mul_f32_e32 v41, v49, v41
	v_cvt_pk_bf16_f32 v68, v48, v44
	v_add_f32_e32 v44, v45, v65
	v_cvt_pk_bf16_f32 v41, v41, v2
	v_mul_f32_e32 v44, 0xbfb8aa3b, v44
	v_lshlrev_b32_e32 v45, 16, v41
	v_mul_f32_e32 v41, 0x3fb8aa3b, v45
	v_exp_f32_e32 v41, v41
	v_exp_f32_e32 v44, v44
	v_exp_f32_e32 v42, v42
	v_add_f32_e32 v43, v43, v75
	v_fma_f32 v48, -v41, v41, 1.0
	v_add_f32_e32 v44, 1.0, v44
	v_max_f32_e32 v48, 0, v48
	v_add_f32_e32 v42, 1.0, v42
	v_rcp_f32_e32 v44, v44
	v_sqrt_f32_e32 v48, v48
	v_rcp_f32_e32 v42, v42
	v_mul_f32_e32 v43, 0xbfb8aa3b, v43
	v_exp_f32_e32 v43, v43
	v_mul_f32_e32 v44, v44, v48
	v_mul_f32_e32 v42, v50, v42
	v_mul_f32_e32 v44, v77, v44
	v_cvt_pk_bf16_f32 v69, v45, v44
	v_cvt_pk_bf16_f32 v42, v42, v2
	v_add_f32_e32 v44, v46, v66
	v_lshlrev_b32_e32 v45, 16, v42
	v_mul_f32_e32 v42, 0x3fb8aa3b, v45
	v_mul_f32_e32 v44, 0xbfb8aa3b, v44
	v_exp_f32_e32 v42, v42
	v_exp_f32_e32 v44, v44
	v_add_f32_e32 v43, 1.0, v43
	v_rcp_f32_e32 v43, v43
	v_fma_f32 v46, -v42, v42, 1.0
	v_add_f32_e32 v44, 1.0, v44
	v_max_f32_e32 v46, 0, v46
	v_rcp_f32_e32 v44, v44
	v_sqrt_f32_e32 v46, v46
	v_mul_f32_e32 v43, v51, v43
	v_mul_f32_e32 v44, v44, v46
	v_mul_f32_e32 v44, v78, v44
	v_cvt_pk_bf16_f32 v70, v45, v44
	v_cvt_pk_bf16_f32 v43, v43, v2
	v_add_f32_e32 v44, v47, v67
	v_lshlrev_b32_e32 v45, 16, v43
	v_mul_f32_e32 v43, 0x3fb8aa3b, v45
	v_mul_f32_e32 v44, 0xbfb8aa3b, v44
	v_exp_f32_e32 v43, v43
	v_exp_f32_e32 v44, v44
	v_fma_f32 v46, -v43, v43, 1.0
	v_add_f32_e32 v44, 1.0, v44
	v_max_f32_e32 v46, 0, v46
	v_rcp_f32_e32 v44, v44
	v_sqrt_f32_e32 v46, v46
	s_nop 0
	v_mul_f32_e32 v44, v44, v46
	v_mul_f32_e32 v44, v79, v44
	v_cvt_pk_bf16_f32 v71, v45, v44
	ds_read_b128 v[44:47], v114 offset:4608
	ds_read_b128 v[48:51], v114 offset:13824
	ds_read_b128 v[64:67], v113 offset:128
	ds_read_b128 v[72:75], v114 offset:4672
	s_waitcnt lgkmcnt(3)
	v_mfma_f32_16x16x32_bf16 v[44:47], v[44:47], v[56:59], 0
	ds_read_b128 v[76:79], v114 offset:13888
	ds_read_b128 v[80:83], v111 offset:128
	ds_read_b128 v[84:87], v120 offset:36992
	s_waitcnt lgkmcnt(3)
	v_mfma_f32_16x16x32_bf16 v[44:47], v[72:75], v[60:63], v[44:47]
	ds_read_b128 v[72:75], v112 offset:128
	v_mfma_f32_16x16x32_bf16 v[48:51], v[48:51], v[56:59], 0
	s_waitcnt lgkmcnt(2)
	s_nop 4
	v_add_f32_e32 v44, v44, v80
	v_mul_f32_e32 v44, 0xbfb8aa3b, v44
	v_exp_f32_e32 v44, v44
	v_mfma_f32_16x16x32_bf16 v[48:51], v[76:79], v[60:63], v[48:51]
	v_add_f32_e32 v45, v45, v81
	v_mul_f32_e32 v45, 0xbfb8aa3b, v45
	v_add_f32_e32 v44, 1.0, v44
	v_rcp_f32_e32 v44, v44
	v_exp_f32_e32 v45, v45
	s_waitcnt lgkmcnt(0)
	s_nop 1
	v_add_f32_e32 v48, v48, v72
	v_mul_f32_e32 v48, 0xbfb8aa3b, v48
	v_mul_f32_e32 v44, v64, v44
	v_cvt_pk_bf16_f32 v44, v44, v2
	v_exp_f32_e32 v48, v48
	v_lshlrev_b32_e32 v64, 16, v44
	v_mul_f32_e32 v44, 0x3fb8aa3b, v64
	v_exp_f32_e32 v44, v44
	v_add_f32_e32 v48, 1.0, v48
	v_rcp_f32_e32 v48, v48
	v_add_f32_e32 v45, 1.0, v45
	v_fma_f32 v72, -v44, v44, 1.0
	v_max_f32_e32 v72, 0, v72
	v_sqrt_f32_e32 v72, v72
	v_rcp_f32_e32 v45, v45
	v_add_f32_e32 v46, v46, v82
	v_mul_f32_e32 v46, 0xbfb8aa3b, v46
	v_mul_f32_e32 v48, v48, v72
	v_mul_f32_e32 v48, v84, v48
	v_mul_f32_e32 v45, v65, v45
	v_cvt_pk_bf16_f32 v72, v64, v48
	v_add_f32_e32 v48, v49, v73
	v_cvt_pk_bf16_f32 v45, v45, v2
	v_mul_f32_e32 v48, 0xbfb8aa3b, v48
	v_lshlrev_b32_e32 v49, 16, v45
	v_mul_f32_e32 v45, 0x3fb8aa3b, v49
	v_exp_f32_e32 v45, v45
	v_exp_f32_e32 v48, v48
	v_exp_f32_e32 v46, v46
	v_add_f32_e32 v47, v47, v83
	v_fma_f32 v64, -v45, v45, 1.0
	v_add_f32_e32 v48, 1.0, v48
	v_max_f32_e32 v64, 0, v64
	v_add_f32_e32 v46, 1.0, v46
	v_rcp_f32_e32 v48, v48
	v_sqrt_f32_e32 v64, v64
	v_rcp_f32_e32 v46, v46
	v_mul_f32_e32 v47, 0xbfb8aa3b, v47
	v_exp_f32_e32 v47, v47
	v_mul_f32_e32 v48, v48, v64
	v_mul_f32_e32 v46, v66, v46
	v_mul_f32_e32 v48, v85, v48
	v_cvt_pk_bf16_f32 v73, v49, v48
	v_cvt_pk_bf16_f32 v46, v46, v2
	v_add_f32_e32 v48, v50, v74
	v_lshlrev_b32_e32 v49, 16, v46
	v_mul_f32_e32 v46, 0x3fb8aa3b, v49
	v_mul_f32_e32 v48, 0xbfb8aa3b, v48
	v_exp_f32_e32 v46, v46
	v_exp_f32_e32 v48, v48
	v_add_f32_e32 v47, 1.0, v47
	v_rcp_f32_e32 v47, v47
	v_fma_f32 v50, -v46, v46, 1.0
	v_add_f32_e32 v48, 1.0, v48
	v_max_f32_e32 v50, 0, v50
	v_rcp_f32_e32 v48, v48
	v_sqrt_f32_e32 v50, v50
	v_mul_f32_e32 v47, v67, v47
	v_mul_f32_e32 v48, v48, v50
	v_mul_f32_e32 v48, v86, v48
	v_cvt_pk_bf16_f32 v74, v49, v48
	v_cvt_pk_bf16_f32 v47, v47, v2
	v_add_f32_e32 v48, v51, v75
	v_lshlrev_b32_e32 v49, 16, v47
	v_mul_f32_e32 v47, 0x3fb8aa3b, v49
	v_mul_f32_e32 v48, 0xbfb8aa3b, v48
	v_exp_f32_e32 v47, v47
	v_exp_f32_e32 v48, v48
	v_fma_f32 v50, -v47, v47, 1.0
	v_add_f32_e32 v48, 1.0, v48
	v_max_f32_e32 v50, 0, v50
	v_rcp_f32_e32 v48, v48
	v_sqrt_f32_e32 v50, v50
	s_nop 0
	v_mul_f32_e32 v48, v48, v50
	v_mul_f32_e32 v48, v87, v48
	v_cvt_pk_bf16_f32 v75, v49, v48
	ds_read_b128 v[48:51], v114 offset:6912
	ds_read_b128 v[64:67], v114 offset:16128
	ds_read_b128 v[76:79], v113 offset:192
	ds_read_b128 v[80:83], v114 offset:6976
	s_waitcnt lgkmcnt(3)
; #define LAS __attribute__((address_space(3)))
; __device__ __forceinline__ unsigned cvt_pk_bf16(float lo, float hi) { unsigned r; asm volatile("v_cvt_pk_bf16_f32 %0, %1, %2" : "=v"(r) : "v"(lo), "v"(hi)); return r; }
; __device__ __forceinline__ float sigmoidf_(float x) { return __builtin_amdgcn_rcpf(1.0f + __expf(-x)); }
; __device__ __forceinline__ void lru_gates(const Frame& F, LAS bf16_t* Wl, const LAS float* CT, LAS float* ucb, float (&av)[2][4][4], unsigned (&pw)[2][4][4]) {
;     ...
;                 const bf16x8 wa = *(const LAS bf16x8*)(Wl + ((d * 2 + 0) * 64 + et * 16 + tk) * 72 + ks * 32 + g * 8);
;                 const bf16x8 wx = *(const LAS bf16x8*)(Wl + ((d * 2 + 1) * 64 + et * 16 + tk) * 72 + ks * 32 + g * 8);
;                 ra = __builtin_amdgcn_mfma_f32_16x16x32_bf16(wa, bfr[ks], ra, 0, 0, 0);
;                 ri = __builtin_amdgcn_mfma_f32_16x16x32_bf16(wx, bfr[ks], ri, 0, 0, 0);
;             }
;             const f32x4 ba4 = *(const LAS f32x4*)(CT + (5 + 3 * d) * 64 + et * 16 + 4 * g), bx4 = *(const LAS f32x4*)(CT + (6 + 3 * d) * 64 + et * 16 + 4 * g), cs4 = *(const LAS f32x4*)(CT + (7 + 3 * d) * 64 + et * 16 + 4 * g);
;             const f32x4 u4 = *(const LAS f32x4*)(ucb + tk * 68 + et * 16 + 4 * g);
; #pragma unroll
;             for (int i = 0; i < 4; ++i) {
;                 const float r = sigmoidf_(ra[i] + ba4[i]), ig = sigmoidf_(ri[i] + bx4[i]);
;                 const float la = __uint_as_float(cvt_pk_bf16(cs4[i] * r, 0.f) << 16), a = __expf(la);
;                 av[d][et][i] = a; pw[d][et][i] = cvt_pk_bf16(la, __builtin_amdgcn_sqrtf(fmaxf(1.0f - a * a, 0.f)) * ig * u4[i]); }
	v_mfma_f32_16x16x32_bf16 v[48:51], v[48:51], v[56:59], 0
	ds_read_b128 v[84:87], v114 offset:16192
	ds_read_b128 v[88:91], v111 offset:192
	ds_read_b128 v[122:125], v120 offset:37056
	s_waitcnt lgkmcnt(3)
	v_mfma_f32_16x16x32_bf16 v[48:51], v[80:83], v[60:63], v[48:51]
	ds_read_b128 v[80:83], v112 offset:192
	v_mfma_f32_16x16x32_bf16 v[64:67], v[64:67], v[56:59], 0
	s_waitcnt lgkmcnt(2)
	s_nop 4
	v_add_f32_e32 v48, v48, v88
	v_mul_f32_e32 v48, 0xbfb8aa3b, v48
	v_exp_f32_e32 v48, v48
	v_mfma_f32_16x16x32_bf16 v[64:67], v[84:87], v[60:63], v[64:67]
	v_add_f32_e32 v49, v49, v89
	v_mul_f32_e32 v49, 0xbfb8aa3b, v49
	v_add_f32_e32 v48, 1.0, v48
	v_rcp_f32_e32 v48, v48
	v_exp_f32_e32 v49, v49
	s_waitcnt lgkmcnt(0)
	s_nop 1
	v_add_f32_e32 v64, v64, v80
	v_mul_f32_e32 v64, 0xbfb8aa3b, v64
	v_mul_f32_e32 v48, v76, v48
	v_cvt_pk_bf16_f32 v48, v48, v2
	v_exp_f32_e32 v64, v64
	v_lshlrev_b32_e32 v76, 16, v48
	v_mul_f32_e32 v48, 0x3fb8aa3b, v76
	v_exp_f32_e32 v48, v48
	v_add_f32_e32 v64, 1.0, v64
	v_rcp_f32_e32 v64, v64
	v_add_f32_e32 v49, 1.0, v49
	v_fma_f32 v80, -v48, v48, 1.0
	v_max_f32_e32 v80, 0, v80
	v_sqrt_f32_e32 v80, v80
	v_rcp_f32_e32 v49, v49
	v_add_f32_e32 v50, v50, v90
	v_mul_f32_e32 v50, 0xbfb8aa3b, v50
	v_mul_f32_e32 v64, v64, v80
	v_mul_f32_e32 v64, v122, v64
	v_mul_f32_e32 v49, v77, v49
	v_cvt_pk_bf16_f32 v76, v76, v64
	v_add_f32_e32 v64, v65, v81
	v_cvt_pk_bf16_f32 v49, v49, v2
	v_mul_f32_e32 v64, 0xbfb8aa3b, v64
	v_lshlrev_b32_e32 v65, 16, v49
	v_mul_f32_e32 v49, 0x3fb8aa3b, v65
	v_exp_f32_e32 v49, v49
	v_exp_f32_e32 v64, v64
	v_exp_f32_e32 v50, v50
	v_add_f32_e32 v51, v51, v91
	v_fma_f32 v77, -v49, v49, 1.0
	v_add_f32_e32 v64, 1.0, v64
	v_max_f32_e32 v77, 0, v77
	v_add_f32_e32 v50, 1.0, v50
	v_rcp_f32_e32 v64, v64
	v_sqrt_f32_e32 v77, v77
	v_rcp_f32_e32 v50, v50
	v_mul_f32_e32 v51, 0xbfb8aa3b, v51
	v_exp_f32_e32 v51, v51
	v_mul_f32_e32 v64, v64, v77
	v_mul_f32_e32 v50, v78, v50
	v_mul_f32_e32 v64, v123, v64
	v_cvt_pk_bf16_f32 v77, v65, v64
	v_cvt_pk_bf16_f32 v50, v50, v2
	v_add_f32_e32 v64, v66, v82
	v_lshlrev_b32_e32 v65, 16, v50
	v_mul_f32_e32 v50, 0x3fb8aa3b, v65
	v_mul_f32_e32 v64, 0xbfb8aa3b, v64
	v_exp_f32_e32 v50, v50
	v_exp_f32_e32 v64, v64
	v_add_f32_e32 v51, 1.0, v51
	v_rcp_f32_e32 v51, v51
	v_fma_f32 v66, -v50, v50, 1.0
	v_add_f32_e32 v64, 1.0, v64
	v_max_f32_e32 v66, 0, v66
	v_rcp_f32_e32 v64, v64
	v_sqrt_f32_e32 v66, v66
	v_mul_f32_e32 v51, v79, v51
	v_mul_f32_e32 v64, v64, v66
	v_mul_f32_e32 v64, v124, v64
	v_cvt_pk_bf16_f32 v78, v65, v64
	v_cvt_pk_bf16_f32 v51, v51, v2
	v_add_f32_e32 v64, v67, v83
	v_lshlrev_b32_e32 v65, 16, v51
	v_mul_f32_e32 v51, 0x3fb8aa3b, v65
	v_mul_f32_e32 v64, 0xbfb8aa3b, v64
	v_exp_f32_e32 v51, v51
	v_exp_f32_e32 v64, v64
	v_fma_f32 v66, -v51, v51, 1.0
	v_add_f32_e32 v64, 1.0, v64
	v_max_f32_e32 v66, 0, v66
	v_rcp_f32_e32 v64, v64
	v_sqrt_f32_e32 v66, v66
	s_nop 0
	v_mul_f32_e32 v64, v64, v66
	v_mul_f32_e32 v64, v125, v64
	v_cvt_pk_bf16_f32 v79, v65, v64
	ds_read_b128 v[64:67], v114 offset:18432
	ds_read_b128 v[80:83], v114 offset:18496
	s_waitcnt lgkmcnt(1)
	v_mfma_f32_16x16x32_bf16 v[64:67], v[64:67], v[56:59], 0
	ds_read_b128 v[84:87], v114 offset:27648
	ds_read_b128 v[88:91], v114 offset:27712
	ds_read_b128 v[122:125], v115
	s_waitcnt lgkmcnt(3)
	v_mfma_f32_16x16x32_bf16 v[64:67], v[80:83], v[60:63], v[64:67]
	ds_read_b128 v[80:83], v116
	s_waitcnt lgkmcnt(3)
	v_mfma_f32_16x16x32_bf16 v[84:87], v[84:87], v[56:59], 0
	s_waitcnt lgkmcnt(2)
	v_mfma_f32_16x16x32_bf16 v[84:87], v[88:91], v[60:63], v[84:87]
	s_waitcnt lgkmcnt(1)
	s_nop 1
	v_add_f32_e32 v64, v64, v122
	v_mul_f32_e32 v64, 0xbfb8aa3b, v64
	v_exp_f32_e32 v64, v64
	ds_read_b128 v[88:91], v117
	ds_read_b128 v[126:129], v120 offset:36864
	s_waitcnt lgkmcnt(2)
	v_add_f32_e32 v80, v84, v80
	v_mul_f32_e32 v80, 0xbfb8aa3b, v80
	v_add_f32_e32 v64, 1.0, v64
	v_rcp_f32_e32 v64, v64
	v_exp_f32_e32 v80, v80
	v_add_f32_e32 v65, v65, v123
	v_mul_f32_e32 v65, 0xbfb8aa3b, v65
	s_waitcnt lgkmcnt(1)
	v_mul_f32_e32 v64, v88, v64
	v_cvt_pk_bf16_f32 v64, v64, v2
	v_add_f32_e32 v80, 1.0, v80
	v_lshlrev_b32_e32 v64, 16, v64
	v_mul_f32_e32 v84, 0x3fb8aa3b, v64
	v_exp_f32_e32 v103, v84
	v_rcp_f32_e32 v80, v80
	v_exp_f32_e32 v65, v65
	v_add_f32_e32 v66, v66, v124
	v_fma_f32 v84, -v103, v103, 1.0
	v_max_f32_e32 v84, 0, v84
	v_sqrt_f32_e32 v84, v84
	v_mul_f32_e32 v66, 0xbfb8aa3b, v66
	v_exp_f32_e32 v66, v66
	v_add_f32_e32 v67, v67, v125
	v_mul_f32_e32 v80, v80, v84
	s_waitcnt lgkmcnt(0)
	v_mul_f32_e32 v80, v126, v80
	v_cvt_pk_bf16_f32 v80, v64, v80
	v_add_f32_e32 v64, 1.0, v65
	v_rcp_f32_e32 v64, v64
	v_add_f32_e32 v65, v85, v81
	v_mul_f32_e32 v65, 0xbfb8aa3b, v65
	v_exp_f32_e32 v65, v65
	v_mul_f32_e32 v64, v89, v64
	v_cvt_pk_bf16_f32 v64, v64, v2
	v_mul_f32_e32 v67, 0xbfb8aa3b, v67
	v_lshlrev_b32_e32 v64, 16, v64
	v_mul_f32_e32 v81, 0x3fb8aa3b, v64
	v_exp_f32_e32 v122, v81
	v_add_f32_e32 v65, 1.0, v65
	v_rcp_f32_e32 v65, v65
	v_exp_f32_e32 v67, v67
	v_fma_f32 v81, -v122, v122, 1.0
	v_max_f32_e32 v81, 0, v81
	v_sqrt_f32_e32 v81, v81
	s_nop 0
	v_mul_f32_e32 v65, v65, v81
	v_mul_f32_e32 v65, v127, v65
	v_cvt_pk_bf16_f32 v81, v64, v65
	v_add_f32_e32 v64, 1.0, v66
	v_rcp_f32_e32 v64, v64
	v_add_f32_e32 v65, v86, v82
	v_mul_f32_e32 v65, 0xbfb8aa3b, v65
	v_exp_f32_e32 v65, v65
	v_mul_f32_e32 v64, v90, v64
	v_cvt_pk_bf16_f32 v64, v64, v2
	v_add_f32_e32 v65, 1.0, v65
	v_lshlrev_b32_e32 v64, 16, v64
	v_mul_f32_e32 v66, 0x3fb8aa3b, v64
	v_exp_f32_e32 v123, v66
	v_rcp_f32_e32 v65, v65
	v_fma_f32 v66, -v123, v123, 1.0
	v_max_f32_e32 v66, 0, v66
	v_sqrt_f32_e32 v66, v66
	s_nop 0
	v_mul_f32_e32 v65, v65, v66
	v_mul_f32_e32 v65, v128, v65
	v_cvt_pk_bf16_f32 v82, v64, v65
	v_add_f32_e32 v64, 1.0, v67
	v_rcp_f32_e32 v64, v64
	v_add_f32_e32 v65, v87, v83
	v_mul_f32_e32 v65, 0xbfb8aa3b, v65
	v_exp_f32_e32 v65, v65
	v_mul_f32_e32 v64, v91, v64
	v_cvt_pk_bf16_f32 v64, v64, v2
	v_add_f32_e32 v65, 1.0, v65
	v_lshlrev_b32_e32 v64, 16, v64
	v_mul_f32_e32 v66, 0x3fb8aa3b, v64
	v_exp_f32_e32 v124, v66
	v_rcp_f32_e32 v65, v65
	v_fma_f32 v66, -v124, v124, 1.0
	v_max_f32_e32 v66, 0, v66
	v_sqrt_f32_e32 v66, v66
	s_nop 0
	v_mul_f32_e32 v65, v65, v66
	v_mul_f32_e32 v65, v129, v65
	v_cvt_pk_bf16_f32 v83, v64, v65
	ds_read_b128 v[64:67], v114 offset:20736
	ds_read_b128 v[84:87], v114 offset:20800
	s_waitcnt lgkmcnt(1)
; #define LAS __attribute__((address_space(3)))
; __device__ __forceinline__ unsigned cvt_pk_bf16(float lo, float hi) { unsigned r; asm volatile("v_cvt_pk_bf16_f32 %0, %1, %2" : "=v"(r) : "v"(lo), "v"(hi)); return r; }
; __device__ __forceinline__ float sigmoidf_(float x) { return __builtin_amdgcn_rcpf(1.0f + __expf(-x)); }
; __device__ __forceinline__ void lru_gates(const Frame& F, LAS bf16_t* Wl, const LAS float* CT, LAS float* ucb, float (&av)[2][4][4], unsigned (&pw)[2][4][4]) {
;     ...
;                 const bf16x8 wa = *(const LAS bf16x8*)(Wl + ((d * 2 + 0) * 64 + et * 16 + tk) * 72 + ks * 32 + g * 8);
;                 const bf16x8 wx = *(const LAS bf16x8*)(Wl + ((d * 2 + 1) * 64 + et * 16 + tk) * 72 + ks * 32 + g * 8);
;                 ra = __builtin_amdgcn_mfma_f32_16x16x32_bf16(wa, bfr[ks], ra, 0, 0, 0);
;                 ri = __builtin_amdgcn_mfma_f32_16x16x32_bf16(wx, bfr[ks], ri, 0, 0, 0);
;             }
;             const f32x4 ba4 = *(const LAS f32x4*)(CT + (5 + 3 * d) * 64 + et * 16 + 4 * g), bx4 = *(const LAS f32x4*)(CT + (6 + 3 * d) * 64 + et * 16 + 4 * g), cs4 = *(const LAS f32x4*)(CT + (7 + 3 * d) * 64 + et * 16 + 4 * g);
;             const f32x4 u4 = *(const LAS f32x4*)(ucb + tk * 68 + et * 16 + 4 * g);
; #pragma unroll
;             for (int i = 0; i < 4; ++i) {
;                 const float r = sigmoidf_(ra[i] + ba4[i]), ig = sigmoidf_(ri[i] + bx4[i]);
;                 const float la = __uint_as_float(cvt_pk_bf16(cs4[i] * r, 0.f) << 16), a = __expf(la);
;                 av[d][et][i] = a; pw[d][et][i] = cvt_pk_bf16(la, __builtin_amdgcn_sqrtf(fmaxf(1.0f - a * a, 0.f)) * ig * u4[i]); }
	v_mfma_f32_16x16x32_bf16 v[64:67], v[64:67], v[56:59], 0
	ds_read_b128 v[88:91], v114 offset:29952
	ds_read_b128 v[126:129], v114 offset:30016
	ds_read_b128 v[130:133], v115 offset:64
	s_waitcnt lgkmcnt(3)
	v_mfma_f32_16x16x32_bf16 v[64:67], v[84:87], v[60:63], v[64:67]
	ds_read_b128 v[84:87], v116 offset:64
	s_waitcnt lgkmcnt(3)
	v_mfma_f32_16x16x32_bf16 v[88:91], v[88:91], v[56:59], 0
	s_waitcnt lgkmcnt(2)
	v_mfma_f32_16x16x32_bf16 v[88:91], v[126:129], v[60:63], v[88:91]
	s_waitcnt lgkmcnt(1)
	s_nop 1
	v_add_f32_e32 v64, v64, v130
	v_mul_f32_e32 v64, 0xbfb8aa3b, v64
	v_exp_f32_e32 v64, v64
	ds_read_b128 v[126:129], v117 offset:64
	ds_read_b128 v[134:137], v120 offset:36928
	s_waitcnt lgkmcnt(2)
	v_add_f32_e32 v84, v88, v84
	v_mul_f32_e32 v84, 0xbfb8aa3b, v84
	v_add_f32_e32 v64, 1.0, v64
	v_rcp_f32_e32 v64, v64
	v_exp_f32_e32 v84, v84
	v_add_f32_e32 v65, v65, v131
	v_mul_f32_e32 v65, 0xbfb8aa3b, v65
	s_waitcnt lgkmcnt(1)
	v_mul_f32_e32 v64, v126, v64
	v_cvt_pk_bf16_f32 v64, v64, v2
	v_add_f32_e32 v84, 1.0, v84
	v_lshlrev_b32_e32 v64, 16, v64
	v_mul_f32_e32 v88, 0x3fb8aa3b, v64
	v_exp_f32_e32 v125, v88
	v_rcp_f32_e32 v84, v84
	v_exp_f32_e32 v65, v65
	v_add_f32_e32 v66, v66, v132
	v_fma_f32 v88, -v125, v125, 1.0
	v_max_f32_e32 v88, 0, v88
	v_sqrt_f32_e32 v88, v88
	v_mul_f32_e32 v66, 0xbfb8aa3b, v66
	v_exp_f32_e32 v66, v66
	v_add_f32_e32 v67, v67, v133
	v_mul_f32_e32 v84, v84, v88
	s_waitcnt lgkmcnt(0)
	v_mul_f32_e32 v84, v134, v84
	v_cvt_pk_bf16_f32 v84, v64, v84
	v_add_f32_e32 v64, 1.0, v65
	v_rcp_f32_e32 v64, v64
	v_add_f32_e32 v65, v89, v85
	v_mul_f32_e32 v65, 0xbfb8aa3b, v65
	v_exp_f32_e32 v65, v65
	v_mul_f32_e32 v64, v127, v64
	v_cvt_pk_bf16_f32 v64, v64, v2
	v_mul_f32_e32 v67, 0xbfb8aa3b, v67
	v_lshlrev_b32_e32 v64, 16, v64
	v_mul_f32_e32 v85, 0x3fb8aa3b, v64
	v_exp_f32_e32 v126, v85
	v_add_f32_e32 v65, 1.0, v65
	v_rcp_f32_e32 v65, v65
	v_exp_f32_e32 v67, v67
	v_fma_f32 v85, -v126, v126, 1.0
	v_max_f32_e32 v85, 0, v85
	v_sqrt_f32_e32 v85, v85
	s_nop 0
	v_mul_f32_e32 v65, v65, v85
	v_mul_f32_e32 v65, v135, v65
	v_cvt_pk_bf16_f32 v85, v64, v65
	v_add_f32_e32 v64, 1.0, v66
	v_rcp_f32_e32 v64, v64
	v_add_f32_e32 v65, v90, v86
	v_mul_f32_e32 v65, 0xbfb8aa3b, v65
	v_exp_f32_e32 v65, v65
	v_mul_f32_e32 v64, v128, v64
	v_cvt_pk_bf16_f32 v64, v64, v2
	v_add_f32_e32 v65, 1.0, v65
	v_lshlrev_b32_e32 v64, 16, v64
	v_mul_f32_e32 v66, 0x3fb8aa3b, v64
	v_exp_f32_e32 v127, v66
	v_rcp_f32_e32 v65, v65
	v_fma_f32 v66, -v127, v127, 1.0
	v_max_f32_e32 v66, 0, v66
	v_sqrt_f32_e32 v66, v66
	s_nop 0
	v_mul_f32_e32 v65, v65, v66
	v_mul_f32_e32 v65, v136, v65
	v_cvt_pk_bf16_f32 v86, v64, v65
	v_add_f32_e32 v64, 1.0, v67
	v_rcp_f32_e32 v64, v64
	v_add_f32_e32 v65, v91, v87
	v_mul_f32_e32 v65, 0xbfb8aa3b, v65
	v_exp_f32_e32 v65, v65
	v_mul_f32_e32 v64, v129, v64
	v_cvt_pk_bf16_f32 v64, v64, v2
	v_add_f32_e32 v65, 1.0, v65
	v_lshlrev_b32_e32 v64, 16, v64
	v_mul_f32_e32 v66, 0x3fb8aa3b, v64
	v_exp_f32_e32 v128, v66
	v_rcp_f32_e32 v65, v65
	v_fma_f32 v66, -v128, v128, 1.0
	v_max_f32_e32 v66, 0, v66
	v_sqrt_f32_e32 v66, v66
	s_nop 0
	v_mul_f32_e32 v65, v65, v66
	v_mul_f32_e32 v65, v137, v65
	v_cvt_pk_bf16_f32 v87, v64, v65
	ds_read_b128 v[64:67], v114 offset:23040
	ds_read_b128 v[88:91], v114 offset:23104
	s_waitcnt lgkmcnt(1)
	v_mfma_f32_16x16x32_bf16 v[64:67], v[64:67], v[56:59], 0
	ds_read_b128 v[130:133], v114 offset:32256
	ds_read_b128 v[134:137], v114 offset:32320
	ds_read_b128 v[138:141], v115 offset:128
	s_waitcnt lgkmcnt(3)
	v_mfma_f32_16x16x32_bf16 v[64:67], v[88:91], v[60:63], v[64:67]
	ds_read_b128 v[88:91], v116 offset:128
	s_waitcnt lgkmcnt(3)
	v_mfma_f32_16x16x32_bf16 v[130:133], v[130:133], v[56:59], 0
	s_waitcnt lgkmcnt(2)
	v_mfma_f32_16x16x32_bf16 v[130:133], v[134:137], v[60:63], v[130:133]
	s_waitcnt lgkmcnt(1)
	s_nop 1
	v_add_f32_e32 v64, v64, v138
	v_mul_f32_e32 v64, 0xbfb8aa3b, v64
	v_exp_f32_e32 v64, v64
	ds_read_b128 v[134:137], v117 offset:128
	ds_read_b128 v[146:149], v120 offset:36992
	s_waitcnt lgkmcnt(2)
	v_add_f32_e32 v88, v130, v88
	v_mul_f32_e32 v88, 0xbfb8aa3b, v88
	v_add_f32_e32 v64, 1.0, v64
	v_rcp_f32_e32 v64, v64
	v_exp_f32_e32 v88, v88
	v_add_f32_e32 v65, v65, v139
	v_mul_f32_e32 v65, 0xbfb8aa3b, v65
	s_waitcnt lgkmcnt(1)
	v_mul_f32_e32 v64, v134, v64
	v_cvt_pk_bf16_f32 v64, v64, v2
	v_add_f32_e32 v88, 1.0, v88
	v_lshlrev_b32_e32 v64, 16, v64
	v_mul_f32_e32 v129, 0x3fb8aa3b, v64
	v_exp_f32_e32 v129, v129
	v_rcp_f32_e32 v88, v88
	v_exp_f32_e32 v65, v65
	v_add_f32_e32 v66, v66, v140
	v_fma_f32 v130, -v129, v129, 1.0
	v_max_f32_e32 v130, 0, v130
	v_sqrt_f32_e32 v130, v130
	v_mul_f32_e32 v66, 0xbfb8aa3b, v66
	v_exp_f32_e32 v66, v66
	v_add_f32_e32 v67, v67, v141
	v_mul_f32_e32 v88, v88, v130
	s_waitcnt lgkmcnt(0)
; #define LAS __attribute__((address_space(3)))
; __device__ __forceinline__ unsigned cvt_pk_bf16(float lo, float hi) { unsigned r; asm volatile("v_cvt_pk_bf16_f32 %0, %1, %2" : "=v"(r) : "v"(lo), "v"(hi)); return r; }
; __device__ __forceinline__ float sigmoidf_(float x) { return __builtin_amdgcn_rcpf(1.0f + __expf(-x)); }
; __device__ __forceinline__ void lru_gates(const Frame& F, LAS bf16_t* Wl, const LAS float* CT, LAS float* ucb, float (&av)[2][4][4], unsigned (&pw)[2][4][4]) {
;     ...
;             const f32x4 ba4 = *(const LAS f32x4*)(CT + (5 + 3 * d) * 64 + et * 16 + 4 * g), bx4 = *(const LAS f32x4*)(CT + (6 + 3 * d) * 64 + et * 16 + 4 * g), cs4 = *(const LAS f32x4*)(CT + (7 + 3 * d) * 64 + et * 16 + 4 * g);
;             const f32x4 u4 = *(const LAS f32x4*)(ucb + tk * 68 + et * 16 + 4 * g);
; #pragma unroll
;             for (int i = 0; i < 4; ++i) {
;                 const float r = sigmoidf_(ra[i] + ba4[i]), ig = sigmoidf_(ri[i] + bx4[i]);
;                 const float la = __uint_as_float(cvt_pk_bf16(cs4[i] * r, 0.f) << 16), a = __expf(la);
;                 av[d][et][i] = a; pw[d][et][i] = cvt_pk_bf16(la, __builtin_amdgcn_sqrtf(fmaxf(1.0f - a * a, 0.f)) * ig * u4[i]); }
; __device__ __forceinline__ void ph_lru_a(const Frame& F, int jj) {
;     ...
;             for (int d = 0; d < 2; ++d)
; #pragma unroll
;                 for (int et = 0; et < 4; ++et) { u32x4 w; w.x = pw[d][et][0]; w.y = pw[d][et][1]; w.z = pw[d][et][2]; w.w = pw[d][et][3];
;                     __builtin_nontemporal_store(w, (u32x4*)(GX + (((size_t)row * 2 + d) * 1024 + kb * 64 + et * 16 + 4 * g) * 2));
; #pragma unroll
;                     for (int i = 0; i < 4; ++i) xv[d][et][i] = __uint_as_float(pw[d][et][i] & 0xffff0000u); }
	v_mul_f32_e32 v88, v146, v88
	v_cvt_pk_bf16_f32 v88, v64, v88
	v_add_f32_e32 v64, 1.0, v65
	v_rcp_f32_e32 v64, v64
	v_add_f32_e32 v65, v131, v89
	v_mul_f32_e32 v65, 0xbfb8aa3b, v65
	v_exp_f32_e32 v65, v65
	v_mul_f32_e32 v64, v135, v64
	v_cvt_pk_bf16_f32 v64, v64, v2
	v_mul_f32_e32 v67, 0xbfb8aa3b, v67
	v_lshlrev_b32_e32 v64, 16, v64
	v_mul_f32_e32 v89, 0x3fb8aa3b, v64
	v_exp_f32_e32 v130, v89
	v_add_f32_e32 v65, 1.0, v65
	v_rcp_f32_e32 v65, v65
	v_exp_f32_e32 v67, v67
	v_fma_f32 v89, -v130, v130, 1.0
	v_max_f32_e32 v89, 0, v89
	v_sqrt_f32_e32 v89, v89
	s_nop 0
	v_mul_f32_e32 v65, v65, v89
	v_mul_f32_e32 v65, v147, v65
	v_cvt_pk_bf16_f32 v89, v64, v65
	v_add_f32_e32 v64, 1.0, v66
	v_rcp_f32_e32 v64, v64
	v_add_f32_e32 v65, v132, v90
	v_mul_f32_e32 v65, 0xbfb8aa3b, v65
	v_exp_f32_e32 v65, v65
	v_mul_f32_e32 v64, v136, v64
	v_cvt_pk_bf16_f32 v64, v64, v2
	v_add_f32_e32 v65, 1.0, v65
	v_lshlrev_b32_e32 v64, 16, v64
	v_mul_f32_e32 v66, 0x3fb8aa3b, v64
	v_exp_f32_e32 v131, v66
	v_rcp_f32_e32 v65, v65
	v_fma_f32 v66, -v131, v131, 1.0
	v_max_f32_e32 v66, 0, v66
	v_sqrt_f32_e32 v66, v66
	s_nop 0
	v_mul_f32_e32 v65, v65, v66
	v_mul_f32_e32 v65, v148, v65
	v_cvt_pk_bf16_f32 v90, v64, v65
	v_add_f32_e32 v64, 1.0, v67
	v_rcp_f32_e32 v64, v64
	v_add_f32_e32 v65, v133, v91
	v_mul_f32_e32 v65, 0xbfb8aa3b, v65
	v_exp_f32_e32 v65, v65
	v_mul_f32_e32 v64, v137, v64
	v_cvt_pk_bf16_f32 v64, v64, v2
	v_add_f32_e32 v65, 1.0, v65
	v_lshlrev_b32_e32 v64, 16, v64
	v_mul_f32_e32 v66, 0x3fb8aa3b, v64
	v_exp_f32_e32 v132, v66
	v_rcp_f32_e32 v65, v65
	v_fma_f32 v66, -v132, v132, 1.0
	v_max_f32_e32 v66, 0, v66
	v_sqrt_f32_e32 v66, v66
	s_nop 0
	v_mul_f32_e32 v65, v65, v66
	v_mul_f32_e32 v65, v149, v65
	v_cvt_pk_bf16_f32 v91, v64, v65
	ds_read_b128 v[64:67], v114 offset:25344
	ds_read_b128 v[134:137], v114 offset:25408
	ds_read_b128 v[138:141], v114 offset:34560
	ds_read_b128 v[146:149], v114 offset:34624
	s_waitcnt lgkmcnt(3)
	v_mfma_f32_16x16x32_bf16 v[64:67], v[64:67], v[56:59], 0
	s_waitcnt lgkmcnt(1)
	v_mfma_f32_16x16x32_bf16 v[56:59], v[138:141], v[56:59], 0
	ds_read_b128 v[138:141], v115 offset:192
	v_mfma_f32_16x16x32_bf16 v[64:67], v[134:137], v[60:63], v[64:67]
	ds_read_b128 v[134:137], v116 offset:192
	s_waitcnt lgkmcnt(2)
	v_mfma_f32_16x16x32_bf16 v[56:59], v[146:149], v[60:63], v[56:59]
	ds_read_b128 v[60:63], v117 offset:192
	ds_read_b128 v[146:149], v120 offset:37056
	s_waitcnt lgkmcnt(3)
	s_nop 1
	v_add_f32_e32 v64, v64, v138
	v_mul_f32_e32 v64, 0xbfb8aa3b, v64
	v_exp_f32_e32 v64, v64
	s_waitcnt lgkmcnt(2)
	v_add_f32_e32 v56, v56, v134
	v_mul_f32_e32 v56, 0xbfb8aa3b, v56
	v_exp_f32_e32 v56, v56
	v_add_f32_e32 v64, 1.0, v64
	v_rcp_f32_e32 v64, v64
	v_add_f32_e32 v65, v65, v139
	v_add_f32_e32 v56, 1.0, v56
	v_rcp_f32_e32 v56, v56
	s_waitcnt lgkmcnt(1)
	v_mul_f32_e32 v60, v60, v64
	v_cvt_pk_bf16_f32 v60, v60, v2
	v_mul_f32_e32 v65, 0xbfb8aa3b, v65
	v_lshlrev_b32_e32 v60, 16, v60
	v_mul_f32_e32 v64, 0x3fb8aa3b, v60
	v_exp_f32_e32 v133, v64
	v_exp_f32_e32 v65, v65
	v_add_f32_e32 v57, v57, v135
	v_mul_f32_e32 v57, 0xbfb8aa3b, v57
	v_fma_f32 v64, -v133, v133, 1.0
	v_max_f32_e32 v64, 0, v64
	v_sqrt_f32_e32 v64, v64
	v_exp_f32_e32 v57, v57
	v_mul_f32_e32 v56, v56, v64
	s_waitcnt lgkmcnt(0)
	v_mul_f32_e32 v56, v146, v56
	v_cvt_pk_bf16_f32 v138, v60, v56
	v_add_f32_e32 v56, 1.0, v65
	v_rcp_f32_e32 v56, v56
	v_add_f32_e32 v57, 1.0, v57
	v_rcp_f32_e32 v57, v57
	v_and_b32_e32 v64, 0xffff0000, v52
	v_mul_f32_e32 v56, v61, v56
	v_cvt_pk_bf16_f32 v56, v56, v2
	v_add_f32_e32 v61, v66, v140
	v_lshlrev_b32_e32 v56, 16, v56
	v_mul_f32_e32 v60, 0x3fb8aa3b, v56
	v_exp_f32_e32 v134, v60
	v_mul_f32_e32 v61, 0xbfb8aa3b, v61
	v_exp_f32_e32 v61, v61
	v_and_b32_e32 v65, 0xffff0000, v53
	v_fma_f32 v60, -v134, v134, 1.0
	v_max_f32_e32 v60, 0, v60
	v_sqrt_f32_e32 v60, v60
	v_and_b32_e32 v66, 0xffff0000, v54
	v_mul_f32_e32 v57, v57, v60
	v_mul_f32_e32 v57, v147, v57
	v_cvt_pk_bf16_f32 v139, v56, v57
	v_add_f32_e32 v56, 1.0, v61
	v_rcp_f32_e32 v56, v56
	v_add_f32_e32 v57, v58, v136
	v_mul_f32_e32 v57, 0xbfb8aa3b, v57
	v_exp_f32_e32 v57, v57
	v_mul_f32_e32 v56, v62, v56
	v_cvt_pk_bf16_f32 v56, v56, v2
	v_add_f32_e32 v60, v67, v141
	v_lshlrev_b32_e32 v56, 16, v56
	v_mul_f32_e32 v58, 0x3fb8aa3b, v56
	v_exp_f32_e32 v135, v58
	v_add_f32_e32 v57, 1.0, v57
	v_rcp_f32_e32 v57, v57
	v_mul_f32_e32 v60, 0xbfb8aa3b, v60
	v_fma_f32 v58, -v135, v135, 1.0
	v_max_f32_e32 v58, 0, v58
	v_sqrt_f32_e32 v58, v58
	v_exp_f32_e32 v60, v60
	v_and_b32_e32 v67, 0xffff0000, v55
	v_and_b32_e32 v61, 0xffff0000, v69
	v_mul_f32_e32 v57, v57, v58
	v_mul_f32_e32 v57, v148, v57
	v_cvt_pk_bf16_f32 v140, v56, v57
	v_add_f32_e32 v56, 1.0, v60
	v_rcp_f32_e32 v56, v56
	v_add_f32_e32 v57, v59, v137
	v_mul_f32_e32 v57, 0xbfb8aa3b, v57
	v_exp_f32_e32 v57, v57
	v_mul_f32_e32 v56, v63, v56
	v_cvt_pk_bf16_f32 v56, v56, v2
	v_and_b32_e32 v60, 0xffff0000, v68
	v_lshlrev_b32_e32 v56, 16, v56
	v_mul_f32_e32 v58, 0x3fb8aa3b, v56
	v_exp_f32_e32 v136, v58
	v_add_f32_e32 v57, 1.0, v57
	v_rcp_f32_e32 v57, v57
	v_and_b32_e32 v62, 0xffff0000, v70
	v_fma_f32 v58, -v136, v136, 1.0
	v_max_f32_e32 v58, 0, v58
	v_sqrt_f32_e32 v58, v58
	v_and_b32_e32 v63, 0xffff0000, v71
	v_and_b32_e32 v59, 0xffff0000, v75
	v_mul_f32_e32 v57, v57, v58
	v_mul_f32_e32 v57, v149, v57
	v_cvt_pk_bf16_f32 v141, v56, v57
	v_add_u32_e32 v56, s8, v121
	v_ashrrev_i32_e32 v57, 31, v56
	v_lshlrev_b64 v[56:57], 13, v[56:57]
	v_lshl_add_u64 v[142:143], v[98:99], 0, v[56:57]
	global_store_dwordx4 v[142:143], v[52:55], off nt
	global_store_dwordx4 v[142:143], v[68:71], off offset:64 nt
	global_store_dwordx4 v[142:143], v[72:75], off offset:128 nt
; __device__ __forceinline__ void ph_lru_a(const Frame& F, int jj) {
;     ...
;                 for (int et = 0; et < 4; ++et) { u32x4 w; w.x = pw[d][et][0]; w.y = pw[d][et][1]; w.z = pw[d][et][2]; w.w = pw[d][et][3];
;                     __builtin_nontemporal_store(w, (u32x4*)(GX + (((size_t)row * 2 + d) * 1024 + kb * 64 + et * 16 + 4 * g) * 2));
	global_store_dwordx4 v[142:143], v[76:79], off offset:192 nt
	v_add_co_u32_e32 v142, vcc, s97, v142
	v_and_b32_e32 v56, 0xffff0000, v72
	s_nop 0
	v_addc_co_u32_e32 v143, vcc, 0, v143, vcc
	v_and_b32_e32 v57, 0xffff0000, v73
	v_and_b32_e32 v58, 0xffff0000, v74
	v_and_b32_e32 v52, 0xffff0000, v76
	v_and_b32_e32 v53, 0xffff0000, v77
	v_and_b32_e32 v54, 0xffff0000, v78
	v_and_b32_e32 v55, 0xffff0000, v79
	global_store_dwordx4 v[142:143], v[80:83], off nt
	v_and_b32_e32 v68, 0xffff0000, v80
	v_and_b32_e32 v69, 0xffff0000, v81
	v_and_b32_e32 v70, 0xffff0000, v82
	v_and_b32_e32 v71, 0xffff0000, v83
	v_and_b32_e32 v72, 0xffff0000, v84
	v_and_b32_e32 v73, 0xffff0000, v85
	v_and_b32_e32 v74, 0xffff0000, v86
	v_and_b32_e32 v75, 0xffff0000, v87
	v_and_b32_e32 v76, 0xffff0000, v88
	v_and_b32_e32 v77, 0xffff0000, v89
	v_and_b32_e32 v78, 0xffff0000, v90
	v_and_b32_e32 v79, 0xffff0000, v91
	v_and_b32_e32 v80, 0xffff0000, v138
	v_and_b32_e32 v81, 0xffff0000, v139
	v_and_b32_e32 v82, 0xffff0000, v140
	v_and_b32_e32 v83, 0xffff0000, v141
	global_store_dwordx4 v[142:143], v[84:87], off offset:64 nt
	global_store_dwordx4 v[142:143], v[88:91], off offset:128 nt
	global_store_dwordx4 v[142:143], v[138:141], off offset:192 nt
	v_fmac_f32_dpp v64, v64, v36 row_shr:1 row_mask:0xf bank_mask:0xf
	v_fmac_f32_dpp v65, v65, v37 row_shr:1 row_mask:0xf bank_mask:0xf
	v_fmac_f32_dpp v66, v66, v38 row_shr:1 row_mask:0xf bank_mask:0xf
	v_fmac_f32_dpp v67, v67, v39 row_shr:1 row_mask:0xf bank_mask:0xf
	v_mul_f32_dpp v36, v36, v36 row_shr:1 row_mask:0xf bank_mask:0xf
	v_mul_f32_dpp v37, v37, v37 row_shr:1 row_mask:0xf bank_mask:0xf
	v_mul_f32_dpp v38, v38, v38 row_shr:1 row_mask:0xf bank_mask:0xf
	v_mul_f32_dpp v39, v39, v39 row_shr:1 row_mask:0xf bank_mask:0xf
	v_fmac_f32_dpp v68, v68, v103 row_shl:1 row_mask:0xf bank_mask:0xf
	v_fmac_f32_dpp v69, v69, v122 row_shl:1 row_mask:0xf bank_mask:0xf
	v_fmac_f32_dpp v70, v70, v123 row_shl:1 row_mask:0xf bank_mask:0xf
	v_fmac_f32_dpp v71, v71, v124 row_shl:1 row_mask:0xf bank_mask:0xf
	v_mul_f32_dpp v103, v103, v103 row_shl:1 row_mask:0xf bank_mask:0xf
	v_mul_f32_dpp v122, v122, v122 row_shl:1 row_mask:0xf bank_mask:0xf
	v_mul_f32_dpp v123, v123, v123 row_shl:1 row_mask:0xf bank_mask:0xf
	v_mul_f32_dpp v124, v124, v124 row_shl:1 row_mask:0xf bank_mask:0xf
	v_fmac_f32_dpp v60, v60, v40 row_shr:1 row_mask:0xf bank_mask:0xf
	v_fmac_f32_dpp v61, v61, v41 row_shr:1 row_mask:0xf bank_mask:0xf
	v_fmac_f32_dpp v62, v62, v42 row_shr:1 row_mask:0xf bank_mask:0xf
	v_fmac_f32_dpp v63, v63, v43 row_shr:1 row_mask:0xf bank_mask:0xf
	v_mul_f32_dpp v40, v40, v40 row_shr:1 row_mask:0xf bank_mask:0xf
	v_mul_f32_dpp v41, v41, v41 row_shr:1 row_mask:0xf bank_mask:0xf
	v_mul_f32_dpp v42, v42, v42 row_shr:1 row_mask:0xf bank_mask:0xf
	v_mul_f32_dpp v43, v43, v43 row_shr:1 row_mask:0xf bank_mask:0xf
	v_fmac_f32_dpp v72, v72, v125 row_shl:1 row_mask:0xf bank_mask:0xf
	v_fmac_f32_dpp v73, v73, v126 row_shl:1 row_mask:0xf bank_mask:0xf
	v_fmac_f32_dpp v74, v74, v127 row_shl:1 row_mask:0xf bank_mask:0xf
	v_fmac_f32_dpp v75, v75, v128 row_shl:1 row_mask:0xf bank_mask:0xf
	v_mul_f32_dpp v125, v125, v125 row_shl:1 row_mask:0xf bank_mask:0xf
	v_mul_f32_dpp v126, v126, v126 row_shl:1 row_mask:0xf bank_mask:0xf
	v_mul_f32_dpp v127, v127, v127 row_shl:1 row_mask:0xf bank_mask:0xf
	v_mul_f32_dpp v128, v128, v128 row_shl:1 row_mask:0xf bank_mask:0xf
	v_fmac_f32_dpp v56, v56, v44 row_shr:1 row_mask:0xf bank_mask:0xf
	v_fmac_f32_dpp v57, v57, v45 row_shr:1 row_mask:0xf bank_mask:0xf
	v_fmac_f32_dpp v58, v58, v46 row_shr:1 row_mask:0xf bank_mask:0xf
	v_fmac_f32_dpp v59, v59, v47 row_shr:1 row_mask:0xf bank_mask:0xf
	v_mul_f32_dpp v44, v44, v44 row_shr:1 row_mask:0xf bank_mask:0xf
	v_mul_f32_dpp v45, v45, v45 row_shr:1 row_mask:0xf bank_mask:0xf
	v_mul_f32_dpp v46, v46, v46 row_shr:1 row_mask:0xf bank_mask:0xf
	v_mul_f32_dpp v47, v47, v47 row_shr:1 row_mask:0xf bank_mask:0xf
	v_fmac_f32_dpp v76, v76, v129 row_shl:1 row_mask:0xf bank_mask:0xf
	v_fmac_f32_dpp v77, v77, v130 row_shl:1 row_mask:0xf bank_mask:0xf
	v_fmac_f32_dpp v78, v78, v131 row_shl:1 row_mask:0xf bank_mask:0xf
	v_fmac_f32_dpp v79, v79, v132 row_shl:1 row_mask:0xf bank_mask:0xf
	v_mul_f32_dpp v129, v129, v129 row_shl:1 row_mask:0xf bank_mask:0xf
	v_mul_f32_dpp v130, v130, v130 row_shl:1 row_mask:0xf bank_mask:0xf
	v_mul_f32_dpp v131, v131, v131 row_shl:1 row_mask:0xf bank_mask:0xf
	v_mul_f32_dpp v132, v132, v132 row_shl:1 row_mask:0xf bank_mask:0xf
	v_fmac_f32_dpp v52, v52, v48 row_shr:1 row_mask:0xf bank_mask:0xf
	v_fmac_f32_dpp v53, v53, v49 row_shr:1 row_mask:0xf bank_mask:0xf
	v_fmac_f32_dpp v54, v54, v50 row_shr:1 row_mask:0xf bank_mask:0xf
	v_fmac_f32_dpp v55, v55, v51 row_shr:1 row_mask:0xf bank_mask:0xf
	v_mul_f32_dpp v48, v48, v48 row_shr:1 row_mask:0xf bank_mask:0xf
	v_mul_f32_dpp v49, v49, v49 row_shr:1 row_mask:0xf bank_mask:0xf
	v_mul_f32_dpp v50, v50, v50 row_shr:1 row_mask:0xf bank_mask:0xf
	v_mul_f32_dpp v51, v51, v51 row_shr:1 row_mask:0xf bank_mask:0xf
	v_fmac_f32_dpp v80, v80, v133 row_shl:1 row_mask:0xf bank_mask:0xf
	v_fmac_f32_dpp v81, v81, v134 row_shl:1 row_mask:0xf bank_mask:0xf
	v_fmac_f32_dpp v82, v82, v135 row_shl:1 row_mask:0xf bank_mask:0xf
	v_fmac_f32_dpp v83, v83, v136 row_shl:1 row_mask:0xf bank_mask:0xf
	v_mul_f32_dpp v133, v133, v133 row_shl:1 row_mask:0xf bank_mask:0xf
	v_mul_f32_dpp v134, v134, v134 row_shl:1 row_mask:0xf bank_mask:0xf
	v_mul_f32_dpp v135, v135, v135 row_shl:1 row_mask:0xf bank_mask:0xf
	v_mul_f32_dpp v136, v136, v136 row_shl:1 row_mask:0xf bank_mask:0xf
	s_nop 0
	v_fmac_f32_dpp v64, v64, v36 row_shr:2 row_mask:0xf bank_mask:0xf
	v_fmac_f32_dpp v65, v65, v37 row_shr:2 row_mask:0xf bank_mask:0xf
	v_fmac_f32_dpp v66, v66, v38 row_shr:2 row_mask:0xf bank_mask:0xf
	v_fmac_f32_dpp v67, v67, v39 row_shr:2 row_mask:0xf bank_mask:0xf
	v_mul_f32_dpp v36, v36, v36 row_shr:2 row_mask:0xf bank_mask:0xf
	v_mul_f32_dpp v37, v37, v37 row_shr:2 row_mask:0xf bank_mask:0xf
	v_mul_f32_dpp v38, v38, v38 row_shr:2 row_mask:0xf bank_mask:0xf
	v_mul_f32_dpp v39, v39, v39 row_shr:2 row_mask:0xf bank_mask:0xf
	v_fmac_f32_dpp v68, v68, v103 row_shl:2 row_mask:0xf bank_mask:0xf
	v_fmac_f32_dpp v69, v69, v122 row_shl:2 row_mask:0xf bank_mask:0xf
	v_fmac_f32_dpp v70, v70, v123 row_shl:2 row_mask:0xf bank_mask:0xf
	v_fmac_f32_dpp v71, v71, v124 row_shl:2 row_mask:0xf bank_mask:0xf
	v_mul_f32_dpp v103, v103, v103 row_shl:2 row_mask:0xf bank_mask:0xf
	v_mul_f32_dpp v122, v122, v122 row_shl:2 row_mask:0xf bank_mask:0xf
	v_mul_f32_dpp v123, v123, v123 row_shl:2 row_mask:0xf bank_mask:0xf
	v_mul_f32_dpp v124, v124, v124 row_shl:2 row_mask:0xf bank_mask:0xf
	v_fmac_f32_dpp v60, v60, v40 row_shr:2 row_mask:0xf bank_mask:0xf
	v_fmac_f32_dpp v61, v61, v41 row_shr:2 row_mask:0xf bank_mask:0xf
	v_fmac_f32_dpp v62, v62, v42 row_shr:2 row_mask:0xf bank_mask:0xf
	v_fmac_f32_dpp v63, v63, v43 row_shr:2 row_mask:0xf bank_mask:0xf
	v_mul_f32_dpp v40, v40, v40 row_shr:2 row_mask:0xf bank_mask:0xf
	v_mul_f32_dpp v41, v41, v41 row_shr:2 row_mask:0xf bank_mask:0xf
	v_mul_f32_dpp v42, v42, v42 row_shr:2 row_mask:0xf bank_mask:0xf
	v_mul_f32_dpp v43, v43, v43 row_shr:2 row_mask:0xf bank_mask:0xf
	v_fmac_f32_dpp v72, v72, v125 row_shl:2 row_mask:0xf bank_mask:0xf
	v_fmac_f32_dpp v73, v73, v126 row_shl:2 row_mask:0xf bank_mask:0xf
	v_fmac_f32_dpp v74, v74, v127 row_shl:2 row_mask:0xf bank_mask:0xf
	v_fmac_f32_dpp v75, v75, v128 row_shl:2 row_mask:0xf bank_mask:0xf
	v_mul_f32_dpp v125, v125, v125 row_shl:2 row_mask:0xf bank_mask:0xf
	v_mul_f32_dpp v126, v126, v126 row_shl:2 row_mask:0xf bank_mask:0xf
	v_mul_f32_dpp v127, v127, v127 row_shl:2 row_mask:0xf bank_mask:0xf
	v_mul_f32_dpp v128, v128, v128 row_shl:2 row_mask:0xf bank_mask:0xf
	v_fmac_f32_dpp v56, v56, v44 row_shr:2 row_mask:0xf bank_mask:0xf
	v_fmac_f32_dpp v57, v57, v45 row_shr:2 row_mask:0xf bank_mask:0xf
	v_fmac_f32_dpp v58, v58, v46 row_shr:2 row_mask:0xf bank_mask:0xf
	v_fmac_f32_dpp v59, v59, v47 row_shr:2 row_mask:0xf bank_mask:0xf
	v_mul_f32_dpp v44, v44, v44 row_shr:2 row_mask:0xf bank_mask:0xf
	v_mul_f32_dpp v45, v45, v45 row_shr:2 row_mask:0xf bank_mask:0xf
	v_mul_f32_dpp v46, v46, v46 row_shr:2 row_mask:0xf bank_mask:0xf
	v_mul_f32_dpp v47, v47, v47 row_shr:2 row_mask:0xf bank_mask:0xf
	v_fmac_f32_dpp v76, v76, v129 row_shl:2 row_mask:0xf bank_mask:0xf
	v_fmac_f32_dpp v77, v77, v130 row_shl:2 row_mask:0xf bank_mask:0xf
	v_fmac_f32_dpp v78, v78, v131 row_shl:2 row_mask:0xf bank_mask:0xf
	v_fmac_f32_dpp v79, v79, v132 row_shl:2 row_mask:0xf bank_mask:0xf
	v_mul_f32_dpp v129, v129, v129 row_shl:2 row_mask:0xf bank_mask:0xf
	v_mul_f32_dpp v130, v130, v130 row_shl:2 row_mask:0xf bank_mask:0xf
	v_mul_f32_dpp v131, v131, v131 row_shl:2 row_mask:0xf bank_mask:0xf
	v_mul_f32_dpp v132, v132, v132 row_shl:2 row_mask:0xf bank_mask:0xf
	v_fmac_f32_dpp v52, v52, v48 row_shr:2 row_mask:0xf bank_mask:0xf
	v_fmac_f32_dpp v53, v53, v49 row_shr:2 row_mask:0xf bank_mask:0xf
	v_fmac_f32_dpp v54, v54, v50 row_shr:2 row_mask:0xf bank_mask:0xf
	v_fmac_f32_dpp v55, v55, v51 row_shr:2 row_mask:0xf bank_mask:0xf
	v_mul_f32_dpp v48, v48, v48 row_shr:2 row_mask:0xf bank_mask:0xf
	v_mul_f32_dpp v49, v49, v49 row_shr:2 row_mask:0xf bank_mask:0xf
	v_mul_f32_dpp v50, v50, v50 row_shr:2 row_mask:0xf bank_mask:0xf
	v_mul_f32_dpp v51, v51, v51 row_shr:2 row_mask:0xf bank_mask:0xf
	v_fmac_f32_dpp v80, v80, v133 row_shl:2 row_mask:0xf bank_mask:0xf
	v_fmac_f32_dpp v81, v81, v134 row_shl:2 row_mask:0xf bank_mask:0xf
	v_fmac_f32_dpp v82, v82, v135 row_shl:2 row_mask:0xf bank_mask:0xf
	v_fmac_f32_dpp v83, v83, v136 row_shl:2 row_mask:0xf bank_mask:0xf
	v_mul_f32_dpp v133, v133, v133 row_shl:2 row_mask:0xf bank_mask:0xf
	v_mul_f32_dpp v134, v134, v134 row_shl:2 row_mask:0xf bank_mask:0xf
	v_mul_f32_dpp v135, v135, v135 row_shl:2 row_mask:0xf bank_mask:0xf
	v_mul_f32_dpp v136, v136, v136 row_shl:2 row_mask:0xf bank_mask:0xf
	s_nop 0
	v_fmac_f32_dpp v64, v64, v36 row_shr:4 row_mask:0xf bank_mask:0xf
	v_fmac_f32_dpp v65, v65, v37 row_shr:4 row_mask:0xf bank_mask:0xf
	v_fmac_f32_dpp v66, v66, v38 row_shr:4 row_mask:0xf bank_mask:0xf
	v_fmac_f32_dpp v67, v67, v39 row_shr:4 row_mask:0xf bank_mask:0xf
	v_mul_f32_dpp v36, v36, v36 row_shr:4 row_mask:0xf bank_mask:0xf
	v_mul_f32_dpp v37, v37, v37 row_shr:4 row_mask:0xf bank_mask:0xf
	v_mul_f32_dpp v38, v38, v38 row_shr:4 row_mask:0xf bank_mask:0xf
	v_mul_f32_dpp v39, v39, v39 row_shr:4 row_mask:0xf bank_mask:0xf
	v_fmac_f32_dpp v68, v68, v103 row_shl:4 row_mask:0xf bank_mask:0xf
	v_fmac_f32_dpp v69, v69, v122 row_shl:4 row_mask:0xf bank_mask:0xf
	v_fmac_f32_dpp v70, v70, v123 row_shl:4 row_mask:0xf bank_mask:0xf
	v_fmac_f32_dpp v71, v71, v124 row_shl:4 row_mask:0xf bank_mask:0xf
	v_mul_f32_dpp v103, v103, v103 row_shl:4 row_mask:0xf bank_mask:0xf
	v_mul_f32_dpp v122, v122, v122 row_shl:4 row_mask:0xf bank_mask:0xf
	v_mul_f32_dpp v123, v123, v123 row_shl:4 row_mask:0xf bank_mask:0xf
	v_mul_f32_dpp v124, v124, v124 row_shl:4 row_mask:0xf bank_mask:0xf
	v_fmac_f32_dpp v60, v60, v40 row_shr:4 row_mask:0xf bank_mask:0xf
	v_fmac_f32_dpp v61, v61, v41 row_shr:4 row_mask:0xf bank_mask:0xf
	v_fmac_f32_dpp v62, v62, v42 row_shr:4 row_mask:0xf bank_mask:0xf
	v_fmac_f32_dpp v63, v63, v43 row_shr:4 row_mask:0xf bank_mask:0xf
	v_mul_f32_dpp v40, v40, v40 row_shr:4 row_mask:0xf bank_mask:0xf
	v_mul_f32_dpp v41, v41, v41 row_shr:4 row_mask:0xf bank_mask:0xf
	v_mul_f32_dpp v42, v42, v42 row_shr:4 row_mask:0xf bank_mask:0xf
	v_mul_f32_dpp v43, v43, v43 row_shr:4 row_mask:0xf bank_mask:0xf
	v_fmac_f32_dpp v72, v72, v125 row_shl:4 row_mask:0xf bank_mask:0xf
	v_fmac_f32_dpp v73, v73, v126 row_shl:4 row_mask:0xf bank_mask:0xf
	v_fmac_f32_dpp v74, v74, v127 row_shl:4 row_mask:0xf bank_mask:0xf
	v_fmac_f32_dpp v75, v75, v128 row_shl:4 row_mask:0xf bank_mask:0xf
	v_mul_f32_dpp v125, v125, v125 row_shl:4 row_mask:0xf bank_mask:0xf
	v_mul_f32_dpp v126, v126, v126 row_shl:4 row_mask:0xf bank_mask:0xf
	v_mul_f32_dpp v127, v127, v127 row_shl:4 row_mask:0xf bank_mask:0xf
	v_mul_f32_dpp v128, v128, v128 row_shl:4 row_mask:0xf bank_mask:0xf
	v_fmac_f32_dpp v56, v56, v44 row_shr:4 row_mask:0xf bank_mask:0xf
	v_fmac_f32_dpp v57, v57, v45 row_shr:4 row_mask:0xf bank_mask:0xf
	v_fmac_f32_dpp v58, v58, v46 row_shr:4 row_mask:0xf bank_mask:0xf
	v_fmac_f32_dpp v59, v59, v47 row_shr:4 row_mask:0xf bank_mask:0xf
	v_mul_f32_dpp v44, v44, v44 row_shr:4 row_mask:0xf bank_mask:0xf
	v_mul_f32_dpp v45, v45, v45 row_shr:4 row_mask:0xf bank_mask:0xf
	v_mul_f32_dpp v46, v46, v46 row_shr:4 row_mask:0xf bank_mask:0xf
	v_mul_f32_dpp v47, v47, v47 row_shr:4 row_mask:0xf bank_mask:0xf
	v_fmac_f32_dpp v76, v76, v129 row_shl:4 row_mask:0xf bank_mask:0xf
	v_fmac_f32_dpp v77, v77, v130 row_shl:4 row_mask:0xf bank_mask:0xf
	v_fmac_f32_dpp v78, v78, v131 row_shl:4 row_mask:0xf bank_mask:0xf
	v_fmac_f32_dpp v79, v79, v132 row_shl:4 row_mask:0xf bank_mask:0xf
	v_mul_f32_dpp v129, v129, v129 row_shl:4 row_mask:0xf bank_mask:0xf
	v_mul_f32_dpp v130, v130, v130 row_shl:4 row_mask:0xf bank_mask:0xf
	v_mul_f32_dpp v131, v131, v131 row_shl:4 row_mask:0xf bank_mask:0xf
	v_mul_f32_dpp v132, v132, v132 row_shl:4 row_mask:0xf bank_mask:0xf
	v_fmac_f32_dpp v52, v52, v48 row_shr:4 row_mask:0xf bank_mask:0xf
	v_fmac_f32_dpp v53, v53, v49 row_shr:4 row_mask:0xf bank_mask:0xf
	v_fmac_f32_dpp v54, v54, v50 row_shr:4 row_mask:0xf bank_mask:0xf
	v_fmac_f32_dpp v55, v55, v51 row_shr:4 row_mask:0xf bank_mask:0xf
	v_mul_f32_dpp v48, v48, v48 row_shr:4 row_mask:0xf bank_mask:0xf
	v_mul_f32_dpp v49, v49, v49 row_shr:4 row_mask:0xf bank_mask:0xf
	v_mul_f32_dpp v50, v50, v50 row_shr:4 row_mask:0xf bank_mask:0xf
	v_mul_f32_dpp v51, v51, v51 row_shr:4 row_mask:0xf bank_mask:0xf
	v_fmac_f32_dpp v80, v80, v133 row_shl:4 row_mask:0xf bank_mask:0xf
	v_fmac_f32_dpp v81, v81, v134 row_shl:4 row_mask:0xf bank_mask:0xf
	v_fmac_f32_dpp v82, v82, v135 row_shl:4 row_mask:0xf bank_mask:0xf
	v_fmac_f32_dpp v83, v83, v136 row_shl:4 row_mask:0xf bank_mask:0xf
	v_mul_f32_dpp v133, v133, v133 row_shl:4 row_mask:0xf bank_mask:0xf
	v_mul_f32_dpp v134, v134, v134 row_shl:4 row_mask:0xf bank_mask:0xf
	v_mul_f32_dpp v135, v135, v135 row_shl:4 row_mask:0xf bank_mask:0xf
	v_mul_f32_dpp v136, v136, v136 row_shl:4 row_mask:0xf bank_mask:0xf
	v_cmp_lt_i32_e32 vcc, 14, v104
	s_mov_b64 s[8:9], 0
	v_fmac_f32_dpp v64, v64, v36 row_shr:8 row_mask:0xf bank_mask:0xf
	v_fmac_f32_dpp v65, v65, v37 row_shr:8 row_mask:0xf bank_mask:0xf
	v_fmac_f32_dpp v66, v66, v38 row_shr:8 row_mask:0xf bank_mask:0xf
	v_fmac_f32_dpp v67, v67, v39 row_shr:8 row_mask:0xf bank_mask:0xf
	v_mul_f32_dpp v36, v36, v36 row_shr:8 row_mask:0xf bank_mask:0xf
	v_mul_f32_dpp v37, v37, v37 row_shr:8 row_mask:0xf bank_mask:0xf
	v_mul_f32_dpp v38, v38, v38 row_shr:8 row_mask:0xf bank_mask:0xf
	v_mul_f32_dpp v39, v39, v39 row_shr:8 row_mask:0xf bank_mask:0xf
	v_fmac_f32_dpp v68, v68, v103 row_shl:8 row_mask:0xf bank_mask:0xf
	v_fmac_f32_dpp v69, v69, v122 row_shl:8 row_mask:0xf bank_mask:0xf
	v_fmac_f32_dpp v70, v70, v123 row_shl:8 row_mask:0xf bank_mask:0xf
; __device__ __forceinline__ void ph_lru_a(const Frame& F, int jj) {
;     ...
; #pragma unroll
;             for (int d = 0; d < 2; ++d) if (tk == (d ? 0 : 15)) {
	v_fmac_f32_dpp v71, v71, v124 row_shl:8 row_mask:0xf bank_mask:0xf
	v_mul_f32_dpp v103, v103, v103 row_shl:8 row_mask:0xf bank_mask:0xf
	v_mul_f32_dpp v122, v122, v122 row_shl:8 row_mask:0xf bank_mask:0xf
	v_mul_f32_dpp v123, v123, v123 row_shl:8 row_mask:0xf bank_mask:0xf
	v_mul_f32_dpp v124, v124, v124 row_shl:8 row_mask:0xf bank_mask:0xf
	v_fmac_f32_dpp v60, v60, v40 row_shr:8 row_mask:0xf bank_mask:0xf
	v_fmac_f32_dpp v61, v61, v41 row_shr:8 row_mask:0xf bank_mask:0xf
	v_fmac_f32_dpp v62, v62, v42 row_shr:8 row_mask:0xf bank_mask:0xf
	v_fmac_f32_dpp v63, v63, v43 row_shr:8 row_mask:0xf bank_mask:0xf
	v_mul_f32_dpp v40, v40, v40 row_shr:8 row_mask:0xf bank_mask:0xf
	v_mul_f32_dpp v41, v41, v41 row_shr:8 row_mask:0xf bank_mask:0xf
	v_mul_f32_dpp v42, v42, v42 row_shr:8 row_mask:0xf bank_mask:0xf
	v_mul_f32_dpp v43, v43, v43 row_shr:8 row_mask:0xf bank_mask:0xf
	v_fmac_f32_dpp v72, v72, v125 row_shl:8 row_mask:0xf bank_mask:0xf
	v_fmac_f32_dpp v73, v73, v126 row_shl:8 row_mask:0xf bank_mask:0xf
	v_fmac_f32_dpp v74, v74, v127 row_shl:8 row_mask:0xf bank_mask:0xf
	v_fmac_f32_dpp v75, v75, v128 row_shl:8 row_mask:0xf bank_mask:0xf
	v_mul_f32_dpp v125, v125, v125 row_shl:8 row_mask:0xf bank_mask:0xf
	v_mul_f32_dpp v126, v126, v126 row_shl:8 row_mask:0xf bank_mask:0xf
	v_mul_f32_dpp v127, v127, v127 row_shl:8 row_mask:0xf bank_mask:0xf
	v_mul_f32_dpp v128, v128, v128 row_shl:8 row_mask:0xf bank_mask:0xf
	v_fmac_f32_dpp v56, v56, v44 row_shr:8 row_mask:0xf bank_mask:0xf
	v_fmac_f32_dpp v57, v57, v45 row_shr:8 row_mask:0xf bank_mask:0xf
	v_fmac_f32_dpp v58, v58, v46 row_shr:8 row_mask:0xf bank_mask:0xf
	v_fmac_f32_dpp v59, v59, v47 row_shr:8 row_mask:0xf bank_mask:0xf
	v_mul_f32_dpp v44, v44, v44 row_shr:8 row_mask:0xf bank_mask:0xf
	v_mul_f32_dpp v45, v45, v45 row_shr:8 row_mask:0xf bank_mask:0xf
	v_mul_f32_dpp v46, v46, v46 row_shr:8 row_mask:0xf bank_mask:0xf
	v_mul_f32_dpp v47, v47, v47 row_shr:8 row_mask:0xf bank_mask:0xf
	v_fmac_f32_dpp v76, v76, v129 row_shl:8 row_mask:0xf bank_mask:0xf
	v_fmac_f32_dpp v77, v77, v130 row_shl:8 row_mask:0xf bank_mask:0xf
	v_fmac_f32_dpp v78, v78, v131 row_shl:8 row_mask:0xf bank_mask:0xf
	v_fmac_f32_dpp v79, v79, v132 row_shl:8 row_mask:0xf bank_mask:0xf
	v_mul_f32_dpp v129, v129, v129 row_shl:8 row_mask:0xf bank_mask:0xf
	v_mul_f32_dpp v130, v130, v130 row_shl:8 row_mask:0xf bank_mask:0xf
	v_mul_f32_dpp v131, v131, v131 row_shl:8 row_mask:0xf bank_mask:0xf
	v_mul_f32_dpp v132, v132, v132 row_shl:8 row_mask:0xf bank_mask:0xf
	v_fmac_f32_dpp v52, v52, v48 row_shr:8 row_mask:0xf bank_mask:0xf
	v_fmac_f32_dpp v53, v53, v49 row_shr:8 row_mask:0xf bank_mask:0xf
	v_fmac_f32_dpp v54, v54, v50 row_shr:8 row_mask:0xf bank_mask:0xf
	v_fmac_f32_dpp v55, v55, v51 row_shr:8 row_mask:0xf bank_mask:0xf
	v_mul_f32_dpp v48, v48, v48 row_shr:8 row_mask:0xf bank_mask:0xf
	v_mul_f32_dpp v49, v49, v49 row_shr:8 row_mask:0xf bank_mask:0xf
	v_mul_f32_dpp v50, v50, v50 row_shr:8 row_mask:0xf bank_mask:0xf
	v_mul_f32_dpp v51, v51, v51 row_shr:8 row_mask:0xf bank_mask:0xf
	v_fmac_f32_dpp v80, v80, v133 row_shl:8 row_mask:0xf bank_mask:0xf
	v_fmac_f32_dpp v81, v81, v134 row_shl:8 row_mask:0xf bank_mask:0xf
	v_fmac_f32_dpp v82, v82, v135 row_shl:8 row_mask:0xf bank_mask:0xf
	v_fmac_f32_dpp v83, v83, v136 row_shl:8 row_mask:0xf bank_mask:0xf
	v_mul_f32_dpp v133, v133, v133 row_shl:8 row_mask:0xf bank_mask:0xf
	v_mul_f32_dpp v134, v134, v134 row_shl:8 row_mask:0xf bank_mask:0xf
	v_mul_f32_dpp v135, v135, v135 row_shl:8 row_mask:0xf bank_mask:0xf
	v_mul_f32_dpp v136, v136, v136 row_shl:8 row_mask:0xf bank_mask:0xf
	s_and_saveexec_b64 s[20:21], vcc
	s_xor_b64 s[24:25], exec, s[20:21]
	s_cbranch_execz .LBB0_469
	s_mov_b64 s[8:9], exec
	s_or_saveexec_b64 s[24:25], s[24:25]
	v_mov_b32_e32 v84, s26
	s_xor_b64 exec, exec, s[24:25]
	s_cbranch_execnz .LBB0_470

; #define LAS __attribute__((address_space(3)))
; __device__ __forceinline__ float sigmoidf_(float x) { return __builtin_amdgcn_rcpf(1.0f + __expf(-x)); }
; template <int CTRL> __device__ __forceinline__ float dpp_add0(float x) { return x + dppf<CTRL>(0.0f, x); }
; template <bool WITHO, bool RAW = false>
; __device__ __forceinline__ void hg_pass(const Frame& F, const bf16_t* P, const float* lbh, int b, int h, int nb, int dir, f32x4 (&S)[4][4], float (&Gsum)[16],
;                                         LAS bf16_t* Vl, LAS bf16_t* Kl, float* OF, const float* ngp) {
;     ...
; #pragma unroll
;         for (int m = 0; m < 4; ++m) { const float z0 = __uint_as_float(zr[m].x << 16), z1 = __uint_as_float(zr[m].x & 0xffff0000u), z2 = __uint_as_float(zr[m].y << 16), z3 = __uint_as_float(zr[m].y & 0xffff0000u);
;             const float zz[4] = {z0, z1, z2, z3};
;             const f32x4 lb4 = *(const f32x4*)(lbh + 16 * m + 4 * g);
; #pragma unroll
;             for (int i = 0; i < 4; ++i) { const float lb = lb4[i]; const float f = fmaxf(lb + (1.0f - lb) * sigmoidf_(zz[i]), 1e-30f); kk[m * 4 + i] = 1.0f - f; c[m * 4 + i] = __logf(f); }
;             *(LAS u32x2*)(Vl + tau * 64 + 16 * m + 4 * g) = vr[m];
;  }
;         if (ci + 1 < HG_U / 16) { const int pos = (ci + 1) * 16 + tau, t = dir ? (HG_U - 1 - pos) : pos; const bf16_t* pr = P + (size_t)hg_row(b, nb, t) * 4096 + h * 64 + 4 * g;
; #pragma unroll
;             for (int m = 0; m < 4; ++m) { zr[m] = *(const u32x2*)(pr + (dir ? 2560 : 2048) + 16 * m); vr[m] = *(const u32x2*)(pr + 3072 + 16 * m); } }
;         float G[16];
; #pragma unroll
;         for (int q = 0; q < 16; ++q) G[q] = c[q];
; #pragma unroll
;         for (int q = 0; q < 16; q += 4) ROW_ALLREDUCE4(G[q], G[q + 1], G[q + 2], G[q + 3]);
; #pragma unroll
;         for (int q = 0; q < 16; ++q) { c[q] = dpp_add0<0x111>(c[q]); c[q] = dpp_add0<0x112>(c[q]); c[q] = dpp_add0<0x114>(c[q]); c[q] = dpp_add0<0x118>(c[q]); }
; #pragma unroll
;         for (int q = 0; q < 16; ++q) Gsum[q] += G[q];
.LBB0_675:
	v_lshlrev_b32_e32 v3, 16, v90
	v_mul_f32_e32 v3, 0xbfb8aa3b, v3
	v_exp_f32_e32 v3, v3
	s_waitcnt vmcnt(0)
	v_sub_f32_e32 v93, 1.0, v80
	v_and_b32_e32 v90, 0xffff0000, v90
	v_mul_f32_e32 v90, 0xbfb8aa3b, v90
	v_add_f32_e32 v3, 1.0, v3
	v_rcp_f32_e32 v3, v3
	v_exp_f32_e32 v90, v90
	v_lshlrev_b32_e32 v92, 16, v91
	v_lshlrev_b32_e32 v198, 16, v98
	v_fma_f32 v3, v3, v93, v80
	v_max_f32_e32 v3, 0xda24260, v3
	v_and_b32_e32 v93, 0xffff0000, v91
	v_add_f32_e32 v90, 1.0, v90
	v_log_f32_e32 v80, v3
	v_sub_f32_e32 v91, 1.0, v3
	v_rcp_f32_e32 v90, v90
	v_and_b32_e32 v98, 0xffff0000, v98
	v_mul_f32_e32 v3, 0x3f317217, v80
	v_fma_f32 v3, v80, s93, -v3
	v_fmac_f32_e32 v3, 0x3377d1cf, v80
	v_fmac_f32_e32 v3, 0x3f317217, v80
	v_mul_f32_e32 v202, 0xbfb8aa3b, v98
	v_exp_f32_e32 v202, v202
	v_sub_f32_e32 v80, 1.0, v81
	v_fma_f32 v80, v90, v80, v81
	v_max_f32_e32 v80, 0xda24260, v80
	v_mul_f32_e32 v90, 0xbfb8aa3b, v92
	v_log_f32_e32 v81, v80
	v_exp_f32_e32 v90, v90
	v_sub_f32_e32 v102, 1.0, v80
	v_mov_b32_e32 v173, v3
	v_mul_f32_e32 v80, 0x3f317217, v81
	v_add_f32_e32 v90, 1.0, v90
	v_fma_f32 v80, v81, s93, -v80
	v_rcp_f32_e32 v90, v90
	v_fmac_f32_e32 v80, 0x3377d1cf, v81
	v_fmac_f32_e32 v80, 0x3f317217, v81
	v_add_f32_dpp v3, v3, v3 row_shr:1 row_mask:0xf bank_mask:0xf bound_ctrl:1
	v_add_f32_e32 v202, 1.0, v202
	v_sub_f32_e32 v81, 1.0, v82
	v_fma_f32 v81, v90, v81, v82
	v_max_f32_e32 v81, 0xda24260, v81
	v_mul_f32_e32 v90, 0xbfb8aa3b, v93
	v_log_f32_e32 v82, v81
	v_exp_f32_e32 v90, v90
	v_sub_f32_e32 v103, 1.0, v81
	v_add_f32_dpp v3, v3, v3 row_shr:2 row_mask:0xf bank_mask:0xf bound_ctrl:1
	v_mul_f32_e32 v81, 0x3f317217, v82
	v_add_f32_e32 v90, 1.0, v90
	v_fma_f32 v81, v82, s93, -v81
	v_rcp_f32_e32 v90, v90
	v_fmac_f32_e32 v81, 0x3377d1cf, v82
	v_fmac_f32_e32 v81, 0x3f317217, v82
	v_add_f32_dpp v3, v3, v3 row_shr:4 row_mask:0xf bank_mask:0xf bound_ctrl:1
	v_mov_b32_e32 v171, v80
	v_sub_f32_e32 v82, 1.0, v83
	v_fmac_f32_e32 v83, v90, v82
	v_max_f32_e32 v82, 0xda24260, v83
	v_lshlrev_b32_e32 v90, 16, v88
	v_log_f32_e32 v83, v82
	v_mul_f32_e32 v90, 0xbfb8aa3b, v90
	v_exp_f32_e32 v90, v90
	v_sub_f32_e32 v104, 1.0, v82
	v_mul_f32_e32 v82, 0x3f317217, v83
	v_fma_f32 v82, v83, s93, -v82
	v_add_f32_e32 v90, 1.0, v90
	v_fmac_f32_e32 v82, 0x3377d1cf, v83
	v_rcp_f32_e32 v90, v90
	v_fmac_f32_e32 v82, 0x3f317217, v83
	v_add_f32_dpp v182, v3, v3 row_shr:8 row_mask:0xf bank_mask:0xf bound_ctrl:1
	v_add_f32_dpp v3, v80, v80 row_shr:1 row_mask:0xf bank_mask:0xf bound_ctrl:1
	v_and_b32_e32 v83, 0xffff0000, v88
	v_sub_f32_e32 v88, 1.0, v76
	v_fma_f32 v76, v90, v88, v76
	v_max_f32_e32 v76, 0xda24260, v76
	v_mul_f32_e32 v83, 0xbfb8aa3b, v83
	v_exp_f32_e32 v83, v83
	v_log_f32_e32 v88, v76
	v_sub_f32_e32 v105, 1.0, v76
	v_add_f32_e32 v83, 1.0, v83
	v_rcp_f32_e32 v83, v83
	v_mul_f32_e32 v76, 0x3f317217, v88
	v_fma_f32 v76, v88, s93, -v76
	v_fmac_f32_e32 v76, 0x3377d1cf, v88
	v_fmac_f32_e32 v76, 0x3f317217, v88
	v_lshlrev_b32_e32 v90, 16, v89
	v_and_b32_e32 v89, 0xffff0000, v89
	v_sub_f32_e32 v88, 1.0, v77
	v_fma_f32 v77, v83, v88, v77
	v_max_f32_e32 v77, 0xda24260, v77
	v_mul_f32_e32 v88, 0xbfb8aa3b, v90
	v_log_f32_e32 v83, v77
	v_exp_f32_e32 v88, v88
	v_sub_f32_e32 v106, 1.0, v77
	v_lshlrev_b32_e32 v90, 16, v0
	v_mul_f32_e32 v77, 0x3f317217, v83
	v_add_f32_e32 v88, 1.0, v88
	v_fma_f32 v77, v83, s93, -v77
	v_rcp_f32_e32 v88, v88
	v_fmac_f32_e32 v77, 0x3377d1cf, v83
	v_fmac_f32_e32 v77, 0x3f317217, v83
	v_mul_f32_e32 v90, 0xbfb8aa3b, v90
	v_exp_f32_e32 v90, v90
	v_sub_f32_e32 v83, 1.0, v78
	v_fma_f32 v78, v88, v83, v78
	v_max_f32_e32 v78, 0xda24260, v78
	v_mul_f32_e32 v88, 0xbfb8aa3b, v89
	v_log_f32_e32 v83, v78
	v_exp_f32_e32 v88, v88
	v_sub_f32_e32 v107, 1.0, v78
	v_lshlrev_b32_e32 v89, 16, v85
	v_mul_f32_e32 v78, 0x3f317217, v83
	v_add_f32_e32 v88, 1.0, v88
	v_fma_f32 v78, v83, s93, -v78
	v_rcp_f32_e32 v88, v88
	v_fmac_f32_e32 v78, 0x3377d1cf, v83
	v_fmac_f32_e32 v78, 0x3f317217, v83
	v_mul_f32_e32 v89, 0xbfb8aa3b, v89
	v_exp_f32_e32 v89, v89
	v_sub_f32_e32 v83, 1.0, v79
	v_fmac_f32_e32 v79, v88, v83
	v_max_f32_e32 v79, 0xda24260, v79
	v_sub_f32_e32 v108, 1.0, v79
	v_mov_b32_e32 v83, v79
	v_lshlrev_b32_e32 v79, 16, v84
	v_log_f32_e32 v83, v83
	v_mul_f32_e32 v79, 0xbfb8aa3b, v79
	v_exp_f32_e32 v79, v79
	v_mov_b32_e32 v88, v78
	v_mul_f32_e32 v78, 0x3f317217, v83
	v_fma_f32 v78, v83, s93, -v78
	v_add_f32_e32 v79, 1.0, v79
	v_fmac_f32_e32 v78, 0x3377d1cf, v83
	v_rcp_f32_e32 v79, v79
	v_fmac_f32_e32 v78, 0x3f317217, v83
	v_and_b32_e32 v84, 0xffff0000, v84
	v_mul_f32_e32 v84, 0xbfb8aa3b, v84
	v_mov_b32_e32 v83, v78
	v_sub_f32_e32 v78, 1.0, v72
	v_fma_f32 v72, v79, v78, v72
	v_max_f32_e32 v72, 0xda24260, v72
	v_cmp_gt_f32_e32 vcc, s92, v72
	v_exp_f32_e32 v84, v84
	v_add_f32_e32 v89, 1.0, v89
	v_cndmask_b32_e64 v78, 0, 32, vcc
	v_ldexp_f32 v78, v72, v78
	v_log_f32_e32 v79, v78
	v_sub_f32_e32 v78, 1.0, v72
	v_add_f32_e32 v84, 1.0, v84
	v_rcp_f32_e32 v84, v84
	v_mul_f32_e32 v72, 0x3f317217, v79
	v_fma_f32 v72, v79, s93, -v72
	v_fmac_f32_e32 v72, 0x3377d1cf, v79
	v_fmac_f32_e32 v72, 0x3f317217, v79
	v_cmp_lt_f32_e64 s[52:53], |v79|, s90
	v_rcp_f32_e32 v89, v89
	v_and_b32_e32 v85, 0xffff0000, v85
	v_cndmask_b32_e64 v72, v79, v72, s[52:53]
	v_sub_f32_e32 v79, 1.0, v73
	v_fma_f32 v73, v84, v79, v73
	v_max_f32_e32 v73, 0xda24260, v73
	v_cmp_gt_f32_e64 s[52:53], s92, v73
	v_mul_f32_e32 v85, 0xbfb8aa3b, v85
	v_exp_f32_e32 v85, v85
	v_cndmask_b32_e64 v79, 0, 32, s[52:53]
	v_ldexp_f32 v79, v73, v79
	v_log_f32_e32 v84, v79
	v_cndmask_b32_e32 v79, 0, v179, vcc
	v_sub_f32_e32 v72, v72, v79
	v_sub_f32_e32 v79, 1.0, v73
	v_mul_f32_e32 v73, 0x3f317217, v84
	v_fma_f32 v73, v84, s93, -v73
; #define LAS __attribute__((address_space(3)))
; __device__ __forceinline__ float sigmoidf_(float x) { return __builtin_amdgcn_rcpf(1.0f + __expf(-x)); }
; template <int CTRL> __device__ __forceinline__ float dpp_add0(float x) { return x + dppf<CTRL>(0.0f, x); }
; template <bool WITHO, bool RAW = false>
; __device__ __forceinline__ void hg_pass(const Frame& F, const bf16_t* P, const float* lbh, int b, int h, int nb, int dir, f32x4 (&S)[4][4], float (&Gsum)[16],
;                                         LAS bf16_t* Vl, LAS bf16_t* Kl, float* OF, const float* ngp) {
;     ...
; #pragma unroll
;         for (int m = 0; m < 4; ++m) { const float z0 = __uint_as_float(zr[m].x << 16), z1 = __uint_as_float(zr[m].x & 0xffff0000u), z2 = __uint_as_float(zr[m].y << 16), z3 = __uint_as_float(zr[m].y & 0xffff0000u);
;             const float zz[4] = {z0, z1, z2, z3};
;             const f32x4 lb4 = *(const f32x4*)(lbh + 16 * m + 4 * g);
; #pragma unroll
;             for (int i = 0; i < 4; ++i) { const float lb = lb4[i]; const float f = fmaxf(lb + (1.0f - lb) * sigmoidf_(zz[i]), 1e-30f); kk[m * 4 + i] = 1.0f - f; c[m * 4 + i] = __logf(f); }
;             *(LAS u32x2*)(Vl + tau * 64 + 16 * m + 4 * g) = vr[m];
;  }
;         if (ci + 1 < HG_U / 16) { const int pos = (ci + 1) * 16 + tau, t = dir ? (HG_U - 1 - pos) : pos; const bf16_t* pr = P + (size_t)hg_row(b, nb, t) * 4096 + h * 64 + 4 * g;
; #pragma unroll
;             for (int m = 0; m < 4; ++m) { zr[m] = *(const u32x2*)(pr + (dir ? 2560 : 2048) + 16 * m); vr[m] = *(const u32x2*)(pr + 3072 + 16 * m); } }
;         float G[16];
; #pragma unroll
;         for (int q = 0; q < 16; ++q) G[q] = c[q];
; #pragma unroll
;         for (int q = 0; q < 16; q += 4) ROW_ALLREDUCE4(G[q], G[q + 1], G[q + 2], G[q + 3]);
; #pragma unroll
;         for (int q = 0; q < 16; ++q) { c[q] = dpp_add0<0x111>(c[q]); c[q] = dpp_add0<0x112>(c[q]); c[q] = dpp_add0<0x114>(c[q]); c[q] = dpp_add0<0x118>(c[q]); }
; #pragma unroll
;         for (int q = 0; q < 16; ++q) Gsum[q] += G[q];
	v_fmac_f32_e32 v73, 0x3377d1cf, v84
	v_fmac_f32_e32 v73, 0x3f317217, v84
	v_cmp_lt_f32_e64 vcc, |v84|, s90
	v_add_f32_e32 v85, 1.0, v85
	v_rcp_f32_e32 v85, v85
	v_cndmask_b32_e32 v73, v84, v73, vcc
	v_sub_f32_e32 v84, 1.0, v74
	v_fma_f32 v74, v89, v84, v74
	v_max_f32_e32 v74, 0xda24260, v74
	v_cndmask_b32_e64 v89, 0, v179, s[52:53]
	v_sub_f32_e32 v73, v73, v89
	v_log_f32_e32 v84, v74
	v_add_f32_e32 v90, 1.0, v90
	v_rcp_f32_e32 v90, v90
	v_and_b32_e32 v0, 0xffff0000, v0
	v_mul_f32_e32 v89, 0x3f317217, v84
	v_fma_f32 v89, v84, s93, -v89
	v_fmac_f32_e32 v89, 0x3377d1cf, v84
	v_fmac_f32_e32 v89, 0x3f317217, v84
	v_mul_f32_e32 v0, 0xbfb8aa3b, v0
	v_exp_f32_e32 v0, v0
	v_mov_b32_e32 v84, v89
	v_sub_f32_e32 v89, 1.0, v75
	v_fmac_f32_e32 v75, v85, v89
	v_max_f32_e32 v75, 0xda24260, v75
	v_log_f32_e32 v85, v75
	v_add_f32_e32 v0, 1.0, v0
	v_rcp_f32_e32 v0, v0
	v_add_f32_dpp v3, v3, v3 row_shr:2 row_mask:0xf bank_mask:0xf bound_ctrl:1
	v_mul_f32_e32 v89, 0x3f317217, v85
	v_fma_f32 v89, v85, s93, -v89
	v_fmac_f32_e32 v89, 0x3377d1cf, v85
	v_fmac_f32_e32 v89, 0x3f317217, v85
	v_add_f32_dpp v3, v3, v3 row_shr:4 row_mask:0xf bank_mask:0xf bound_ctrl:1
	v_mov_b32_e32 v170, v82
	v_mov_b32_e32 v85, v89
	v_sub_f32_e32 v89, 1.0, v68
	v_fma_f32 v68, v90, v89, v68
	v_max_f32_e32 v68, 0xda24260, v68
	v_sub_f32_e32 v109, 1.0, v68
	v_lshlrev_b32_e32 v90, 16, v1
	v_log_f32_e32 v89, v68
	v_and_b32_e32 v1, 0xffff0000, v1
	v_mul_f32_e32 v1, 0xbfb8aa3b, v1
	v_exp_f32_e32 v1, v1
	v_mul_f32_e32 v68, 0x3f317217, v89
	v_fma_f32 v68, v89, s93, -v68
	v_fmac_f32_e32 v68, 0x3377d1cf, v89
	v_fmac_f32_e32 v68, 0x3f317217, v89
	v_add_f32_e32 v1, 1.0, v1
	v_rcp_f32_e32 v1, v1
	v_sub_f32_e32 v89, 1.0, v69
	v_fma_f32 v0, v0, v89, v69
	v_max_f32_e32 v0, 0xda24260, v0
	v_mul_f32_e32 v89, 0xbfb8aa3b, v90
	v_log_f32_e32 v69, v0
	v_exp_f32_e32 v89, v89
	v_sub_f32_e32 v110, 1.0, v0
	v_add_f32_dpp v183, v3, v3 row_shr:8 row_mask:0xf bank_mask:0xf bound_ctrl:1
	v_mul_f32_e32 v0, 0x3f317217, v69
	v_add_f32_e32 v89, 1.0, v89
	v_fma_f32 v0, v69, s93, -v0
	v_rcp_f32_e32 v89, v89
	v_fmac_f32_e32 v0, 0x3377d1cf, v69
	v_fmac_f32_e32 v0, 0x3f317217, v69
	v_add_f32_dpp v3, v81, v81 row_shr:1 row_mask:0xf bank_mask:0xf bound_ctrl:1
	v_mov_b32_e32 v172, v81
	v_sub_f32_e32 v69, 1.0, v70
	v_fma_f32 v69, v89, v69, v70
	v_max_f32_e32 v69, 0xda24260, v69
	v_cmp_gt_f32_e32 vcc, s92, v69
	v_add_f32_dpp v3, v3, v3 row_shr:2 row_mask:0xf bank_mask:0xf bound_ctrl:1
	s_nop 1
	v_add_f32_dpp v173, v173, v173 quad_perm:[1,0,3,2] row_mask:0xf bank_mask:0xf
	v_add_f32_dpp v171, v171, v171 quad_perm:[1,0,3,2] row_mask:0xf bank_mask:0xf
	v_add_f32_dpp v172, v172, v172 quad_perm:[1,0,3,2] row_mask:0xf bank_mask:0xf
	v_add_f32_dpp v170, v170, v170 quad_perm:[1,0,3,2] row_mask:0xf bank_mask:0xf
	v_add_f32_dpp v173, v173, v173 quad_perm:[2,3,0,1] row_mask:0xf bank_mask:0xf
	v_add_f32_dpp v171, v171, v171 quad_perm:[2,3,0,1] row_mask:0xf bank_mask:0xf
	v_add_f32_dpp v172, v172, v172 quad_perm:[2,3,0,1] row_mask:0xf bank_mask:0xf
	v_add_f32_dpp v170, v170, v170 quad_perm:[2,3,0,1] row_mask:0xf bank_mask:0xf
	v_add_f32_dpp v173, v173, v173 row_half_mirror row_mask:0xf bank_mask:0xf
	v_add_f32_dpp v171, v171, v171 row_half_mirror row_mask:0xf bank_mask:0xf
	v_add_f32_dpp v172, v172, v172 row_half_mirror row_mask:0xf bank_mask:0xf
	v_add_f32_dpp v170, v170, v170 row_half_mirror row_mask:0xf bank_mask:0xf
	v_add_f32_dpp v173, v173, v173 row_mirror row_mask:0xf bank_mask:0xf
	v_add_f32_dpp v171, v171, v171 row_mirror row_mask:0xf bank_mask:0xf
	v_add_f32_dpp v172, v172, v172 row_mirror row_mask:0xf bank_mask:0xf
	v_add_f32_dpp v170, v170, v170 row_mirror row_mask:0xf bank_mask:0xf
	v_rcp_f32_e32 v202, v202
	v_cndmask_b32_e64 v70, 0, 32, vcc
	v_ldexp_f32 v70, v69, v70
	v_log_f32_e32 v89, v70
	v_sub_f32_e32 v70, 1.0, v69
	v_mul_f32_e32 v69, 0x3f317217, v89
	v_fma_f32 v69, v89, s93, -v69
	v_fmac_f32_e32 v69, 0x3377d1cf, v89
	v_fmac_f32_e32 v69, 0x3f317217, v89
	v_cmp_lt_f32_e64 s[52:53], |v89|, s90
	v_add_f32_dpp v3, v3, v3 row_shr:4 row_mask:0xf bank_mask:0xf bound_ctrl:1
	v_mov_b32_e32 v162, v0
	v_cndmask_b32_e64 v69, v89, v69, s[52:53]
	v_sub_f32_e32 v89, 1.0, v71
	v_fmac_f32_e32 v71, v1, v89
	v_max_f32_e32 v1, 0xda24260, v71
	v_cmp_gt_f32_e64 s[52:53], s92, v1
	v_add_f32_dpp v184, v3, v3 row_shr:8 row_mask:0xf bank_mask:0xf bound_ctrl:1
	v_add_f32_dpp v3, v82, v82 row_shr:1 row_mask:0xf bank_mask:0xf bound_ctrl:1
	v_cndmask_b32_e64 v71, 0, 32, s[52:53]
	v_ldexp_f32 v71, v1, v71
	v_log_f32_e32 v89, v71
	v_add_f32_dpp v3, v3, v3 row_shr:2 row_mask:0xf bank_mask:0xf bound_ctrl:1
	v_mul_f32_e32 v82, 0xbfb8aa3b, v198
	v_exp_f32_e32 v199, v82
	v_add_f32_dpp v3, v3, v3 row_shr:4 row_mask:0xf bank_mask:0xf bound_ctrl:1
	v_cndmask_b32_e32 v71, 0, v179, vcc
	v_sub_f32_e32 v69, v69, v71
	v_add_f32_dpp v185, v3, v3 row_shr:8 row_mask:0xf bank_mask:0xf bound_ctrl:1
	v_add_f32_dpp v3, v76, v76 row_shr:1 row_mask:0xf bank_mask:0xf bound_ctrl:1
	v_sub_f32_e32 v71, 1.0, v1
	v_mul_f32_e32 v1, 0x3f317217, v89
	v_add_f32_dpp v3, v3, v3 row_shr:2 row_mask:0xf bank_mask:0xf bound_ctrl:1
	v_add_f32_dpp v0, v0, v0 row_shr:1 row_mask:0xf bank_mask:0xf bound_ctrl:1
	v_fma_f32 v1, v89, s93, -v1
	v_add_f32_dpp v3, v3, v3 row_shr:4 row_mask:0xf bank_mask:0xf bound_ctrl:1
	v_add_f32_dpp v0, v0, v0 row_shr:2 row_mask:0xf bank_mask:0xf bound_ctrl:1
	v_fmac_f32_e32 v1, 0x3377d1cf, v89
	v_add_f32_dpp v190, v3, v3 row_shr:8 row_mask:0xf bank_mask:0xf bound_ctrl:1
	v_add_f32_dpp v3, v77, v77 row_shr:1 row_mask:0xf bank_mask:0xf bound_ctrl:1
	v_add_f32_dpp v0, v0, v0 row_shr:4 row_mask:0xf bank_mask:0xf bound_ctrl:1
	v_add_f32_e32 v199, 1.0, v199
; template <bool WITHO, bool RAW = false>
; __device__ __forceinline__ void hg_pass(const Frame& F, const bf16_t* P, const float* lbh, int b, int h, int nb, int dir, f32x4 (&S)[4][4], float (&Gsum)[16],
;                                         LAS bf16_t* Vl, LAS bf16_t* Kl, float* OF, const float* ngp) {
;     ...
;         for (int q = 0; q < 16; ++q) { c[q] = dpp_add0<0x111>(c[q]); c[q] = dpp_add0<0x112>(c[q]); c[q] = dpp_add0<0x114>(c[q]); c[q] = dpp_add0<0x118>(c[q]); }
; #pragma unroll
;         for (int q = 0; q < 16; ++q) Gsum[q] += G[q];
; #pragma unroll
;         for (int m = 0; m < 4; ++m) { float kh[4];
; #pragma unroll
;             for (int i = 0; i < 4; ++i) kh[i] = kk[m * 4 + i] * __expf(G[m * 4 + i] - c[m * 4 + i]);
;             u32x2 w; w.x = cvt_pk_bf16(kh[0], kh[1]); w.y = cvt_pk_bf16(kh[2], kh[3]);
;             *(LAS u32x2*)(Kl + tau * 64 + 16 * m + 4 * g) = w; }
;         float ofv[4][4], gtv[4][4]; int orow[4];
;         if (WITHO) {
; #pragma unroll
;             for (int i = 0; i < 4; ++i) { const int p2 = ci * 16 + 4 * g + i, t2 = dir ? (HG_U - 1 - p2) : p2; orow[i] = hg_row(b, nb, t2); }
;             if (dir && !RAW) {
; #pragma unroll
;                 for (int i = 0; i < 4; ++i)
; #pragma unroll
;                     for (int vt = 0; vt < 4; ++vt) { ofv[i][vt] = OF[(size_t)orow[i] * 512 + h * 64 + 16 * vt + tau]; gtv[i][vt] = bf2f(P[(size_t)orow[i] * 4096 + 3584 + h * 64 + 16 * vt + tau]); }
;             }
;         }
;         asm volatile("s_waitcnt lgkmcnt(0)" ::: "memory");
;         u32x2 vtr[4], ktr[4];
;         asm volatile("ds_read_b64_tr_b16 %0, %8\n\tds_read_b64_tr_b16 %1, %8 offset:32\n\tds_read_b64_tr_b16 %2, %8 offset:64\n\tds_read_b64_tr_b16 %3, %8 offset:96\n\t"
;                      "ds_read_b64_tr_b16 %4, %9\n\tds_read_b64_tr_b16 %5, %9 offset:32\n\tds_read_b64_tr_b16 %6, %9 offset:64\n\tds_read_b64_tr_b16 %7, %9 offset:96\n\ts_waitcnt lgkmcnt(0)"
;                      : "=&v"(vtr[0]), "=&v"(vtr[1]), "=&v"(vtr[2]), "=&v"(vtr[3]), "=&v"(ktr[0]), "=&v"(ktr[1]), "=&v"(ktr[2]), "=&v"(ktr[3]) : "v"(vaddr), "v"(kaddr) : "memory");
;         bf16x8 Vf[4], Kf[4];
; #pragma unroll
;         for (int q = 0; q < 4; ++q) { u32x4 w; w.x = vtr[q].x; w.y = vtr[q].y; w.z = 0u; w.w = 0u; __builtin_memcpy(&Vf[q], &w, 16); u32x4 w2; w2.x = ktr[q].x; w2.y = ktr[q].y; w2.z = 0u; w2.w = 0u; __builtin_memcpy(&Kf[q], &w2, 16); }
	v_add_f32_dpp v3, v3, v3 row_shr:2 row_mask:0xf bank_mask:0xf bound_ctrl:1
	v_fmac_f32_e32 v1, 0x3f317217, v89
	v_cmp_lt_f32_e64 vcc, |v89|, s90
	v_add_f32_dpp v3, v3, v3 row_shr:4 row_mask:0xf bank_mask:0xf bound_ctrl:1
	v_add_f32_dpp v151, v0, v0 row_shr:8 row_mask:0xf bank_mask:0xf bound_ctrl:1
	v_add_f32_dpp v0, v69, v69 row_shr:1 row_mask:0xf bank_mask:0xf bound_ctrl:1
	v_rcp_f32_e32 v199, v199
	v_cndmask_b32_e32 v1, v89, v1, vcc
	v_cndmask_b32_e64 v89, 0, v179, s[52:53]
	v_add_f32_dpp v191, v3, v3 row_shr:8 row_mask:0xf bank_mask:0xf bound_ctrl:1
	v_add_f32_dpp v3, v88, v88 row_shr:1 row_mask:0xf bank_mask:0xf bound_ctrl:1
	v_add_f32_dpp v0, v0, v0 row_shr:2 row_mask:0xf bank_mask:0xf bound_ctrl:1
	v_sub_f32_e32 v1, v1, v89
	v_add_f32_dpp v3, v3, v3 row_shr:2 row_mask:0xf bank_mask:0xf bound_ctrl:1
	v_add_f32_dpp v0, v0, v0 row_shr:4 row_mask:0xf bank_mask:0xf bound_ctrl:1
	v_mul_f32_e32 v198, v199, v198
	v_add_f32_dpp v3, v3, v3 row_shr:4 row_mask:0xf bank_mask:0xf bound_ctrl:1
	v_add_f32_dpp v149, v0, v0 row_shr:8 row_mask:0xf bank_mask:0xf bound_ctrl:1
	v_add_f32_dpp v0, v1, v1 row_shr:1 row_mask:0xf bank_mask:0xf bound_ctrl:1
	v_add_f32_dpp v192, v3, v3 row_shr:8 row_mask:0xf bank_mask:0xf bound_ctrl:1
	v_add_f32_dpp v3, v83, v83 row_shr:1 row_mask:0xf bank_mask:0xf bound_ctrl:1
	v_add_f32_dpp v0, v0, v0 row_shr:2 row_mask:0xf bank_mask:0xf bound_ctrl:1
	v_fma_f32 v199, -0.5, v173, v182
	v_add_f32_dpp v3, v3, v3 row_shr:2 row_mask:0xf bank_mask:0xf bound_ctrl:1
	v_add_f32_dpp v0, v0, v0 row_shr:4 row_mask:0xf bank_mask:0xf bound_ctrl:1
	v_med3_f32 v199, v199, s94, v180
	v_add_f32_dpp v3, v3, v3 row_shr:4 row_mask:0xf bank_mask:0xf bound_ctrl:1
	v_add_f32_dpp v111, v0, v0 row_shr:8 row_mask:0xf bank_mask:0xf bound_ctrl:1
	v_sub_f32_e32 v0, v173, v182
	v_mul_f32_e32 v201, 0x3fb8aa3b, v199
	v_mul_f32_e32 v182, 0x3fb8aa3b, v182
	v_add_f32_dpp v193, v3, v3 row_shr:8 row_mask:0xf bank_mask:0xf bound_ctrl:1
	v_add_f32_dpp v3, v72, v72 row_shr:1 row_mask:0xf bank_mask:0xf bound_ctrl:1
	v_lshlrev_b32_e32 v200, 16, v99
	v_exp_f32_e32 v201, v201
	v_exp_f32_e32 v182, v182
	v_add_f32_dpp v3, v3, v3 row_shr:2 row_mask:0xf bank_mask:0xf bound_ctrl:1
	v_mul_f32_e32 v0, 0x3fb8aa3b, v0
	v_mul_f32_e32 v199, 0xbfb8aa3b, v199
	v_mul_f32_e32 v98, v202, v98
	v_mul_f32_e32 v202, 0xbfb8aa3b, v200
	v_add_f32_dpp v3, v3, v3 row_shr:4 row_mask:0xf bank_mask:0xf bound_ctrl:1
	v_exp_f32_e32 v0, v0
	v_exp_f32_e32 v199, v199
	v_exp_f32_e32 v202, v202
	v_add_f32_dpp v194, v3, v3 row_shr:8 row_mask:0xf bank_mask:0xf bound_ctrl:1
	v_add_f32_dpp v3, v73, v73 row_shr:1 row_mask:0xf bank_mask:0xf bound_ctrl:1
	v_mul_f32_e32 v198, 0x3e000000, v198
	v_mul_f32_e32 v201, v198, v201
	v_add_f32_dpp v3, v3, v3 row_shr:2 row_mask:0xf bank_mask:0xf bound_ctrl:1
	v_mul_f32_e32 v182, v198, v182
	v_fma_f32 v198, -0.5, v171, v183
	v_add_f32_dpp v3, v3, v3 row_shr:4 row_mask:0xf bank_mask:0xf bound_ctrl:1
	v_med3_f32 v198, v198, s94, v180
	v_mov_b32_e32 v159, v1
	v_add_f32_dpp v195, v3, v3 row_shr:8 row_mask:0xf bank_mask:0xf bound_ctrl:1
	v_add_f32_dpp v3, v84, v84 row_shr:1 row_mask:0xf bank_mask:0xf bound_ctrl:1
	v_sub_f32_e32 v1, v171, v183
	v_mul_f32_e32 v0, v91, v0
	v_mul_f32_e32 v91, v91, v199
	v_mul_f32_e32 v199, 0x3fb8aa3b, v198
	v_mul_f32_e32 v183, 0x3fb8aa3b, v183
	v_add_f32_e32 v202, 1.0, v202
	v_add_f32_dpp v3, v3, v3 row_shr:2 row_mask:0xf bank_mask:0xf bound_ctrl:1
	v_exp_f32_e32 v199, v199
	v_exp_f32_e32 v183, v183
	v_rcp_f32_e32 v202, v202
	v_add_f32_dpp v3, v3, v3 row_shr:4 row_mask:0xf bank_mask:0xf bound_ctrl:1
	v_mul_f32_e32 v1, 0x3fb8aa3b, v1
	v_mul_f32_e32 v198, 0xbfb8aa3b, v198
	v_add_f32_dpp v196, v3, v3 row_shr:8 row_mask:0xf bank_mask:0xf bound_ctrl:1
	v_add_f32_dpp v3, v85, v85 row_shr:1 row_mask:0xf bank_mask:0xf bound_ctrl:1
	v_exp_f32_e32 v1, v1
	v_exp_f32_e32 v198, v198
	v_add_f32_dpp v3, v3, v3 row_shr:2 row_mask:0xf bank_mask:0xf bound_ctrl:1
	v_and_b32_e32 v99, 0xffff0000, v99
	v_mul_f32_e32 v98, 0x3e000000, v98
	v_add_f32_dpp v3, v3, v3 row_shr:4 row_mask:0xf bank_mask:0xf bound_ctrl:1
	v_mul_f32_e32 v199, v98, v199
	v_mul_f32_e32 v98, v98, v183
	v_mul_f32_e32 v183, v202, v200
	v_mul_f32_e32 v202, 0xbfb8aa3b, v99
	v_add_f32_dpp v197, v3, v3 row_shr:8 row_mask:0xf bank_mask:0xf bound_ctrl:1
	v_add_f32_dpp v3, v68, v68 row_shr:1 row_mask:0xf bank_mask:0xf bound_ctrl:1
	v_exp_f32_e32 v202, v202
	v_mul_f32_e32 v1, v102, v1
	v_add_f32_dpp v3, v3, v3 row_shr:2 row_mask:0xf bank_mask:0xf bound_ctrl:1
	v_mul_f32_e32 v102, v102, v198
	v_fma_f32 v198, -0.5, v172, v184
	v_add_f32_dpp v3, v3, v3 row_shr:4 row_mask:0xf bank_mask:0xf bound_ctrl:1
	v_med3_f32 v198, v198, s94, v180
	v_mul_f32_e32 v200, 0x3fb8aa3b, v198
	v_add_f32_dpp v153, v3, v3 row_shr:8 row_mask:0xf bank_mask:0xf bound_ctrl:1
	v_sub_f32_e32 v3, v172, v184
	v_mul_f32_e32 v184, 0x3fb8aa3b, v184
	v_exp_f32_e32 v200, v200
	v_exp_f32_e32 v184, v184
	v_add_f32_e32 v202, 1.0, v202
	v_mul_f32_e32 v3, 0x3fb8aa3b, v3
	v_mul_f32_e32 v198, 0xbfb8aa3b, v198
	v_rcp_f32_e32 v202, v202
	v_exp_f32_e32 v3, v3
	v_exp_f32_e32 v198, v198
	v_mul_f32_e32 v183, 0x3e000000, v183
	v_mul_f32_e32 v200, v183, v200
	v_mul_f32_e32 v183, v183, v184
	v_fma_f32 v184, -0.5, v170, v185
	v_mov_b32_e32 v161, v68
	v_sub_f32_e32 v68, v170, v185
	v_mul_f32_e32 v99, v202, v99
	v_med3_f32 v184, v184, s94, v180
	v_lshlrev_b32_e32 v202, 16, v96
	v_mul_f32_e32 v68, 0x3fb8aa3b, v68
	v_mul_f32_e32 v3, v103, v3
	v_mul_f32_e32 v103, v103, v198
	v_mul_f32_e32 v198, 0x3fb8aa3b, v184
	v_mul_f32_e32 v184, 0xbfb8aa3b, v184
	v_mul_f32_e32 v203, 0xbfb8aa3b, v202
	v_exp_f32_e32 v68, v68
	v_exp_f32_e32 v184, v184
	v_exp_f32_e32 v203, v203
; #define LAS __attribute__((address_space(3)))
; template <bool WITHO, bool RAW = false>
; __device__ __forceinline__ void hg_pass(const Frame& F, const bf16_t* P, const float* lbh, int b, int h, int nb, int dir, f32x4 (&S)[4][4], float (&Gsum)[16],
;                                         LAS bf16_t* Vl, LAS bf16_t* Kl, float* OF, const float* ngp) {
;     ...
;         for (int q = 0; q < 16; q += 4) ROW_ALLREDUCE4(G[q], G[q + 1], G[q + 2], G[q + 3]);
; #pragma unroll
;         for (int q = 0; q < 16; ++q) { c[q] = dpp_add0<0x111>(c[q]); c[q] = dpp_add0<0x112>(c[q]); c[q] = dpp_add0<0x114>(c[q]); c[q] = dpp_add0<0x118>(c[q]); }
; #pragma unroll
;         for (int q = 0; q < 16; ++q) Gsum[q] += G[q];
; #pragma unroll
;         for (int m = 0; m < 4; ++m) { float kh[4];
; #pragma unroll
;             for (int i = 0; i < 4; ++i) kh[i] = kk[m * 4 + i] * __expf(G[m * 4 + i] - c[m * 4 + i]);
;             u32x2 w; w.x = cvt_pk_bf16(kh[0], kh[1]); w.y = cvt_pk_bf16(kh[2], kh[3]);
;             *(LAS u32x2*)(Kl + tau * 64 + 16 * m + 4 * g) = w; }
;         float ofv[4][4], gtv[4][4]; int orow[4];
;         if (WITHO) {
; #pragma unroll
;             for (int i = 0; i < 4; ++i) { const int p2 = ci * 16 + 4 * g + i, t2 = dir ? (HG_U - 1 - p2) : p2; orow[i] = hg_row(b, nb, t2); }
;             if (dir && !RAW) {
; #pragma unroll
;                 for (int i = 0; i < 4; ++i)
; #pragma unroll
;                     for (int vt = 0; vt < 4; ++vt) { ofv[i][vt] = OF[(size_t)orow[i] * 512 + h * 64 + 16 * vt + tau]; gtv[i][vt] = bf2f(P[(size_t)orow[i] * 4096 + 3584 + h * 64 + 16 * vt + tau]); }
;             }
;         }
;         asm volatile("s_waitcnt lgkmcnt(0)" ::: "memory");
;         u32x2 vtr[4], ktr[4];
;         asm volatile("ds_read_b64_tr_b16 %0, %8\n\tds_read_b64_tr_b16 %1, %8 offset:32\n\tds_read_b64_tr_b16 %2, %8 offset:64\n\tds_read_b64_tr_b16 %3, %8 offset:96\n\t"
;                      "ds_read_b64_tr_b16 %4, %9\n\tds_read_b64_tr_b16 %5, %9 offset:32\n\tds_read_b64_tr_b16 %6, %9 offset:64\n\tds_read_b64_tr_b16 %7, %9 offset:96\n\ts_waitcnt lgkmcnt(0)"
;                      : "=&v"(vtr[0]), "=&v"(vtr[1]), "=&v"(vtr[2]), "=&v"(vtr[3]), "=&v"(ktr[0]), "=&v"(ktr[1]), "=&v"(ktr[2]), "=&v"(ktr[3]) : "v"(vaddr), "v"(kaddr) : "memory");
;         bf16x8 Vf[4], Kf[4];
; #pragma unroll
	v_and_b32_e32 v96, 0xffff0000, v96
	v_mul_f32_e32 v68, v104, v68
	v_mul_f32_e32 v104, v104, v184
	v_add_f32_e32 v184, 1.0, v203
	v_mul_f32_e32 v204, 0xbfb8aa3b, v96
	v_mov_b32_e32 v168, v76
	v_mov_b32_e32 v147, v88
	v_mov_b32_e32 v169, v77
	v_mov_b32_e32 v167, v83
	v_mov_b32_e32 v164, v73
	v_mov_b32_e32 v163, v85
	v_mov_b32_e32 v166, v72
	v_mov_b32_e32 v165, v84
	v_mov_b32_e32 v160, v69
	v_rcp_f32_e32 v184, v184
	v_exp_f32_e32 v204, v204
	s_nop 1
	v_add_f32_dpp v168, v168, v168 quad_perm:[1,0,3,2] row_mask:0xf bank_mask:0xf
	v_add_f32_dpp v169, v169, v169 quad_perm:[1,0,3,2] row_mask:0xf bank_mask:0xf
	v_add_f32_dpp v147, v147, v147 quad_perm:[1,0,3,2] row_mask:0xf bank_mask:0xf
	v_add_f32_dpp v167, v167, v167 quad_perm:[1,0,3,2] row_mask:0xf bank_mask:0xf
	v_add_f32_dpp v168, v168, v168 quad_perm:[2,3,0,1] row_mask:0xf bank_mask:0xf
	v_add_f32_dpp v169, v169, v169 quad_perm:[2,3,0,1] row_mask:0xf bank_mask:0xf
	v_add_f32_dpp v147, v147, v147 quad_perm:[2,3,0,1] row_mask:0xf bank_mask:0xf
	v_add_f32_dpp v167, v167, v167 quad_perm:[2,3,0,1] row_mask:0xf bank_mask:0xf
	v_add_f32_dpp v168, v168, v168 row_half_mirror row_mask:0xf bank_mask:0xf
	v_add_f32_dpp v169, v169, v169 row_half_mirror row_mask:0xf bank_mask:0xf
	v_add_f32_dpp v147, v147, v147 row_half_mirror row_mask:0xf bank_mask:0xf
	v_add_f32_dpp v167, v167, v167 row_half_mirror row_mask:0xf bank_mask:0xf
	v_add_f32_dpp v168, v168, v168 row_mirror row_mask:0xf bank_mask:0xf
	v_add_f32_dpp v169, v169, v169 row_mirror row_mask:0xf bank_mask:0xf
	v_add_f32_dpp v147, v147, v147 row_mirror row_mask:0xf bank_mask:0xf
	v_add_f32_dpp v167, v167, v167 row_mirror row_mask:0xf bank_mask:0xf
	s_nop 1
	v_add_f32_dpp v166, v166, v166 quad_perm:[1,0,3,2] row_mask:0xf bank_mask:0xf
	v_add_f32_dpp v164, v164, v164 quad_perm:[1,0,3,2] row_mask:0xf bank_mask:0xf
	v_add_f32_dpp v165, v165, v165 quad_perm:[1,0,3,2] row_mask:0xf bank_mask:0xf
	v_add_f32_dpp v163, v163, v163 quad_perm:[1,0,3,2] row_mask:0xf bank_mask:0xf
	v_add_f32_dpp v166, v166, v166 quad_perm:[2,3,0,1] row_mask:0xf bank_mask:0xf
	v_add_f32_dpp v164, v164, v164 quad_perm:[2,3,0,1] row_mask:0xf bank_mask:0xf
	v_add_f32_dpp v165, v165, v165 quad_perm:[2,3,0,1] row_mask:0xf bank_mask:0xf
	v_add_f32_dpp v163, v163, v163 quad_perm:[2,3,0,1] row_mask:0xf bank_mask:0xf
	v_add_f32_dpp v166, v166, v166 row_half_mirror row_mask:0xf bank_mask:0xf
	v_add_f32_dpp v164, v164, v164 row_half_mirror row_mask:0xf bank_mask:0xf
	v_add_f32_dpp v165, v165, v165 row_half_mirror row_mask:0xf bank_mask:0xf
	v_add_f32_dpp v163, v163, v163 row_half_mirror row_mask:0xf bank_mask:0xf
	v_add_f32_dpp v166, v166, v166 row_mirror row_mask:0xf bank_mask:0xf
	v_add_f32_dpp v164, v164, v164 row_mirror row_mask:0xf bank_mask:0xf
	v_add_f32_dpp v165, v165, v165 row_mirror row_mask:0xf bank_mask:0xf
	v_add_f32_dpp v163, v163, v163 row_mirror row_mask:0xf bank_mask:0xf
	s_nop 1
	v_add_f32_dpp v161, v161, v161 quad_perm:[1,0,3,2] row_mask:0xf bank_mask:0xf
	v_add_f32_dpp v162, v162, v162 quad_perm:[1,0,3,2] row_mask:0xf bank_mask:0xf
	v_add_f32_dpp v160, v160, v160 quad_perm:[1,0,3,2] row_mask:0xf bank_mask:0xf
	v_add_f32_dpp v159, v159, v159 quad_perm:[1,0,3,2] row_mask:0xf bank_mask:0xf
	v_add_f32_dpp v161, v161, v161 quad_perm:[2,3,0,1] row_mask:0xf bank_mask:0xf
	v_add_f32_dpp v162, v162, v162 quad_perm:[2,3,0,1] row_mask:0xf bank_mask:0xf
	v_add_f32_dpp v160, v160, v160 quad_perm:[2,3,0,1] row_mask:0xf bank_mask:0xf
	v_add_f32_dpp v159, v159, v159 quad_perm:[2,3,0,1] row_mask:0xf bank_mask:0xf
	v_add_f32_dpp v161, v161, v161 row_half_mirror row_mask:0xf bank_mask:0xf
	v_add_f32_dpp v162, v162, v162 row_half_mirror row_mask:0xf bank_mask:0xf
	v_add_f32_dpp v160, v160, v160 row_half_mirror row_mask:0xf bank_mask:0xf
	v_add_f32_dpp v159, v159, v159 row_half_mirror row_mask:0xf bank_mask:0xf
	v_add_f32_dpp v161, v161, v161 row_mirror row_mask:0xf bank_mask:0xf
	v_add_f32_dpp v162, v162, v162 row_mirror row_mask:0xf bank_mask:0xf
	v_add_f32_dpp v160, v160, v160 row_mirror row_mask:0xf bank_mask:0xf
	v_add_f32_dpp v159, v159, v159 row_mirror row_mask:0xf bank_mask:0xf
	v_cvt_pk_bf16_f32 v0, v0, v1
	v_cvt_pk_bf16_f32 v1, v3, v68
	ds_write_b64 v117, v[0:1] offset:34816
	v_sub_f32_e32 v0, v168, v190
	v_sub_f32_e32 v1, v169, v191
	v_mul_f32_e32 v0, 0x3fb8aa3b, v0
	v_mul_f32_e32 v1, 0x3fb8aa3b, v1
	v_sub_f32_e32 v3, v147, v192
	v_sub_f32_e32 v68, v167, v193
	v_mul_f32_e32 v185, 0x3fb8aa3b, v185
	v_exp_f32_e32 v0, v0
	v_exp_f32_e32 v1, v1
	v_mul_f32_e32 v3, 0x3fb8aa3b, v3
	v_mul_f32_e32 v68, 0x3fb8aa3b, v68
	v_exp_f32_e32 v198, v198
	v_exp_f32_e32 v185, v185
	v_mul_f32_e32 v184, v184, v202
	v_fma_f32 v202, -0.5, v168, v190
	v_add_f32_e32 v204, 1.0, v204
	v_exp_f32_e32 v3, v3
	v_exp_f32_e32 v68, v68
	v_med3_f32 v202, v202, s94, v180
	v_rcp_f32_e32 v204, v204
	v_mul_f32_e32 v203, 0x3fb8aa3b, v202
	v_mul_f32_e32 v190, 0x3fb8aa3b, v190
	v_mul_f32_e32 v99, 0x3e000000, v99
	v_exp_f32_e32 v203, v203
	v_exp_f32_e32 v190, v190
	v_mul_f32_e32 v0, v105, v0
	v_mul_f32_e32 v1, v106, v1
	v_mul_f32_e32 v198, v99, v198
	v_mul_f32_e32 v99, v99, v185
	v_lshlrev_b32_e32 v185, 16, v97
	v_mul_f32_e32 v3, v107, v3
	v_mul_f32_e32 v68, v108, v68
	v_cvt_pk_bf16_f32 v0, v0, v1
	v_cvt_pk_bf16_f32 v1, v3, v68
	v_mul_f32_e32 v202, 0xbfb8aa3b, v202
	v_mul_f32_e32 v96, v204, v96
	v_mul_f32_e32 v204, 0xbfb8aa3b, v185
	ds_write_b64 v117, v[0:1] offset:34848
	v_sub_f32_e32 v0, v166, v194
	v_sub_f32_e32 v1, v164, v195
	v_mul_f32_e32 v184, 0x3e000000, v184
	v_exp_f32_e32 v202, v202
	v_exp_f32_e32 v204, v204
	v_mul_f32_e32 v0, 0x3fb8aa3b, v0
	v_mul_f32_e32 v1, 0x3fb8aa3b, v1
	v_sub_f32_e32 v3, v165, v196
; template <bool WITHO, bool RAW = false>
; __device__ __forceinline__ void hg_pass(const Frame& F, const bf16_t* P, const float* lbh, int b, int h, int nb, int dir, f32x4 (&S)[4][4], float (&Gsum)[16],
;                                         LAS bf16_t* Vl, LAS bf16_t* Kl, float* OF, const float* ngp) {
;     ...
;         for (int m = 0; m < 4; ++m) { float kh[4];
; #pragma unroll
;             for (int i = 0; i < 4; ++i) kh[i] = kk[m * 4 + i] * __expf(G[m * 4 + i] - c[m * 4 + i]);
;             u32x2 w; w.x = cvt_pk_bf16(kh[0], kh[1]); w.y = cvt_pk_bf16(kh[2], kh[3]);
;             *(LAS u32x2*)(Kl + tau * 64 + 16 * m + 4 * g) = w; }
;         float ofv[4][4], gtv[4][4]; int orow[4];
;         if (WITHO) {
; #pragma unroll
;             for (int i = 0; i < 4; ++i) { const int p2 = ci * 16 + 4 * g + i, t2 = dir ? (HG_U - 1 - p2) : p2; orow[i] = hg_row(b, nb, t2); }
;             if (dir && !RAW) {
; #pragma unroll
;                 for (int i = 0; i < 4; ++i)
; #pragma unroll
;                     for (int vt = 0; vt < 4; ++vt) { ofv[i][vt] = OF[(size_t)orow[i] * 512 + h * 64 + 16 * vt + tau]; gtv[i][vt] = bf2f(P[(size_t)orow[i] * 4096 + 3584 + h * 64 + 16 * vt + tau]); }
;             }
;         }
;         asm volatile("s_waitcnt lgkmcnt(0)" ::: "memory");
;         u32x2 vtr[4], ktr[4];
;         asm volatile("ds_read_b64_tr_b16 %0, %8\n\tds_read_b64_tr_b16 %1, %8 offset:32\n\tds_read_b64_tr_b16 %2, %8 offset:64\n\tds_read_b64_tr_b16 %3, %8 offset:96\n\t"
;                      "ds_read_b64_tr_b16 %4, %9\n\tds_read_b64_tr_b16 %5, %9 offset:32\n\tds_read_b64_tr_b16 %6, %9 offset:64\n\tds_read_b64_tr_b16 %7, %9 offset:96\n\ts_waitcnt lgkmcnt(0)"
;                      : "=&v"(vtr[0]), "=&v"(vtr[1]), "=&v"(vtr[2]), "=&v"(vtr[3]), "=&v"(ktr[0]), "=&v"(ktr[1]), "=&v"(ktr[2]), "=&v"(ktr[3]) : "v"(vaddr), "v"(kaddr) : "memory");
;         bf16x8 Vf[4], Kf[4];
; #pragma unroll
;         for (int q = 0; q < 4; ++q) { u32x4 w; w.x = vtr[q].x; w.y = vtr[q].y; w.z = 0u; w.w = 0u; __builtin_memcpy(&Vf[q], &w, 16); u32x4 w2; w2.x = ktr[q].x; w2.y = ktr[q].y; w2.z = 0u; w2.w = 0u; __builtin_memcpy(&Kf[q], &w2, 16); }
;         if (WITHO) {
;             bf16x8 Ktf[2], Qtf[2], Qhf[2];
; #pragma unroll
;             for (int ks = 0; ks < 2; ++ks) { float kt_[8], qt_[8], qh_[8];
; #pragma unroll
;                 for (int mm = 0; mm < 2; ++mm) { const int m = 2 * ks + mm;
	v_sub_f32_e32 v68, v163, v197
	v_mul_f32_e32 v203, v184, v203
	v_mul_f32_e32 v184, v184, v190
	v_fma_f32 v190, -0.5, v169, v191
	v_mul_f32_e32 v191, 0x3fb8aa3b, v191
	v_exp_f32_e32 v0, v0
	v_exp_f32_e32 v1, v1
	v_mul_f32_e32 v3, 0x3fb8aa3b, v3
	v_mul_f32_e32 v68, 0x3fb8aa3b, v68
	v_exp_f32_e32 v191, v191
	v_exp_f32_e32 v3, v3
	v_exp_f32_e32 v68, v68
	v_med3_f32 v190, v190, s94, v180
	v_mul_f32_e32 v105, v105, v202
	v_mul_f32_e32 v202, 0x3fb8aa3b, v190
	v_add_f32_e32 v204, 1.0, v204
	v_and_b32_e32 v97, 0xffff0000, v97
	v_mul_f32_e32 v96, 0x3e000000, v96
	v_exp_f32_e32 v202, v202
	v_rcp_f32_e32 v204, v204
	v_sub_f32_e32 v74, 1.0, v74
	v_sub_f32_e32 v75, 1.0, v75
	v_mul_f32_e32 v0, v78, v0
	v_mul_f32_e32 v1, v79, v1
	v_mul_f32_e32 v190, 0xbfb8aa3b, v190
	v_mul_f32_e32 v205, v96, v191
	v_mul_f32_e32 v191, 0xbfb8aa3b, v97
	v_mul_f32_e32 v3, v74, v3
	v_mul_f32_e32 v68, v75, v68
	v_cvt_pk_bf16_f32 v0, v0, v1
	v_cvt_pk_bf16_f32 v1, v3, v68
	v_exp_f32_e32 v190, v190
	v_exp_f32_e32 v191, v191
	ds_write_b64 v117, v[0:1] offset:34880
	v_sub_f32_e32 v0, v161, v153
	v_sub_f32_e32 v1, v162, v151
	v_mul_f32_e32 v0, 0x3fb8aa3b, v0
	v_mul_f32_e32 v1, 0x3fb8aa3b, v1
	v_sub_f32_e32 v3, v160, v149
	v_sub_f32_e32 v68, v159, v111
	v_mul_f32_e32 v202, v96, v202
	v_mul_f32_e32 v96, v204, v185
	v_fma_f32 v185, -0.5, v147, v192
	v_exp_f32_e32 v0, v0
	v_exp_f32_e32 v1, v1
	v_mul_f32_e32 v3, 0x3fb8aa3b, v3
	v_mul_f32_e32 v68, 0x3fb8aa3b, v68
	v_med3_f32 v185, v185, s94, v180
	v_exp_f32_e32 v3, v3
	v_exp_f32_e32 v68, v68
	v_mul_f32_e32 v106, v106, v190
	v_mul_f32_e32 v190, 0x3fb8aa3b, v185
	v_mul_f32_e32 v185, 0xbfb8aa3b, v185
	v_mul_f32_e32 v192, 0x3fb8aa3b, v192
	v_add_f32_e32 v191, 1.0, v191
	v_exp_f32_e32 v190, v190
	v_exp_f32_e32 v185, v185
	v_exp_f32_e32 v192, v192
	v_rcp_f32_e32 v191, v191
	v_mul_f32_e32 v0, v109, v0
	v_mul_f32_e32 v1, v110, v1
	v_mul_f32_e32 v3, v70, v3
	v_mul_f32_e32 v68, v71, v68
	v_cvt_pk_bf16_f32 v0, v0, v1
	v_cvt_pk_bf16_f32 v1, v3, v68
	v_mul_f32_e32 v96, 0x3e000000, v96
	ds_write_b64 v117, v[0:1] offset:34912
	v_add_u32_e32 v1, s4, v157
	v_mul_f32_e32 v204, v96, v190
	v_mul_f32_e32 v107, v107, v185
	v_mul_f32_e32 v185, v96, v192
	v_mul_f32_e32 v96, v191, v97
	v_fma_f32 v97, -0.5, v167, v193
	v_add_u32_e32 v0, s5, v116
	v_add_u32_e32 v3, 0x7f, v1
	v_med3_f32 v97, v97, s94, v180
	v_cndmask_b32_e64 v3, v0, v3, s[34:35]
	v_mul_f32_e32 v190, 0x3fb8aa3b, v97
	v_mul_f32_e32 v97, 0xbfb8aa3b, v97
	v_add_u32_e32 v152, v3, v158
	v_add_u32_e32 v3, 1, v0
	v_add_u32_e32 v68, 0x7e, v1
	v_exp_f32_e32 v97, v97
	v_cndmask_b32_e64 v3, v3, v68, s[34:35]
	v_add_u32_e32 v150, v3, v158
	v_add_u32_e32 v3, 2, v0
	v_add_u32_e32 v68, 0x7d, v1
	v_add_u32_e32 v0, 3, v0
	v_add_u32_e32 v1, 0x7c, v1
	v_cndmask_b32_e64 v0, v0, v1, s[34:35]
	s_waitcnt lgkmcnt(0)
	v_cndmask_b32_e64 v3, v3, v68, s[34:35]
	v_add_u32_e32 v146, v0, v158
	ds_read_b64_tr_b16 v[0:1], v155
	ds_read_b64_tr_b16 v[80:81], v155 offset:32
	ds_read_b64_tr_b16 v[76:77], v155 offset:64
	ds_read_b64_tr_b16 v[72:73], v155 offset:96
	ds_read_b64_tr_b16 v[92:93], v156
	ds_read_b64_tr_b16 v[88:89], v156 offset:32
	ds_read_b64_tr_b16 v[84:85], v156 offset:64
	ds_read_b64_tr_b16 v[68:69], v156 offset:96
	s_waitcnt lgkmcnt(0)
	v_exp_f32_e32 v190, v190
	v_mul_f32_e32 v191, 0x3fb8aa3b, v193
	v_mul_f32_e32 v97, v108, v97
	v_cvt_pk_bf16_f32 v102, v91, v102
	v_lshlrev_b32_e32 v91, 16, v100
	v_exp_f32_e32 v191, v191
	v_cvt_pk_bf16_f32 v103, v103, v104
	v_cvt_pk_bf16_f32 v104, v105, v106
	v_cvt_pk_bf16_f32 v105, v107, v97
	v_mul_f32_e32 v97, 0xbfb8aa3b, v91
	v_exp_f32_e32 v106, v97
	v_mul_f32_e32 v96, 0x3e000000, v96
	v_mul_f32_e32 v193, v96, v190
	v_and_b32_e32 v100, 0xffff0000, v100
	v_mul_f32_e32 v108, v96, v191
	v_cvt_pk_bf16_f32 v190, v201, v199
	v_cvt_pk_bf16_f32 v191, v200, v198
	v_cvt_pk_bf16_f32 v192, v203, v202
	v_cvt_pk_bf16_f32 v193, v204, v193
	v_cvt_pk_bf16_f32 v96, v182, v98
	v_mul_f32_e32 v182, 0xbfb8aa3b, v100
	v_add_f32_e32 v106, 1.0, v106
	v_exp_f32_e32 v182, v182
	v_rcp_f32_e32 v106, v106
	v_cvt_pk_bf16_f32 v97, v183, v99
	v_cvt_pk_bf16_f32 v98, v184, v205
	v_add_f32_e32 v182, 1.0, v182
	v_mul_f32_e32 v91, v106, v91
	v_fma_f32 v106, -0.5, v166, v194
	v_rcp_f32_e32 v182, v182
	v_med3_f32 v106, v106, s94, v180
	v_cvt_pk_bf16_f32 v99, v185, v108
	v_mul_f32_e32 v108, 0x3fb8aa3b, v106
	v_mul_f32_e32 v106, 0xbfb8aa3b, v106
	v_lshlrev_b32_e32 v107, 16, v101
	v_exp_f32_e32 v106, v106
	v_mul_f32_e32 v100, v182, v100
	v_mul_f32_e32 v182, 0xbfb8aa3b, v107
	v_exp_f32_e32 v108, v108
	v_exp_f32_e32 v182, v182
	v_mul_f32_e32 v78, v78, v106
	v_fma_f32 v106, -0.5, v164, v195
	v_mul_f32_e32 v91, 0x3e000000, v91
	v_mul_f32_e32 v183, 0x3fb8aa3b, v194
	v_med3_f32 v106, v106, s94, v180
	v_exp_f32_e32 v183, v183
	v_mul_f32_e32 v184, v91, v108
	v_mul_f32_e32 v108, 0x3fb8aa3b, v106
	v_mul_f32_e32 v106, 0xbfb8aa3b, v106
	v_add_f32_e32 v182, 1.0, v182
	v_exp_f32_e32 v106, v106
	v_rcp_f32_e32 v182, v182
	v_and_b32_e32 v101, 0xffff0000, v101
	v_mul_f32_e32 v91, v91, v183
	v_mul_f32_e32 v183, 0x3fb8aa3b, v195
	v_exp_f32_e32 v108, v108
	v_exp_f32_e32 v183, v183
	v_mul_f32_e32 v79, v79, v106
	v_mul_f32_e32 v106, v182, v107
	v_mul_f32_e32 v182, 0xbfb8aa3b, v101
	v_exp_f32_e32 v182, v182
	v_fma_f32 v107, -0.5, v165, v196
	v_mul_f32_e32 v100, 0x3e000000, v100
	v_med3_f32 v107, v107, s94, v180
	v_mul_f32_e32 v185, v100, v108
	v_mul_f32_e32 v100, v100, v183
	v_mul_f32_e32 v108, 0x3fb8aa3b, v107
	v_mul_f32_e32 v183, 0x3fb8aa3b, v196
	v_exp_f32_e32 v108, v108
	v_exp_f32_e32 v183, v183
	v_add_f32_e32 v182, 1.0, v182
	v_mul_f32_e32 v107, 0xbfb8aa3b, v107
	v_rcp_f32_e32 v182, v182
	v_exp_f32_e32 v107, v107
	v_mul_f32_e32 v106, 0x3e000000, v106
; __device__ __forceinline__ float siluf_(float x) { return x * sigmoidf_(x); }
; template <bool WITHO, bool RAW = false>
; __device__ __forceinline__ void hg_pass(const Frame& F, const bf16_t* P, const float* lbh, int b, int h, int nb, int dir, f32x4 (&S)[4][4], float (&Gsum)[16],
;                                         LAS bf16_t* Vl, LAS bf16_t* Kl, float* OF, const float* ngp) {
;     ...
;             for (int ks = 0; ks < 2; ++ks) { float kt_[8], qt_[8], qh_[8];
; #pragma unroll
;                 for (int mm = 0; mm < 2; ++mm) { const int m = 2 * ks + mm;
;                     const float qq[4] = {__uint_as_float(qr[m].x << 16), __uint_as_float(qr[m].x & 0xffff0000u), __uint_as_float(qr[m].y << 16), __uint_as_float(qr[m].y & 0xffff0000u)};
; #pragma unroll
;                     for (int i = 0; i < 4; ++i) { const int q = m * 4 + i; const float qv = siluf_(qq[i]) * 0.125f; const float d = fminf(fmaxf(c[q] - 0.5f * G[q], -80.0f), 80.0f);
;                         qt_[mm * 4 + i] = qv * __expf(d); kt_[mm * 4 + i] = kk[q] * __expf(-d); qh_[mm * 4 + i] = qv * __expf(c[q]); } }
;                 u32x4 w; w.x = cvt_pk_bf16(kt_[0], kt_[1]); w.y = cvt_pk_bf16(kt_[2], kt_[3]); w.z = cvt_pk_bf16(kt_[4], kt_[5]); w.w = cvt_pk_bf16(kt_[6], kt_[7]); __builtin_memcpy(&Ktf[ks], &w, 16);
;                 w.x = cvt_pk_bf16(qt_[0], qt_[1]); w.y = cvt_pk_bf16(qt_[2], qt_[3]); w.z = cvt_pk_bf16(qt_[4], qt_[5]); w.w = cvt_pk_bf16(qt_[6], qt_[7]); __builtin_memcpy(&Qtf[ks], &w, 16);
;                 w.x = cvt_pk_bf16(qh_[0], qh_[1]); w.y = cvt_pk_bf16(qh_[2], qh_[3]); w.z = cvt_pk_bf16(qh_[4], qh_[5]); w.w = cvt_pk_bf16(qh_[6], qh_[7]); __builtin_memcpy(&Qhf[ks], &w, 16); }
;             f32x4 AT = (f32x4){0.f, 0.f, 0.f, 0.f};
;             AT = __builtin_amdgcn_mfma_f32_16x16x32_bf16(Ktf[0], Qtf[0], AT, 0, 0, 0); AT = __builtin_amdgcn_mfma_f32_16x16x32_bf16(Ktf[1], Qtf[1], AT, 0, 0, 0);
; #pragma unroll
;             for (int i = 0; i < 4; ++i) AT[i] = (4 * g + i <= tau) ? AT[i] : 0.0f;
;             bf16x8 Af; { u32x4 w; w.x = cvt_pk_bf16(AT[0], AT[1]); w.y = cvt_pk_bf16(AT[2], AT[3]); w.z = 0u; w.w = 0u; __builtin_memcpy(&Af, &w, 16); }
;             f32x4 o[4];
; #pragma unroll
;             for (int vt = 0; vt < 4; ++vt) { o[vt] = __builtin_amdgcn_mfma_f32_16x16x32_bf16(Af, Vf[vt], (f32x4){0.f, 0.f, 0.f, 0.f}, 0, 0, 0);
; #pragma unroll
	v_mul_f32_e32 v195, v106, v108
	v_mul_f32_e32 v183, v106, v183
	v_fma_f32 v106, -0.5, v163, v197
	v_mul_f32_e32 v101, v182, v101
	v_med3_f32 v106, v106, s94, v180
	v_lshlrev_b32_e32 v182, 16, v86
	v_mul_f32_e32 v74, v74, v107
	v_mul_f32_e32 v107, 0x3fb8aa3b, v106
	v_mul_f32_e32 v108, 0x3fb8aa3b, v197
	v_mul_f32_e32 v194, 0xbfb8aa3b, v182
	v_exp_f32_e32 v107, v107
	v_exp_f32_e32 v108, v108
	v_exp_f32_e32 v194, v194
	v_mul_f32_e32 v101, 0x3e000000, v101
	v_mul_f32_e32 v196, v101, v107
	v_mul_f32_e32 v199, v101, v108
	v_add_f32_e32 v101, 1.0, v194
	v_rcp_f32_e32 v101, v101
	v_fma_f32 v107, -0.5, v161, v153
	v_mul_f32_e32 v106, 0xbfb8aa3b, v106
	v_med3_f32 v107, v107, s94, v180
	v_exp_f32_e32 v106, v106
	v_and_b32_e32 v86, 0xffff0000, v86
	v_mul_f32_e32 v108, 0x3fb8aa3b, v107
	v_mul_f32_e32 v107, 0xbfb8aa3b, v107
	v_mul_f32_e32 v101, v101, v182
	v_exp_f32_e32 v108, v108
	v_mul_f32_e32 v182, 0xbfb8aa3b, v86
	v_exp_f32_e32 v107, v107
	v_mul_f32_e32 v153, 0x3fb8aa3b, v153
	v_exp_f32_e32 v182, v182
	v_exp_f32_e32 v153, v153
	v_mul_f32_e32 v75, v75, v106
	v_lshlrev_b32_e32 v106, 16, v87
	v_mul_f32_e32 v101, 0x3e000000, v101
	v_mul_f32_e32 v197, v101, v108
	v_mul_f32_e32 v108, v109, v107
	v_mul_f32_e32 v109, 0xbfb8aa3b, v106
	v_add_f32_e32 v182, 1.0, v182
	v_mul_f32_e32 v153, v101, v153
	v_fma_f32 v101, -0.5, v162, v151
	v_exp_f32_e32 v109, v109
	v_rcp_f32_e32 v182, v182
	v_med3_f32 v101, v101, s94, v180
	v_mul_f32_e32 v107, 0x3fb8aa3b, v101
	v_exp_f32_e32 v107, v107
	v_mul_f32_e32 v101, 0xbfb8aa3b, v101
	v_add_f32_e32 v109, 1.0, v109
	v_mul_f32_e32 v86, v182, v86
	v_exp_f32_e32 v101, v101
	v_rcp_f32_e32 v109, v109
	v_mul_f32_e32 v86, 0x3e000000, v86
	v_mul_f32_e32 v182, v86, v107
	v_fma_f32 v107, -0.5, v160, v149
	v_and_b32_e32 v87, 0xffff0000, v87
	v_med3_f32 v107, v107, s94, v180
	v_mul_f32_e32 v151, 0x3fb8aa3b, v151
	v_mul_f32_e32 v101, v110, v101
	v_mul_f32_e32 v106, v109, v106
	v_mul_f32_e32 v109, 0x3fb8aa3b, v107
	v_mul_f32_e32 v110, 0xbfb8aa3b, v87
	v_mul_f32_e32 v149, 0x3fb8aa3b, v149
	v_exp_f32_e32 v151, v151
	v_exp_f32_e32 v109, v109
	v_exp_f32_e32 v110, v110
	v_exp_f32_e32 v149, v149
	v_mul_f32_e32 v107, 0xbfb8aa3b, v107
	v_exp_f32_e32 v107, v107
	v_mul_f32_e32 v106, 0x3e000000, v106
	v_mul_f32_e32 v86, v86, v151
	v_add_f32_e32 v110, 1.0, v110
	v_mul_f32_e32 v151, v106, v109
	v_mul_f32_e32 v149, v106, v149
	v_fma_f32 v106, -0.5, v159, v111
	v_rcp_f32_e32 v110, v110
	v_med3_f32 v106, v106, s94, v180
	v_mul_f32_e32 v70, v70, v107
	v_mul_f32_e32 v107, 0x3fb8aa3b, v106
	v_mul_f32_e32 v106, 0xbfb8aa3b, v106
	v_mul_f32_e32 v109, 0x3fb8aa3b, v111
	v_exp_f32_e32 v107, v107
	v_exp_f32_e32 v106, v106
	v_exp_f32_e32 v109, v109
	v_mul_f32_e32 v87, v110, v87
	v_mul_f32_e32 v87, 0x3e000000, v87
	v_mul_f32_e32 v110, v87, v107
	v_mul_f32_e32 v71, v71, v106
	v_mul_f32_e32 v87, v87, v109
	v_cvt_pk_bf16_f32 v106, v78, v79
	v_cvt_pk_bf16_f32 v107, v74, v75
	v_cvt_pk_bf16_f32 v108, v108, v101
	v_cvt_pk_bf16_f32 v109, v70, v71
	v_cvt_pk_bf16_f32 v194, v184, v185
	v_cvt_pk_bf16_f32 v195, v195, v196
	v_cvt_pk_bf16_f32 v196, v197, v182
	v_cvt_pk_bf16_f32 v197, v151, v110
	v_cvt_pk_bf16_f32 v198, v91, v100
	v_mfma_f32_16x16x32_bf16 v[100:103], v[102:105], v[190:193], 0
	v_mov_b32_e32 v192, v2
	v_mov_b32_e32 v193, v2
	v_add_u32_e32 v148, v3, v158
	v_mfma_f32_16x16x32_bf16 v[100:103], v[106:109], v[194:197], v[100:103]
	v_mov_b32_e32 v3, v2
	v_cvt_pk_bf16_f32 v199, v183, v199
	v_cvt_pk_bf16_f32 v200, v153, v86
	v_cvt_pk_bf16_f32 v201, v149, v87
	v_mov_b32_e32 v82, v2
	s_nop 5
	v_cndmask_b32_e64 v70, v100, 0, s[42:43]
	v_cndmask_b32_e64 v71, 0, v101, s[44:45]
	v_cndmask_b32_e64 v74, v102, 0, s[46:47]
	v_cndmask_b32_e64 v75, v103, 0, s[48:49]
	v_cvt_pk_bf16_f32 v190, v70, v71
	v_cvt_pk_bf16_f32 v191, v74, v75
	v_cvt_pk_bf16_f32 v104, v4, v5
	v_cvt_pk_bf16_f32 v105, v6, v7
	v_cvt_pk_bf16_f32 v106, v8, v9
	v_cvt_pk_bf16_f32 v107, v10, v11
	v_mov_b32_e32 v83, v2
	v_mfma_f32_16x16x32_bf16 v[100:103], v[190:193], v[0:3], 0
	v_mov_b32_e32 v78, v2
	v_mov_b32_e32 v79, v2
	v_mov_b32_e32 v74, v2
	v_mfma_f32_16x16x32_bf16 v[100:103], v[96:99], v[104:107], v[100:103]
	v_cvt_pk_bf16_f32 v104, v12, v13
	v_cvt_pk_bf16_f32 v105, v14, v15
	v_cvt_pk_bf16_f32 v106, v16, v17
	v_cvt_pk_bf16_f32 v107, v18, v19
	v_cvt_pk_bf16_f32 v108, v20, v21
	v_cvt_pk_bf16_f32 v109, v22, v23
	v_cvt_pk_bf16_f32 v110, v24, v25
	v_cvt_pk_bf16_f32 v111, v26, v27
	v_mov_b32_e32 v75, v2
	v_mfma_f32_16x16x32_bf16 v[100:103], v[198:201], v[104:107], v[100:103]
	v_ashrrev_i32_e32 v153, 31, v152
	v_ashrrev_i32_e32 v151, 31, v150
	v_lshlrev_b64 v[152:153], 11, v[152:153]
	v_mfma_f32_16x16x32_bf16 v[104:107], v[190:193], v[80:83], 0
	v_lshlrev_b64 v[150:151], 11, v[150:151]
	v_lshl_add_u64 v[152:153], v[122:123], 0, v[152:153]
	v_lshl_add_u64 v[150:151], v[122:123], 0, v[150:151]
	v_mfma_f32_16x16x32_bf16 v[104:107], v[96:99], v[108:111], v[104:107]
	v_cvt_pk_bf16_f32 v108, v28, v29
	v_cvt_pk_bf16_f32 v109, v30, v31
	v_cvt_pk_bf16_f32 v110, v32, v33
	v_cvt_pk_bf16_f32 v111, v34, v35
	v_cvt_pk_bf16_f32 v194, v36, v37
	v_cvt_pk_bf16_f32 v195, v38, v39
	v_cvt_pk_bf16_f32 v196, v40, v41
	v_cvt_pk_bf16_f32 v197, v42, v43
	v_mov_b32_e32 v94, v2
	v_mfma_f32_16x16x32_bf16 v[104:107], v[198:201], v[108:111], v[104:107]
	v_mov_b32_e32 v95, v2
	v_mov_b32_e32 v90, v2
	v_mov_b32_e32 v91, v2
	v_mfma_f32_16x16x32_bf16 v[108:111], v[190:193], v[76:79], 0
	v_mov_b32_e32 v86, v2
	v_mov_b32_e32 v87, v2
	v_mov_b32_e32 v70, v2
	v_mfma_f32_16x16x32_bf16 v[108:111], v[96:99], v[194:197], v[108:111]
; __device__ __forceinline__ unsigned cvt_pk_bf16(float lo, float hi) { unsigned r; asm volatile("v_cvt_pk_bf16_f32 %0, %1, %2" : "=v"(r) : "v"(lo), "v"(hi)); return r; }
; template <bool WITHO, bool RAW = false>
; __device__ __forceinline__ void hg_pass(const Frame& F, const bf16_t* P, const float* lbh, int b, int h, int nb, int dir, f32x4 (&S)[4][4], float (&Gsum)[16],
;                                         LAS bf16_t* Vl, LAS bf16_t* Kl, float* OF, const float* ngp) {
;     ...
;             for (int vt = 0; vt < 4; ++vt) { o[vt] = __builtin_amdgcn_mfma_f32_16x16x32_bf16(Af, Vf[vt], (f32x4){0.f, 0.f, 0.f, 0.f}, 0, 0, 0);
; #pragma unroll
;                 for (int ks = 0; ks < 2; ++ks) { u32x4 w; w.x = cvt_pk_bf16(S[2 * ks][vt][0], S[2 * ks][vt][1]); w.y = cvt_pk_bf16(S[2 * ks][vt][2], S[2 * ks][vt][3]);
;                     w.z = cvt_pk_bf16(S[2 * ks + 1][vt][0], S[2 * ks + 1][vt][1]); w.w = cvt_pk_bf16(S[2 * ks + 1][vt][2], S[2 * ks + 1][vt][3]); bf16x8 Sf; __builtin_memcpy(&Sf, &w, 16);
;                     o[vt] = __builtin_amdgcn_mfma_f32_16x16x32_bf16(Qhf[ks], Sf, o[vt], 0, 0, 0); } }
;             if (dir == 0 || RAW) {
; #pragma unroll
;                 for (int i = 0; i < 4; ++i)
; #pragma unroll
;                     for (int vt = 0; vt < 4; ++vt) OF[(size_t)orow[i] * 512 + h * 64 + 16 * vt + tau] = o[vt][i];
;             } else {
;                 { float tot[4][4], sq[4];
; #pragma unroll
;                 for (int i = 0; i < 4; ++i) { sq[i] = 0.f;
; #pragma unroll
;                     for (int vt = 0; vt < 4; ++vt) { tot[i][vt] = o[vt][i] + ofv[i][vt]; sq[i] = fmaf(tot[i][vt], tot[i][vt], sq[i]); } }
;                 ROW_ALLREDUCE4(sq[0], sq[1], sq[2], sq[3]);
; #pragma unroll
;                 for (int i = 0; i < 4; ++i) { const float rs = rsqrtf(sq[i] * (1.0f / 64.0f) + 1e-6f);
; #pragma unroll
;                     for (int vt = 0; vt < 4; ++vt) F.MIX[(size_t)orow[i] * DM + 512 + h * 64 + 16 * vt + tau] = f2bf(tot[i][vt] * rs * ngv[vt] * siluf_(gtv[i][vt])); } }
;             }
;         }
; #pragma unroll
;         for (int kt = 0; kt < 4; ++kt) { f32x4 eg;
; #pragma unroll
;             for (int i = 0; i < 4; ++i) eg[i] = __expf(G[kt * 4 + i]);
; #pragma unroll
;             for (int vt = 0; vt < 4; ++vt) S[kt][vt] = __builtin_amdgcn_mfma_f32_16x16x32_bf16(Kf[kt], Vf[vt], S[kt][vt] * eg, 0, 0, 0); }
	v_cvt_pk_bf16_f32 v194, v44, v45
	v_cvt_pk_bf16_f32 v195, v46, v47
	v_cvt_pk_bf16_f32 v196, v48, v49
	v_mfma_f32_16x16x32_bf16 v[190:193], v[190:193], v[72:75], 0
	v_cvt_pk_bf16_f32 v197, v50, v51
	v_mov_b32_e32 v71, v2
	v_ashrrev_i32_e32 v149, 31, v148
	v_mfma_f32_16x16x32_bf16 v[108:111], v[198:201], v[194:197], v[108:111]
	v_cvt_pk_bf16_f32 v194, v56, v57
	v_cvt_pk_bf16_f32 v195, v58, v59
	v_cvt_pk_bf16_f32 v196, v60, v61
	v_cvt_pk_bf16_f32 v197, v62, v63
	s_add_i32 s5, s5, 16
	v_mfma_f32_16x16x32_bf16 v[96:99], v[96:99], v[194:197], v[190:193]
	v_cvt_pk_bf16_f32 v190, v64, v65
	v_cvt_pk_bf16_f32 v191, v66, v67
	v_cvt_pk_bf16_f32 v192, v52, v53
	v_cvt_pk_bf16_f32 v193, v54, v55
	s_add_i32 s4, s4, -16
	s_nop 1
	v_mfma_f32_16x16x32_bf16 v[96:99], v[198:201], v[190:193], v[96:99]
	global_store_dword v[152:153], v100, off
	global_store_dword v[152:153], v104, off offset:64
	global_store_dword v[152:153], v108, off offset:128
	s_nop 4
	global_store_dword v[152:153], v96, off offset:192
	global_store_dword v[150:151], v101, off
	global_store_dword v[150:151], v105, off offset:64
	global_store_dword v[150:151], v109, off offset:128
	global_store_dword v[150:151], v97, off offset:192
	v_mul_f32_e32 v96, 0x3fb8aa3b, v173
	v_mul_f32_e32 v97, 0x3fb8aa3b, v171
	v_mul_f32_e32 v100, 0x3fb8aa3b, v172
	v_mul_f32_e32 v101, 0x3fb8aa3b, v170
	v_exp_f32_e32 v96, v96
	v_exp_f32_e32 v100, v100
	v_exp_f32_e32 v101, v101
	v_exp_f32_e32 v97, v97
	v_lshlrev_b64 v[104:105], 11, v[148:149]
	v_lshl_add_u64 v[104:105], v[122:123], 0, v[104:105]
	v_pk_mul_f32 v[6:7], v[6:7], v[100:101]
	v_pk_mul_f32 v[4:5], v[4:5], v[96:97]
	v_pk_mul_f32 v[22:23], v[22:23], v[100:101]
	v_pk_mul_f32 v[20:21], v[20:21], v[96:97]
	v_pk_mul_f32 v[38:39], v[38:39], v[100:101]
	v_pk_mul_f32 v[36:37], v[36:37], v[96:97]
	v_pk_mul_f32 v[58:59], v[58:59], v[100:101]
	v_pk_mul_f32 v[56:57], v[56:57], v[96:97]
	v_mul_f32_e32 v96, 0x3fb8aa3b, v168
	v_mul_f32_e32 v97, 0x3fb8aa3b, v169
	v_mul_f32_e32 v100, 0x3fb8aa3b, v147
	v_mul_f32_e32 v101, 0x3fb8aa3b, v167
	v_mfma_f32_16x16x32_bf16 v[4:7], v[92:95], v[0:3], v[4:7]
	v_exp_f32_e32 v96, v96
	v_exp_f32_e32 v100, v100
	v_exp_f32_e32 v101, v101
	v_mfma_f32_16x16x32_bf16 v[20:23], v[92:95], v[80:83], v[20:23]
	v_exp_f32_e32 v97, v97
	v_ashrrev_i32_e32 v147, 31, v146
	v_pk_mul_f32 v[10:11], v[10:11], v[100:101]
	v_mfma_f32_16x16x32_bf16 v[36:39], v[92:95], v[76:79], v[36:39]
	v_mul_f32_e64 v8, v8, v96
	v_mul_f32_e64 v9, v9, v97
	v_pk_mul_f32 v[26:27], v[26:27], v[100:101]
	v_pk_mul_f32 v[24:25], v[24:25], v[96:97]
	v_mfma_f32_16x16x32_bf16 v[56:59], v[92:95], v[72:75], v[56:59]
	v_mul_f32_e32 v92, 0x3fb8aa3b, v166
	v_mul_f32_e32 v93, 0x3fb8aa3b, v164
	v_exp_f32_e32 v92, v92
	v_exp_f32_e32 v93, v93
	v_pk_mul_f32 v[42:43], v[42:43], v[100:101]
	v_pk_mul_f32 v[40:41], v[40:41], v[96:97]
	v_pk_mul_f32 v[62:63], v[62:63], v[100:101]
	v_pk_mul_f32 v[60:61], v[60:61], v[96:97]
	v_mfma_f32_16x16x32_bf16 v[8:11], v[88:91], v[0:3], v[8:11]
	v_mul_f32_e32 v94, 0x3fb8aa3b, v165
	v_mul_f32_e32 v95, 0x3fb8aa3b, v163
	v_pk_mul_f32 v[12:13], v[12:13], v[92:93]
	v_mfma_f32_16x16x32_bf16 v[24:27], v[88:91], v[80:83], v[24:27]
	v_mul_f32_e64 v28, v28, v92
	v_mul_f32_e64 v29, v29, v93
	v_pk_mul_f32 v[44:45], v[44:45], v[92:93]
	v_pk_mul_f32 v[64:65], v[64:65], v[92:93]
	v_mfma_f32_16x16x32_bf16 v[40:43], v[88:91], v[76:79], v[40:43]
	v_mul_f32_e32 v92, 0x3fb8aa3b, v160
	v_mul_f32_e32 v93, 0x3fb8aa3b, v159
	v_exp_f32_e32 v94, v94
	v_mfma_f32_16x16x32_bf16 v[60:63], v[88:91], v[72:75], v[60:63]
	v_mul_f32_e32 v90, 0x3fb8aa3b, v161
	v_mul_f32_e32 v91, 0x3fb8aa3b, v162
	v_exp_f32_e32 v95, v95
	v_exp_f32_e32 v90, v90
	v_exp_f32_e32 v92, v92
	v_exp_f32_e32 v93, v93
	v_exp_f32_e32 v91, v91
	v_pk_mul_f32 v[14:15], v[14:15], v[94:95]
	v_pk_mul_f32 v[30:31], v[30:31], v[94:95]
	v_pk_mul_f32 v[46:47], v[46:47], v[94:95]
	v_pk_mul_f32 v[66:67], v[66:67], v[94:95]
	v_pk_mul_f32 v[18:19], v[18:19], v[92:93]
	v_pk_mul_f32 v[16:17], v[16:17], v[90:91]
	v_pk_mul_f32 v[34:35], v[34:35], v[92:93]
	v_pk_mul_f32 v[32:33], v[32:33], v[90:91]
	v_pk_mul_f32 v[50:51], v[50:51], v[92:93]
	v_pk_mul_f32 v[48:49], v[48:49], v[90:91]
	v_pk_mul_f32 v[54:55], v[54:55], v[92:93]
	v_pk_mul_f32 v[52:53], v[52:53], v[90:91]
	v_mfma_f32_16x16x32_bf16 v[12:15], v[84:87], v[0:3], v[12:15]
	v_lshlrev_b64 v[88:89], 11, v[146:147]
	v_lshl_add_u64 v[88:89], v[122:123], 0, v[88:89]
	s_cmpk_lg_i32 s5, 0x80
	v_mfma_f32_16x16x32_bf16 v[28:31], v[84:87], v[80:83], v[28:31]
	global_store_dword v[104:105], v102, off
	global_store_dword v[104:105], v106, off offset:64
	global_store_dword v[104:105], v110, off offset:128
	v_mfma_f32_16x16x32_bf16 v[44:47], v[84:87], v[76:79], v[44:47]
	global_store_dword v[104:105], v98, off offset:192
	global_store_dword v[88:89], v103, off
	global_store_dword v[88:89], v107, off offset:64
	v_mfma_f32_16x16x32_bf16 v[64:67], v[84:87], v[72:75], v[64:67]
	global_store_dword v[88:89], v111, off offset:128
	global_store_dword v[88:89], v99, off offset:192
	v_mfma_f32_16x16x32_bf16 v[16:19], v[68:71], v[0:3], v[16:19]
	v_mfma_f32_16x16x32_bf16 v[32:35], v[68:71], v[80:83], v[32:35]
	v_mfma_f32_16x16x32_bf16 v[48:51], v[68:71], v[76:79], v[48:51]
	v_mfma_f32_16x16x32_bf16 v[52:55], v[68:71], v[72:75], v[52:55]
	s_cbranch_scc0 .LBB0_677
	v_mov_b64_e32 v[90:91], v[128:129]
	v_mov_b64_e32 v[88:89], v[134:135]
	v_mov_b64_e32 v[84:85], v[140:141]
	v_mov_b64_e32 v[0:1], v[142:143]
	s_branch .LBB0_673

; #define LAS __attribute__((address_space(3)))
; __device__ __forceinline__ float sigmoidf_(float x) { return __builtin_amdgcn_rcpf(1.0f + __expf(-x)); }
; template <bool WITHO, bool RAW = false>
; __device__ __forceinline__ void hg_pass(const Frame& F, const bf16_t* P, const float* lbh, int b, int h, int nb, int dir, f32x4 (&S)[4][4], float (&Gsum)[16],
;                                         LAS bf16_t* Vl, LAS bf16_t* Kl, float* OF, const float* ngp) {
;     ...
; #pragma unroll
;         for (int m = 0; m < 4; ++m) { const float z0 = __uint_as_float(zr[m].x << 16), z1 = __uint_as_float(zr[m].x & 0xffff0000u), z2 = __uint_as_float(zr[m].y << 16), z3 = __uint_as_float(zr[m].y & 0xffff0000u);
;             const float zz[4] = {z0, z1, z2, z3};
;             const f32x4 lb4 = *(const f32x4*)(lbh + 16 * m + 4 * g);
; #pragma unroll
;             for (int i = 0; i < 4; ++i) { const float lb = lb4[i]; const float f = fmaxf(lb + (1.0f - lb) * sigmoidf_(zz[i]), 1e-30f); kk[m * 4 + i] = 1.0f - f; c[m * 4 + i] = __logf(f); }
;             *(LAS u32x2*)(Vl + tau * 64 + 16 * m + 4 * g) = vr[m];
;  }
;         if (ci + 1 < HG_U / 16) { const int pos = (ci + 1) * 16 + tau, t = dir ? (HG_U - 1 - pos) : pos; const bf16_t* pr = P + (size_t)hg_row(b, nb, t) * 4096 + h * 64 + 4 * g;
; #pragma unroll
;             for (int m = 0; m < 4; ++m) { zr[m] = *(const u32x2*)(pr + (dir ? 2560 : 2048) + 16 * m); vr[m] = *(const u32x2*)(pr + 3072 + 16 * m); } }
;         float G[16];
; #pragma unroll
;         for (int q = 0; q < 16; ++q) G[q] = c[q];
; #pragma unroll
;         for (int q = 0; q < 16; q += 4) ROW_ALLREDUCE4(G[q], G[q + 1], G[q + 2], G[q + 3]);
.LBB0_689:
	v_lshlrev_b32_e32 v3, 16, v134
	v_mul_f32_e32 v3, 0xbfb8aa3b, v3
	v_exp_f32_e32 v3, v3
	s_waitcnt vmcnt(0)
	v_sub_f32_e32 v137, 1.0, v80
	v_and_b32_e32 v134, 0xffff0000, v134
	v_mul_f32_e32 v134, 0xbfb8aa3b, v134
	v_add_f32_e32 v3, 1.0, v3
	v_rcp_f32_e32 v3, v3
	v_exp_f32_e32 v134, v134
	v_lshlrev_b32_e32 v136, 16, v135
	v_mul_f32_e32 v136, 0xbfb8aa3b, v136
	v_fma_f32 v3, v137, v3, v80
	v_max_f32_e32 v3, 0xda24260, v3
	v_add_f32_e32 v134, 1.0, v134
	v_rcp_f32_e32 v134, v134
	v_log_f32_e32 v80, v3
	v_exp_f32_e32 v136, v136
	v_and_b32_e32 v135, 0xffff0000, v135
	v_mul_f32_e32 v135, 0xbfb8aa3b, v135
	v_mul_f32_e32 v137, 0x3f317217, v80
	v_fma_f32 v137, v80, s93, -v137
	v_fmac_f32_e32 v137, 0x3377d1cf, v80
	v_fmac_f32_e32 v137, 0x3f317217, v80
	v_add_f32_e32 v136, 1.0, v136
	v_rcp_f32_e32 v136, v136
	v_mov_b32_e32 v80, v137
	v_sub_f32_e32 v137, 1.0, v81
	v_fma_f32 v81, v137, v134, v81
	v_max_f32_e32 v81, 0xda24260, v81
	v_mov_b32_e32 v148, v80
	v_log_f32_e32 v134, v81
	v_sub_f32_e32 v80, 1.0, v81
	v_exp_f32_e32 v135, v135
	v_sub_f32_e32 v3, 1.0, v3
	v_mul_f32_e32 v81, 0x3f317217, v134
	v_fma_f32 v81, v134, s93, -v81
	v_fmac_f32_e32 v81, 0x3377d1cf, v134
	v_fmac_f32_e32 v81, 0x3f317217, v134
	v_add_f32_e32 v135, 1.0, v135
	v_rcp_f32_e32 v135, v135
	v_sub_f32_e32 v134, 1.0, v82
	v_fma_f32 v82, v134, v136, v82
	v_max_f32_e32 v82, 0xda24260, v82
	v_mov_b32_e32 v149, v81
	v_log_f32_e32 v134, v82
	v_sub_f32_e32 v81, 1.0, v82
	s_add_i32 s5, s5, -16
	v_add_u32_e32 v147, 16, v147
	v_mul_f32_e32 v82, 0x3f317217, v134
	v_fma_f32 v82, v134, s93, -v82
	v_fmac_f32_e32 v82, 0x3377d1cf, v134
	v_fmac_f32_e32 v82, 0x3f317217, v134
	s_cmpk_lg_i32 s5, 0xffef
	s_nop 0
	v_sub_f32_e32 v134, 1.0, v83
	v_fmac_f32_e32 v83, v134, v135
	v_max_f32_e32 v83, 0xda24260, v83
	v_mov_b32_e32 v150, v82
	v_lshlrev_b32_e32 v135, 16, v132
	v_log_f32_e32 v134, v83
	v_mul_f32_e32 v135, 0xbfb8aa3b, v135
	v_exp_f32_e32 v135, v135
	v_sub_f32_e32 v82, 1.0, v83
	v_mul_f32_e32 v83, 0x3f317217, v134
	v_fma_f32 v83, v134, s93, -v83
	v_add_f32_e32 v135, 1.0, v135
	v_fmac_f32_e32 v83, 0x3377d1cf, v134
	v_rcp_f32_e32 v135, v135
	v_fmac_f32_e32 v83, 0x3f317217, v134
	v_and_b32_e32 v132, 0xffff0000, v132
	v_mul_f32_e32 v132, 0xbfb8aa3b, v132
	v_sub_f32_e32 v134, 1.0, v76
	v_fma_f32 v76, v135, v134, v76
	v_max_f32_e32 v76, 0xda24260, v76
	v_exp_f32_e32 v132, v132
	v_lshlrev_b32_e32 v135, 16, v133
	v_log_f32_e32 v134, v76
	v_add_f32_e32 v132, 1.0, v132
	v_rcp_f32_e32 v132, v132
	v_mul_f32_e32 v135, 0xbfb8aa3b, v135
	v_mul_f32_e32 v136, 0x3f317217, v134
	v_fma_f32 v136, v134, s93, -v136
	v_fmac_f32_e32 v136, 0x3377d1cf, v134
	v_fmac_f32_e32 v136, 0x3f317217, v134
	v_exp_f32_e32 v135, v135
	v_and_b32_e32 v133, 0xffff0000, v133
	v_mov_b32_e32 v134, v136
	v_sub_f32_e32 v136, 1.0, v77
	v_fma_f32 v77, v132, v136, v77
	v_max_f32_e32 v77, 0xda24260, v77
	v_mov_b32_e32 v151, v134
	v_log_f32_e32 v132, v77
	v_add_f32_e32 v135, 1.0, v135
	v_rcp_f32_e32 v135, v135
	v_mov_b32_e32 v139, v151
	v_mul_f32_e32 v134, 0x3f317217, v132
	v_fma_f32 v134, v132, s93, -v134
	v_fmac_f32_e32 v134, 0x3377d1cf, v132
	v_fmac_f32_e32 v134, 0x3f317217, v132
	v_add_f32_dpp v151, v151, v151 row_shr:1 row_mask:0xf bank_mask:0xf bound_ctrl:1
	v_sub_f32_e32 v76, 1.0, v76
	v_mov_b32_e32 v132, v134
	v_sub_f32_e32 v134, 1.0, v78
	v_fma_f32 v78, v135, v134, v78
	v_max_f32_e32 v78, 0xda24260, v78
	v_mov_b32_e32 v152, v132
	v_mul_f32_e32 v132, 0xbfb8aa3b, v133
	v_exp_f32_e32 v132, v132
	v_sub_f32_e32 v153, 1.0, v78
	v_log_f32_e32 v134, v78
	v_add_f32_e32 v132, 1.0, v132
	v_rcp_f32_e32 v132, v132
	v_sub_f32_e32 v133, 1.0, v79
	v_mul_f32_e32 v78, 0x3f317217, v134
	v_fma_f32 v78, v134, s93, -v78
	v_fmac_f32_e32 v78, 0x3377d1cf, v134
	v_fmac_f32_e32 v79, v132, v133
	v_fmac_f32_e32 v78, 0x3f317217, v134
	v_max_f32_e32 v79, 0xda24260, v79
	v_sub_f32_e32 v155, 1.0, v79
	v_mov_b32_e32 v154, v78
	v_mov_b32_e32 v132, v79
	v_lshlrev_b32_e32 v79, 16, v130
	v_log_f32_e32 v132, v132
	v_mul_f32_e32 v79, 0xbfb8aa3b, v79
	v_exp_f32_e32 v79, v79
	v_mov_b32_e32 v138, v152
	v_mul_f32_e32 v78, 0x3f317217, v132
	v_fma_f32 v78, v132, s93, -v78
	v_add_f32_e32 v79, 1.0, v79
	v_fmac_f32_e32 v78, 0x3377d1cf, v132
	v_rcp_f32_e32 v79, v79
	v_fmac_f32_e32 v78, 0x3f317217, v132
	v_add_f32_dpp v152, v152, v152 row_shr:1 row_mask:0xf bank_mask:0xf bound_ctrl:1
	v_add_f32_dpp v151, v151, v151 row_shr:2 row_mask:0xf bank_mask:0xf bound_ctrl:1
	v_mov_b32_e32 v156, v78
	v_and_b32_e32 v78, 0xffff0000, v130
	v_sub_f32_e32 v130, 1.0, v72
	v_fma_f32 v72, v79, v130, v72
	v_max_f32_e32 v72, 0xda24260, v72
	v_mul_f32_e32 v78, 0xbfb8aa3b, v78
	v_exp_f32_e32 v78, v78
	v_log_f32_e32 v79, v72
	v_add_f32_e32 v78, 1.0, v78
	v_rcp_f32_e32 v78, v78
	v_lshlrev_b32_e32 v130, 16, v131
	v_mul_f32_e32 v132, 0x3f317217, v79
	v_fma_f32 v132, v79, s93, -v132
	v_fmac_f32_e32 v132, 0x3377d1cf, v79
	v_fmac_f32_e32 v132, 0x3f317217, v79
	v_mul_f32_e32 v130, 0xbfb8aa3b, v130
	v_exp_f32_e32 v130, v130
	v_mov_b32_e32 v79, v132
	v_sub_f32_e32 v132, 1.0, v73
	v_fma_f32 v73, v78, v132, v73
	v_max_f32_e32 v73, 0xda24260, v73
	v_mov_b32_e32 v157, v79
	v_log_f32_e32 v78, v73
	v_add_f32_e32 v130, 1.0, v130
	v_rcp_f32_e32 v130, v130
	v_and_b32_e32 v131, 0xffff0000, v131
	v_mul_f32_e32 v79, 0x3f317217, v78
	v_fma_f32 v79, v78, s93, -v79
	v_fmac_f32_e32 v79, 0x3377d1cf, v78
	v_fmac_f32_e32 v79, 0x3f317217, v78
	v_add_f32_dpp v152, v152, v152 row_shr:2 row_mask:0xf bank_mask:0xf bound_ctrl:1
	v_mov_b32_e32 v137, v157
	v_mov_b32_e32 v78, v79
	v_sub_f32_e32 v79, 1.0, v74
	v_fma_f32 v74, v130, v79, v74
	v_max_f32_e32 v74, 0xda24260, v74
	v_mov_b32_e32 v158, v78
	v_mul_f32_e32 v78, 0xbfb8aa3b, v131
; #define LAS __attribute__((address_space(3)))
; __device__ __forceinline__ float sigmoidf_(float x) { return __builtin_amdgcn_rcpf(1.0f + __expf(-x)); }
; template <int CTRL> __device__ __forceinline__ float dpp_add0(float x) { return x + dppf<CTRL>(0.0f, x); }
; template <bool WITHO, bool RAW = false>
; __device__ __forceinline__ void hg_pass(const Frame& F, const bf16_t* P, const float* lbh, int b, int h, int nb, int dir, f32x4 (&S)[4][4], float (&Gsum)[16],
;                                         LAS bf16_t* Vl, LAS bf16_t* Kl, float* OF, const float* ngp) {
;     ...
;         for (int m = 0; m < 4; ++m) { const float z0 = __uint_as_float(zr[m].x << 16), z1 = __uint_as_float(zr[m].x & 0xffff0000u), z2 = __uint_as_float(zr[m].y << 16), z3 = __uint_as_float(zr[m].y & 0xffff0000u);
;             const float zz[4] = {z0, z1, z2, z3};
;             const f32x4 lb4 = *(const f32x4*)(lbh + 16 * m + 4 * g);
; #pragma unroll
;             for (int i = 0; i < 4; ++i) { const float lb = lb4[i]; const float f = fmaxf(lb + (1.0f - lb) * sigmoidf_(zz[i]), 1e-30f); kk[m * 4 + i] = 1.0f - f; c[m * 4 + i] = __logf(f); }
;             *(LAS u32x2*)(Vl + tau * 64 + 16 * m + 4 * g) = vr[m];
;  }
;         if (ci + 1 < HG_U / 16) { const int pos = (ci + 1) * 16 + tau, t = dir ? (HG_U - 1 - pos) : pos; const bf16_t* pr = P + (size_t)hg_row(b, nb, t) * 4096 + h * 64 + 4 * g;
; #pragma unroll
;             for (int m = 0; m < 4; ++m) { zr[m] = *(const u32x2*)(pr + (dir ? 2560 : 2048) + 16 * m); vr[m] = *(const u32x2*)(pr + 3072 + 16 * m); } }
;         float G[16];
; #pragma unroll
;         for (int q = 0; q < 16; ++q) G[q] = c[q];
; #pragma unroll
;         for (int q = 0; q < 16; q += 4) ROW_ALLREDUCE4(G[q], G[q + 1], G[q + 2], G[q + 3]);
; #pragma unroll
;         for (int q = 0; q < 16; ++q) { c[q] = dpp_add0<0x111>(c[q]); c[q] = dpp_add0<0x112>(c[q]); c[q] = dpp_add0<0x114>(c[q]); c[q] = dpp_add0<0x118>(c[q]); }
; #pragma unroll
;         for (int q = 0; q < 16; ++q) Gsum[q] += G[q];
	v_log_f32_e32 v79, v74
	v_exp_f32_e32 v78, v78
	v_sub_f32_e32 v159, 1.0, v74
	v_mov_b32_e32 v136, v158
	v_mul_f32_e32 v74, 0x3f317217, v79
	v_add_f32_e32 v78, 1.0, v78
	v_fma_f32 v74, v79, s93, -v74
	v_rcp_f32_e32 v78, v78
	v_fmac_f32_e32 v74, 0x3377d1cf, v79
	v_fmac_f32_e32 v74, 0x3f317217, v79
	v_add_f32_dpp v151, v151, v151 row_shr:4 row_mask:0xf bank_mask:0xf bound_ctrl:1
	v_add_f32_dpp v152, v152, v152 row_shr:4 row_mask:0xf bank_mask:0xf bound_ctrl:1
	v_sub_f32_e32 v79, 1.0, v75
	v_fmac_f32_e32 v75, v78, v79
	v_max_f32_e32 v75, 0xda24260, v75
	v_sub_f32_e32 v161, 1.0, v75
	v_mov_b32_e32 v78, v75
	v_lshlrev_b32_e32 v75, 16, v0
	v_log_f32_e32 v78, v78
	v_mul_f32_e32 v75, 0xbfb8aa3b, v75
	v_exp_f32_e32 v75, v75
	v_mov_b32_e32 v160, v74
	v_mul_f32_e32 v74, 0x3f317217, v78
	v_fma_f32 v74, v78, s93, -v74
	v_add_f32_e32 v75, 1.0, v75
	v_fmac_f32_e32 v74, 0x3377d1cf, v78
	v_rcp_f32_e32 v75, v75
	v_fmac_f32_e32 v74, 0x3f317217, v78
	v_and_b32_e32 v0, 0xffff0000, v0
	v_mul_f32_e32 v0, 0xbfb8aa3b, v0
	v_mov_b32_e32 v162, v74
	v_sub_f32_e32 v74, 1.0, v68
	v_fma_f32 v68, v75, v74, v68
	v_max_f32_e32 v68, 0xda24260, v68
	v_exp_f32_e32 v0, v0
	v_lshlrev_b32_e32 v75, 16, v1
	v_log_f32_e32 v74, v68
	v_add_f32_e32 v0, 1.0, v0
	v_rcp_f32_e32 v0, v0
	v_and_b32_e32 v1, 0xffff0000, v1
	v_mul_f32_e32 v78, 0x3f317217, v74
	v_fma_f32 v78, v74, s93, -v78
	v_fmac_f32_e32 v78, 0x3377d1cf, v74
	v_fmac_f32_e32 v78, 0x3f317217, v74
	v_mul_f32_e32 v1, 0xbfb8aa3b, v1
	v_exp_f32_e32 v1, v1
	v_mov_b32_e32 v74, v78
	v_sub_f32_e32 v78, 1.0, v69
	v_fma_f32 v0, v0, v78, v69
	v_max_f32_e32 v0, 0xda24260, v0
	v_mov_b32_e32 v163, v74
	v_mul_f32_e32 v74, 0xbfb8aa3b, v75
	v_log_f32_e32 v69, v0
	v_exp_f32_e32 v74, v74
	v_sub_f32_e32 v164, 1.0, v0
	v_add_f32_e32 v1, 1.0, v1
	v_mul_f32_e32 v0, 0x3f317217, v69
	v_add_f32_e32 v74, 1.0, v74
	v_fma_f32 v0, v69, s93, -v0
	v_rcp_f32_e32 v74, v74
	v_fmac_f32_e32 v0, 0x3377d1cf, v69
	v_fmac_f32_e32 v0, 0x3f317217, v69
	v_rcp_f32_e32 v1, v1
	v_mov_b32_e32 v75, v148
	v_sub_f32_e32 v69, 1.0, v70
	v_fma_f32 v69, v74, v69, v70
	v_max_f32_e32 v69, 0xda24260, v69
	v_log_f32_e32 v70, v69
	v_mov_b32_e32 v132, v0
	v_add_f32_dpp v0, v0, v0 row_shr:1 row_mask:0xf bank_mask:0xf bound_ctrl:1
	v_add_f32_dpp v148, v148, v148 row_shr:1 row_mask:0xf bank_mask:0xf bound_ctrl:1
	v_mul_f32_e32 v74, 0x3f317217, v70
	v_fma_f32 v74, v70, s93, -v74
	v_fmac_f32_e32 v74, 0x3377d1cf, v70
	v_fmac_f32_e32 v74, 0x3f317217, v70
	v_add_f32_dpp v0, v0, v0 row_shr:2 row_mask:0xf bank_mask:0xf bound_ctrl:1
	v_mov_b32_e32 v78, v83
	v_mov_b32_e32 v70, v74
	v_sub_f32_e32 v74, 1.0, v71
	v_fmac_f32_e32 v71, v1, v74
	v_max_f32_e32 v1, 0xda24260, v71
	v_sub_f32_e32 v166, 1.0, v1
	v_log_f32_e32 v71, v1
	v_mov_b32_e32 v165, v70
	v_add_f32_dpp v0, v0, v0 row_shr:4 row_mask:0xf bank_mask:0xf bound_ctrl:1
	v_mul_f32_e32 v1, 0x3f317217, v71
	v_fma_f32 v1, v71, s93, -v1
	v_fmac_f32_e32 v1, 0x3377d1cf, v71
	v_fmac_f32_e32 v1, 0x3f317217, v71
	v_add_f32_dpp v167, v0, v0 row_shr:8 row_mask:0xf bank_mask:0xf bound_ctrl:1
	v_add_f32_dpp v0, v165, v165 row_shr:1 row_mask:0xf bank_mask:0xf bound_ctrl:1
	s_nop 1
	v_add_f32_dpp v0, v0, v0 row_shr:2 row_mask:0xf bank_mask:0xf bound_ctrl:1
	v_mov_b32_e32 v74, v149
	v_add_f32_dpp v149, v149, v149 row_shr:1 row_mask:0xf bank_mask:0xf bound_ctrl:1
	v_add_f32_dpp v0, v0, v0 row_shr:4 row_mask:0xf bank_mask:0xf bound_ctrl:1
	v_mov_b32_e32 v79, v150
	v_mov_b32_e32 v131, v165
	v_add_f32_dpp v148, v148, v148 row_shr:2 row_mask:0xf bank_mask:0xf bound_ctrl:1
	v_add_f32_dpp v149, v149, v149 row_shr:2 row_mask:0xf bank_mask:0xf bound_ctrl:1
	v_add_f32_dpp v150, v150, v150 row_shr:1 row_mask:0xf bank_mask:0xf bound_ctrl:1
	v_add_f32_dpp v83, v83, v83 row_shr:1 row_mask:0xf bank_mask:0xf bound_ctrl:1
	v_add_f32_dpp v165, v0, v0 row_shr:8 row_mask:0xf bank_mask:0xf bound_ctrl:1
	v_add_f32_dpp v0, v1, v1 row_shr:1 row_mask:0xf bank_mask:0xf bound_ctrl:1
	v_add_f32_dpp v148, v148, v148 row_shr:4 row_mask:0xf bank_mask:0xf bound_ctrl:1
	v_add_f32_dpp v149, v149, v149 row_shr:4 row_mask:0xf bank_mask:0xf bound_ctrl:1
	v_add_f32_dpp v150, v150, v150 row_shr:2 row_mask:0xf bank_mask:0xf bound_ctrl:1
	v_add_f32_dpp v83, v83, v83 row_shr:2 row_mask:0xf bank_mask:0xf bound_ctrl:1
	v_add_f32_dpp v0, v0, v0 row_shr:2 row_mask:0xf bank_mask:0xf bound_ctrl:1
	v_add_f32_dpp v148, v148, v148 row_shr:8 row_mask:0xf bank_mask:0xf bound_ctrl:1
	v_add_f32_dpp v149, v149, v149 row_shr:8 row_mask:0xf bank_mask:0xf bound_ctrl:1
	v_add_f32_dpp v150, v150, v150 row_shr:4 row_mask:0xf bank_mask:0xf bound_ctrl:1
	v_add_f32_dpp v83, v83, v83 row_shr:4 row_mask:0xf bank_mask:0xf bound_ctrl:1
	v_add_f32_dpp v0, v0, v0 row_shr:4 row_mask:0xf bank_mask:0xf bound_ctrl:1
	s_nop 1
	v_add_f32_dpp v75, v75, v75 quad_perm:[1,0,3,2] row_mask:0xf bank_mask:0xf
	v_add_f32_dpp v74, v74, v74 quad_perm:[1,0,3,2] row_mask:0xf bank_mask:0xf
	v_add_f32_dpp v79, v79, v79 quad_perm:[1,0,3,2] row_mask:0xf bank_mask:0xf
	v_add_f32_dpp v78, v78, v78 quad_perm:[1,0,3,2] row_mask:0xf bank_mask:0xf
	v_add_f32_dpp v75, v75, v75 quad_perm:[2,3,0,1] row_mask:0xf bank_mask:0xf
	v_add_f32_dpp v74, v74, v74 quad_perm:[2,3,0,1] row_mask:0xf bank_mask:0xf
	v_add_f32_dpp v79, v79, v79 quad_perm:[2,3,0,1] row_mask:0xf bank_mask:0xf
	v_add_f32_dpp v78, v78, v78 quad_perm:[2,3,0,1] row_mask:0xf bank_mask:0xf
	v_add_f32_dpp v75, v75, v75 row_half_mirror row_mask:0xf bank_mask:0xf
	v_add_f32_dpp v74, v74, v74 row_half_mirror row_mask:0xf bank_mask:0xf
	v_add_f32_dpp v79, v79, v79 row_half_mirror row_mask:0xf bank_mask:0xf
	v_add_f32_dpp v78, v78, v78 row_half_mirror row_mask:0xf bank_mask:0xf
; #define LAS __attribute__((address_space(3)))
; __device__ __forceinline__ unsigned cvt_pk_bf16(float lo, float hi) { unsigned r; asm volatile("v_cvt_pk_bf16_f32 %0, %1, %2" : "=v"(r) : "v"(lo), "v"(hi)); return r; }
; template <int CTRL> __device__ __forceinline__ float dpp_add0(float x) { return x + dppf<CTRL>(0.0f, x); }
; template <bool WITHO, bool RAW = false>
; __device__ __forceinline__ void hg_pass(const Frame& F, const bf16_t* P, const float* lbh, int b, int h, int nb, int dir, f32x4 (&S)[4][4], float (&Gsum)[16],
;                                         LAS bf16_t* Vl, LAS bf16_t* Kl, float* OF, const float* ngp) {
;     ...
;         float G[16];
; #pragma unroll
;         for (int q = 0; q < 16; ++q) G[q] = c[q];
; #pragma unroll
;         for (int q = 0; q < 16; q += 4) ROW_ALLREDUCE4(G[q], G[q + 1], G[q + 2], G[q + 3]);
; #pragma unroll
;         for (int q = 0; q < 16; ++q) { c[q] = dpp_add0<0x111>(c[q]); c[q] = dpp_add0<0x112>(c[q]); c[q] = dpp_add0<0x114>(c[q]); c[q] = dpp_add0<0x118>(c[q]); }
; #pragma unroll
;         for (int q = 0; q < 16; ++q) Gsum[q] += G[q];
; #pragma unroll
;         for (int m = 0; m < 4; ++m) { float kh[4];
; #pragma unroll
;             for (int i = 0; i < 4; ++i) kh[i] = kk[m * 4 + i] * __expf(G[m * 4 + i] - c[m * 4 + i]);
;             u32x2 w; w.x = cvt_pk_bf16(kh[0], kh[1]); w.y = cvt_pk_bf16(kh[2], kh[3]);
;             *(LAS u32x2*)(Kl + tau * 64 + 16 * m + 4 * g) = w; }
	v_add_f32_dpp v75, v75, v75 row_mirror row_mask:0xf bank_mask:0xf
	v_add_f32_dpp v74, v74, v74 row_mirror row_mask:0xf bank_mask:0xf
	v_add_f32_dpp v79, v79, v79 row_mirror row_mask:0xf bank_mask:0xf
	v_add_f32_dpp v78, v78, v78 row_mirror row_mask:0xf bank_mask:0xf
	v_mov_b32_e32 v130, v1
	v_add_f32_dpp v150, v150, v150 row_shr:8 row_mask:0xf bank_mask:0xf bound_ctrl:1
	v_add_f32_dpp v83, v83, v83 row_shr:8 row_mask:0xf bank_mask:0xf bound_ctrl:1
	v_add_f32_dpp v168, v0, v0 row_shr:8 row_mask:0xf bank_mask:0xf bound_ctrl:1
	v_sub_f32_e32 v0, v75, v148
	v_sub_f32_e32 v1, v74, v149
	v_mul_f32_e32 v0, 0x3fb8aa3b, v0
	v_mul_f32_e32 v1, 0x3fb8aa3b, v1
	v_sub_f32_e32 v148, v79, v150
	v_sub_f32_e32 v83, v78, v83
	v_exp_f32_e32 v0, v0
	v_exp_f32_e32 v1, v1
	v_mul_f32_e32 v148, 0x3fb8aa3b, v148
	v_mul_f32_e32 v83, 0x3fb8aa3b, v83
	v_exp_f32_e32 v148, v148
	v_exp_f32_e32 v83, v83
	v_mov_b32_e32 v71, v154
	v_mov_b32_e32 v70, v156
	v_add_f32_dpp v154, v154, v154 row_shr:1 row_mask:0xf bank_mask:0xf bound_ctrl:1
	v_add_f32_dpp v156, v156, v156 row_shr:1 row_mask:0xf bank_mask:0xf bound_ctrl:1
	v_mov_b32_e32 v134, v162
	v_mov_b32_e32 v135, v160
	v_mov_b32_e32 v133, v163
	v_add_f32_dpp v154, v154, v154 row_shr:2 row_mask:0xf bank_mask:0xf bound_ctrl:1
	v_add_f32_dpp v156, v156, v156 row_shr:2 row_mask:0xf bank_mask:0xf bound_ctrl:1
	v_mul_f32_e32 v0, v3, v0
	v_mul_f32_e32 v1, v80, v1
	s_nop 1
	v_add_f32_dpp v139, v139, v139 quad_perm:[1,0,3,2] row_mask:0xf bank_mask:0xf
	v_add_f32_dpp v138, v138, v138 quad_perm:[1,0,3,2] row_mask:0xf bank_mask:0xf
	v_add_f32_dpp v71, v71, v71 quad_perm:[1,0,3,2] row_mask:0xf bank_mask:0xf
	v_add_f32_dpp v70, v70, v70 quad_perm:[1,0,3,2] row_mask:0xf bank_mask:0xf
	v_add_f32_dpp v139, v139, v139 quad_perm:[2,3,0,1] row_mask:0xf bank_mask:0xf
	v_add_f32_dpp v138, v138, v138 quad_perm:[2,3,0,1] row_mask:0xf bank_mask:0xf
	v_add_f32_dpp v71, v71, v71 quad_perm:[2,3,0,1] row_mask:0xf bank_mask:0xf
	v_add_f32_dpp v70, v70, v70 quad_perm:[2,3,0,1] row_mask:0xf bank_mask:0xf
	v_add_f32_dpp v139, v139, v139 row_half_mirror row_mask:0xf bank_mask:0xf
	v_add_f32_dpp v138, v138, v138 row_half_mirror row_mask:0xf bank_mask:0xf
	v_add_f32_dpp v71, v71, v71 row_half_mirror row_mask:0xf bank_mask:0xf
	v_add_f32_dpp v70, v70, v70 row_half_mirror row_mask:0xf bank_mask:0xf
	v_add_f32_dpp v139, v139, v139 row_mirror row_mask:0xf bank_mask:0xf
	v_add_f32_dpp v138, v138, v138 row_mirror row_mask:0xf bank_mask:0xf
	v_add_f32_dpp v71, v71, v71 row_mirror row_mask:0xf bank_mask:0xf
	v_add_f32_dpp v70, v70, v70 row_mirror row_mask:0xf bank_mask:0xf
	s_nop 1
	v_add_f32_dpp v137, v137, v137 quad_perm:[1,0,3,2] row_mask:0xf bank_mask:0xf
	v_add_f32_dpp v136, v136, v136 quad_perm:[1,0,3,2] row_mask:0xf bank_mask:0xf
	v_add_f32_dpp v135, v135, v135 quad_perm:[1,0,3,2] row_mask:0xf bank_mask:0xf
	v_add_f32_dpp v134, v134, v134 quad_perm:[1,0,3,2] row_mask:0xf bank_mask:0xf
	v_add_f32_dpp v137, v137, v137 quad_perm:[2,3,0,1] row_mask:0xf bank_mask:0xf
	v_add_f32_dpp v136, v136, v136 quad_perm:[2,3,0,1] row_mask:0xf bank_mask:0xf
	v_add_f32_dpp v135, v135, v135 quad_perm:[2,3,0,1] row_mask:0xf bank_mask:0xf
	v_add_f32_dpp v134, v134, v134 quad_perm:[2,3,0,1] row_mask:0xf bank_mask:0xf
	v_add_f32_dpp v137, v137, v137 row_half_mirror row_mask:0xf bank_mask:0xf
	v_add_f32_dpp v136, v136, v136 row_half_mirror row_mask:0xf bank_mask:0xf
	v_add_f32_dpp v135, v135, v135 row_half_mirror row_mask:0xf bank_mask:0xf
	v_add_f32_dpp v134, v134, v134 row_half_mirror row_mask:0xf bank_mask:0xf
	v_add_f32_dpp v137, v137, v137 row_mirror row_mask:0xf bank_mask:0xf
	v_add_f32_dpp v136, v136, v136 row_mirror row_mask:0xf bank_mask:0xf
	v_add_f32_dpp v135, v135, v135 row_mirror row_mask:0xf bank_mask:0xf
	v_add_f32_dpp v134, v134, v134 row_mirror row_mask:0xf bank_mask:0xf
	s_nop 1
	v_add_f32_dpp v133, v133, v133 quad_perm:[1,0,3,2] row_mask:0xf bank_mask:0xf
	v_add_f32_dpp v132, v132, v132 quad_perm:[1,0,3,2] row_mask:0xf bank_mask:0xf
	v_add_f32_dpp v131, v131, v131 quad_perm:[1,0,3,2] row_mask:0xf bank_mask:0xf
	v_add_f32_dpp v130, v130, v130 quad_perm:[1,0,3,2] row_mask:0xf bank_mask:0xf
	v_add_f32_dpp v133, v133, v133 quad_perm:[2,3,0,1] row_mask:0xf bank_mask:0xf
	v_add_f32_dpp v132, v132, v132 quad_perm:[2,3,0,1] row_mask:0xf bank_mask:0xf
	v_add_f32_dpp v131, v131, v131 quad_perm:[2,3,0,1] row_mask:0xf bank_mask:0xf
	v_add_f32_dpp v130, v130, v130 quad_perm:[2,3,0,1] row_mask:0xf bank_mask:0xf
	v_add_f32_dpp v133, v133, v133 row_half_mirror row_mask:0xf bank_mask:0xf
	v_add_f32_dpp v132, v132, v132 row_half_mirror row_mask:0xf bank_mask:0xf
	v_add_f32_dpp v131, v131, v131 row_half_mirror row_mask:0xf bank_mask:0xf
	v_add_f32_dpp v130, v130, v130 row_half_mirror row_mask:0xf bank_mask:0xf
	v_add_f32_dpp v133, v133, v133 row_mirror row_mask:0xf bank_mask:0xf
	v_add_f32_dpp v132, v132, v132 row_mirror row_mask:0xf bank_mask:0xf
	v_add_f32_dpp v131, v131, v131 row_mirror row_mask:0xf bank_mask:0xf
	v_add_f32_dpp v130, v130, v130 row_mirror row_mask:0xf bank_mask:0xf
	v_add_f32_dpp v151, v151, v151 row_shr:8 row_mask:0xf bank_mask:0xf bound_ctrl:1
	v_add_f32_dpp v152, v152, v152 row_shr:8 row_mask:0xf bank_mask:0xf bound_ctrl:1
	v_add_f32_dpp v154, v154, v154 row_shr:4 row_mask:0xf bank_mask:0xf bound_ctrl:1
	v_add_f32_dpp v156, v156, v156 row_shr:4 row_mask:0xf bank_mask:0xf bound_ctrl:1
	v_mul_f32_e32 v3, v81, v148
	v_mul_f32_e32 v80, v82, v83
	v_cvt_pk_bf16_f32 v0, v0, v1
	v_cvt_pk_bf16_f32 v1, v3, v80
	v_add_f32_dpp v154, v154, v154 row_shr:8 row_mask:0xf bank_mask:0xf bound_ctrl:1
	v_add_f32_dpp v156, v156, v156 row_shr:8 row_mask:0xf bank_mask:0xf bound_ctrl:1
; #define LAS __attribute__((address_space(3)))
; __device__ __forceinline__ float bf2f(unsigned short b) { return __uint_as_float(((unsigned)b) << 16); }
; __device__ __forceinline__ unsigned cvt_pk_bf16(float lo, float hi) { unsigned r; asm volatile("v_cvt_pk_bf16_f32 %0, %1, %2" : "=v"(r) : "v"(lo), "v"(hi)); return r; }
; template <int CTRL> __device__ __forceinline__ float dpp_add0(float x) { return x + dppf<CTRL>(0.0f, x); }
; template <bool WITHO, bool RAW = false>
; __device__ __forceinline__ void hg_pass(const Frame& F, const bf16_t* P, const float* lbh, int b, int h, int nb, int dir, f32x4 (&S)[4][4], float (&Gsum)[16],
;                                         LAS bf16_t* Vl, LAS bf16_t* Kl, float* OF, const float* ngp) {
;     ...
;         for (int q = 0; q < 16; q += 4) ROW_ALLREDUCE4(G[q], G[q + 1], G[q + 2], G[q + 3]);
; #pragma unroll
;         for (int q = 0; q < 16; ++q) { c[q] = dpp_add0<0x111>(c[q]); c[q] = dpp_add0<0x112>(c[q]); c[q] = dpp_add0<0x114>(c[q]); c[q] = dpp_add0<0x118>(c[q]); }
; #pragma unroll
;         for (int q = 0; q < 16; ++q) Gsum[q] += G[q];
; #pragma unroll
;         for (int m = 0; m < 4; ++m) { float kh[4];
; #pragma unroll
;             for (int i = 0; i < 4; ++i) kh[i] = kk[m * 4 + i] * __expf(G[m * 4 + i] - c[m * 4 + i]);
;             u32x2 w; w.x = cvt_pk_bf16(kh[0], kh[1]); w.y = cvt_pk_bf16(kh[2], kh[3]);
;             *(LAS u32x2*)(Kl + tau * 64 + 16 * m + 4 * g) = w; }
;         float ofv[4][4], gtv[4][4]; int orow[4];
;         if (WITHO) {
; #pragma unroll
;             for (int i = 0; i < 4; ++i) { const int p2 = ci * 16 + 4 * g + i, t2 = dir ? (HG_U - 1 - p2) : p2; orow[i] = hg_row(b, nb, t2); }
;             if (dir && !RAW) {
; #pragma unroll
;                 for (int i = 0; i < 4; ++i)
; #pragma unroll
;                     for (int vt = 0; vt < 4; ++vt) { ofv[i][vt] = OF[(size_t)orow[i] * 512 + h * 64 + 16 * vt + tau]; gtv[i][vt] = bf2f(P[(size_t)orow[i] * 4096 + 3584 + h * 64 + 16 * vt + tau]); }
;             }
;         }
;         asm volatile("s_waitcnt lgkmcnt(0)" ::: "memory");
;     ...
; #pragma unroll
;         for (int kt = 0; kt < 4; ++kt) { f32x4 eg;
; #pragma unroll
;             for (int i = 0; i < 4; ++i) eg[i] = __expf(G[kt * 4 + i]);
; #pragma unroll
;             for (int vt = 0; vt < 4; ++vt) S[kt][vt] = __builtin_amdgcn_mfma_f32_16x16x32_bf16(Kf[kt], Vf[vt], S[kt][vt] * eg, 0, 0, 0); }
	ds_write_b64 v143, v[0:1] offset:34816
	v_sub_f32_e32 v0, v139, v151
	v_sub_f32_e32 v1, v138, v152
	v_mul_f32_e32 v0, 0x3fb8aa3b, v0
	v_mul_f32_e32 v1, 0x3fb8aa3b, v1
	v_sub_f32_e32 v3, v71, v154
	v_sub_f32_e32 v80, v70, v156
	v_exp_f32_e32 v0, v0
	v_exp_f32_e32 v1, v1
	v_mul_f32_e32 v3, 0x3fb8aa3b, v3
	v_mul_f32_e32 v80, 0x3fb8aa3b, v80
	v_exp_f32_e32 v3, v3
	v_exp_f32_e32 v80, v80
	v_add_f32_dpp v157, v157, v157 row_shr:1 row_mask:0xf bank_mask:0xf bound_ctrl:1
	v_add_f32_dpp v158, v158, v158 row_shr:1 row_mask:0xf bank_mask:0xf bound_ctrl:1
	v_sub_f32_e32 v77, 1.0, v77
	v_add_f32_dpp v157, v157, v157 row_shr:2 row_mask:0xf bank_mask:0xf bound_ctrl:1
	v_add_f32_dpp v158, v158, v158 row_shr:2 row_mask:0xf bank_mask:0xf bound_ctrl:1
	v_add_f32_dpp v160, v160, v160 row_shr:1 row_mask:0xf bank_mask:0xf bound_ctrl:1
	v_add_f32_dpp v162, v162, v162 row_shr:1 row_mask:0xf bank_mask:0xf bound_ctrl:1
	v_add_f32_dpp v157, v157, v157 row_shr:4 row_mask:0xf bank_mask:0xf bound_ctrl:1
	v_add_f32_dpp v158, v158, v158 row_shr:4 row_mask:0xf bank_mask:0xf bound_ctrl:1
	v_add_f32_dpp v160, v160, v160 row_shr:2 row_mask:0xf bank_mask:0xf bound_ctrl:1
	v_add_f32_dpp v162, v162, v162 row_shr:2 row_mask:0xf bank_mask:0xf bound_ctrl:1
	v_mul_f32_e32 v0, v76, v0
	v_mul_f32_e32 v1, v77, v1
	v_add_f32_dpp v157, v157, v157 row_shr:8 row_mask:0xf bank_mask:0xf bound_ctrl:1
	v_add_f32_dpp v158, v158, v158 row_shr:8 row_mask:0xf bank_mask:0xf bound_ctrl:1
	v_add_f32_dpp v160, v160, v160 row_shr:4 row_mask:0xf bank_mask:0xf bound_ctrl:1
	v_add_f32_dpp v162, v162, v162 row_shr:4 row_mask:0xf bank_mask:0xf bound_ctrl:1
	v_mul_f32_e32 v3, v153, v3
	v_mul_f32_e32 v76, v155, v80
	v_cvt_pk_bf16_f32 v0, v0, v1
	v_cvt_pk_bf16_f32 v1, v3, v76
	v_add_f32_dpp v160, v160, v160 row_shr:8 row_mask:0xf bank_mask:0xf bound_ctrl:1
	v_add_f32_dpp v162, v162, v162 row_shr:8 row_mask:0xf bank_mask:0xf bound_ctrl:1
	ds_write_b64 v143, v[0:1] offset:34848
	v_sub_f32_e32 v0, v137, v157
	v_sub_f32_e32 v1, v136, v158
	v_mul_f32_e32 v0, 0x3fb8aa3b, v0
	v_mul_f32_e32 v1, 0x3fb8aa3b, v1
	v_sub_f32_e32 v3, v135, v160
	v_sub_f32_e32 v76, v134, v162
	v_exp_f32_e32 v0, v0
	v_exp_f32_e32 v1, v1
	v_mul_f32_e32 v3, 0x3fb8aa3b, v3
	v_mul_f32_e32 v76, 0x3fb8aa3b, v76
	v_exp_f32_e32 v3, v3
	v_exp_f32_e32 v76, v76
	v_add_f32_dpp v163, v163, v163 row_shr:1 row_mask:0xf bank_mask:0xf bound_ctrl:1
	v_sub_f32_e32 v72, 1.0, v72
	v_sub_f32_e32 v73, 1.0, v73
	v_add_f32_dpp v163, v163, v163 row_shr:2 row_mask:0xf bank_mask:0xf bound_ctrl:1
	v_pk_add_f32 v[108:109], v[108:109], v[74:75]
	v_mul_f32_e32 v75, 0x3fb8aa3b, v75
	v_add_f32_dpp v163, v163, v163 row_shr:4 row_mask:0xf bank_mask:0xf bound_ctrl:1
	v_mul_f32_e32 v0, v72, v0
	v_mul_f32_e32 v1, v73, v1
	v_exp_f32_e32 v150, v75
	v_mul_f32_e32 v74, 0x3fb8aa3b, v74
	v_mul_f32_e32 v75, 0x3fb8aa3b, v79
	v_add_f32_dpp v163, v163, v163 row_shr:8 row_mask:0xf bank_mask:0xf bound_ctrl:1
	v_mul_f32_e32 v3, v159, v3
	v_mul_f32_e32 v72, v161, v76
	v_cvt_pk_bf16_f32 v0, v0, v1
	v_cvt_pk_bf16_f32 v1, v3, v72
	v_exp_f32_e32 v160, v75
	v_mul_f32_e32 v75, 0x3fb8aa3b, v78
	v_exp_f32_e32 v151, v74
	ds_write_b64 v143, v[0:1] offset:34880
	v_sub_f32_e32 v0, v133, v163
	v_sub_f32_e32 v1, v132, v167
	v_exp_f32_e32 v161, v75
	v_mul_f32_e32 v0, 0x3fb8aa3b, v0
	v_mul_f32_e32 v1, 0x3fb8aa3b, v1
	v_sub_f32_e32 v3, v131, v165
	v_sub_f32_e32 v72, v130, v168
	v_exp_f32_e32 v0, v0
	v_exp_f32_e32 v1, v1
	v_mul_f32_e32 v3, 0x3fb8aa3b, v3
	v_mul_f32_e32 v72, 0x3fb8aa3b, v72
	v_exp_f32_e32 v3, v3
	v_exp_f32_e32 v72, v72
	v_pk_mul_f32 v[64:65], v[64:65], v[150:151]
	v_pk_mul_f32 v[60:61], v[60:61], v[150:151]
	v_pk_mul_f32 v[52:53], v[52:53], v[150:151]
	v_pk_mul_f32 v[56:57], v[56:57], v[150:151]
	v_mul_f32_e32 v150, 0x3fb8aa3b, v139
	v_mul_f32_e32 v151, 0x3fb8aa3b, v71
	v_pk_mul_f32 v[66:67], v[66:67], v[160:161]
	v_pk_mul_f32 v[62:63], v[62:63], v[160:161]
	v_pk_mul_f32 v[54:55], v[54:55], v[160:161]
	v_pk_mul_f32 v[58:59], v[58:59], v[160:161]
	v_exp_f32_e32 v160, v150
	v_mul_f32_e32 v150, 0x3fb8aa3b, v138
	v_exp_f32_e32 v162, v151
	v_mul_f32_e32 v151, 0x3fb8aa3b, v70
	v_sub_f32_e32 v68, 1.0, v68
	v_mov_b32_e32 v158, v2
	v_mov_b32_e32 v159, v2
	v_mov_b32_e32 v154, v2
	v_mov_b32_e32 v155, v2
	v_exp_f32_e32 v163, v151
	v_exp_f32_e32 v161, v150
	v_pk_add_f32 v[104:105], v[104:105], v[138:139]
	v_mul_f32_e32 v138, 0x3fb8aa3b, v137
	v_mul_f32_e32 v139, 0x3fb8aa3b, v136
	v_sub_f32_e32 v69, 1.0, v69
	v_mul_f32_e32 v0, v68, v0
	v_mul_f32_e32 v1, v164, v1
	v_exp_f32_e32 v138, v138
	v_exp_f32_e32 v139, v139
	v_mul_f32_e32 v3, v69, v3
	v_mul_f32_e32 v68, v166, v72
	v_cvt_pk_bf16_f32 v0, v0, v1
	v_cvt_pk_bf16_f32 v1, v3, v68
	ds_write_b64 v143, v[0:1] offset:34912
	s_waitcnt lgkmcnt(0)
; template <bool WITHO, bool RAW = false>
; __device__ __forceinline__ void hg_pass(const Frame& F, const bf16_t* P, const float* lbh, int b, int h, int nb, int dir, f32x4 (&S)[4][4], float (&Gsum)[16],
;                                         LAS bf16_t* Vl, LAS bf16_t* Kl, float* OF, const float* ngp) {
;     ...
;         asm volatile("s_waitcnt lgkmcnt(0)" ::: "memory");
;         u32x2 vtr[4], ktr[4];
;         asm volatile("ds_read_b64_tr_b16 %0, %8\n\tds_read_b64_tr_b16 %1, %8 offset:32\n\tds_read_b64_tr_b16 %2, %8 offset:64\n\tds_read_b64_tr_b16 %3, %8 offset:96\n\t"
;                      "ds_read_b64_tr_b16 %4, %9\n\tds_read_b64_tr_b16 %5, %9 offset:32\n\tds_read_b64_tr_b16 %6, %9 offset:64\n\tds_read_b64_tr_b16 %7, %9 offset:96\n\ts_waitcnt lgkmcnt(0)"
;                      : "=&v"(vtr[0]), "=&v"(vtr[1]), "=&v"(vtr[2]), "=&v"(vtr[3]), "=&v"(ktr[0]), "=&v"(ktr[1]), "=&v"(ktr[2]), "=&v"(ktr[3]) : "v"(vaddr), "v"(kaddr) : "memory");
;         bf16x8 Vf[4], Kf[4];
; #pragma unroll
;         for (int q = 0; q < 4; ++q) { u32x4 w; w.x = vtr[q].x; w.y = vtr[q].y; w.z = 0u; w.w = 0u; __builtin_memcpy(&Vf[q], &w, 16); u32x4 w2; w2.x = ktr[q].x; w2.y = ktr[q].y; w2.z = 0u; w2.w = 0u; __builtin_memcpy(&Kf[q], &w2, 16); }
;     ...
; #pragma unroll
;         for (int kt = 0; kt < 4; ++kt) { f32x4 eg;
; #pragma unroll
;             for (int i = 0; i < 4; ++i) eg[i] = __expf(G[kt * 4 + i]);
; #pragma unroll
;             for (int vt = 0; vt < 4; ++vt) S[kt][vt] = __builtin_amdgcn_mfma_f32_16x16x32_bf16(Kf[kt], Vf[vt], S[kt][vt] * eg, 0, 0, 0); }
	v_pk_add_f32 v[106:107], v[106:107], v[78:79]
	ds_read_b64_tr_b16 v[0:1], v140
	ds_read_b64_tr_b16 v[80:81], v140 offset:32
	ds_read_b64_tr_b16 v[76:77], v140 offset:64
	ds_read_b64_tr_b16 v[72:73], v140 offset:96
	ds_read_b64_tr_b16 v[156:157], v141
	ds_read_b64_tr_b16 v[152:153], v141 offset:32
	ds_read_b64_tr_b16 v[148:149], v141 offset:64
	ds_read_b64_tr_b16 v[68:69], v141 offset:96
	s_waitcnt lgkmcnt(0)
	v_mov_b32_e32 v3, v2
	v_mov_b32_e32 v82, v2
	v_mov_b32_e32 v83, v2
	v_mov_b32_e32 v78, v2
	v_mov_b32_e32 v79, v2
	v_mov_b32_e32 v74, v2
	v_mov_b32_e32 v75, v2
	v_pk_mul_f32 v[50:51], v[50:51], v[162:163]
	v_pk_mul_f32 v[48:49], v[48:49], v[160:161]
	v_pk_mul_f32 v[46:47], v[46:47], v[162:163]
	v_pk_mul_f32 v[44:45], v[44:45], v[160:161]
	v_pk_mul_f32 v[38:39], v[38:39], v[162:163]
	v_pk_mul_f32 v[36:37], v[36:37], v[160:161]
	v_pk_mul_f32 v[42:43], v[42:43], v[162:163]
	v_pk_mul_f32 v[40:41], v[40:41], v[160:161]
	v_mfma_f32_16x16x32_bf16 v[64:67], v[156:159], v[0:3], v[64:67]
	v_mul_f32_e64 v32, v32, v138
	v_mul_f32_e64 v33, v33, v139
	v_pk_mul_f32 v[28:29], v[28:29], v[138:139]
	v_pk_mul_f32 v[20:21], v[20:21], v[138:139]
	v_mfma_f32_16x16x32_bf16 v[60:63], v[156:159], v[80:83], v[60:63]
	v_mul_f32_e64 v24, v24, v138
	v_mul_f32_e64 v25, v25, v139
	v_mul_f32_e32 v138, 0x3fb8aa3b, v133
	v_mul_f32_e32 v139, 0x3fb8aa3b, v132
	v_mfma_f32_16x16x32_bf16 v[52:55], v[156:159], v[76:79], v[52:55]
	v_mov_b32_e32 v150, v2
	v_mov_b32_e32 v151, v2
	v_pk_add_f32 v[102:103], v[102:103], v[70:71]
	v_mfma_f32_16x16x32_bf16 v[56:59], v[156:159], v[72:75], v[56:59]
	v_mul_f32_e32 v156, 0x3fb8aa3b, v135
	v_mul_f32_e32 v157, 0x3fb8aa3b, v134
	v_exp_f32_e32 v156, v156
	v_mfma_f32_16x16x32_bf16 v[48:51], v[152:155], v[0:3], v[48:51]
	v_exp_f32_e32 v157, v157
	v_mov_b32_e32 v70, v2
	v_mov_b32_e32 v71, v2
	v_mfma_f32_16x16x32_bf16 v[44:47], v[152:155], v[80:83], v[44:47]
	v_exp_f32_e32 v138, v138
	v_exp_f32_e32 v139, v139
	v_pk_mul_f32 v[34:35], v[34:35], v[156:157]
	v_mfma_f32_16x16x32_bf16 v[36:39], v[152:155], v[76:79], v[36:39]
	v_mul_f32_e64 v30, v30, v156
	v_mul_f32_e64 v31, v31, v157
	v_pk_mul_f32 v[22:23], v[22:23], v[156:157]
	v_pk_mul_f32 v[26:27], v[26:27], v[156:157]
	v_mfma_f32_16x16x32_bf16 v[40:43], v[152:155], v[72:75], v[40:43]
	v_mul_f32_e32 v152, 0x3fb8aa3b, v131
	v_mul_f32_e32 v153, 0x3fb8aa3b, v130
	v_exp_f32_e32 v152, v152
	v_exp_f32_e32 v153, v153
	v_pk_mul_f32 v[16:17], v[16:17], v[138:139]
	v_pk_mul_f32 v[12:13], v[12:13], v[138:139]
	v_pk_mul_f32 v[8:9], v[8:9], v[138:139]
	v_pk_mul_f32 v[18:19], v[18:19], v[152:153]
	v_pk_mul_f32 v[14:15], v[14:15], v[152:153]
	v_pk_mul_f32 v[10:11], v[10:11], v[152:153]
	v_pk_mul_f32 v[6:7], v[6:7], v[152:153]
	v_pk_mul_f32 v[4:5], v[4:5], v[138:139]
	v_mfma_f32_16x16x32_bf16 v[32:35], v[148:151], v[0:3], v[32:35]
	v_add_f32_e64 v100, v100, v136
	v_add_f32_e64 v101, v101, v137
	v_pk_add_f32 v[98:99], v[98:99], v[134:135]
	v_pk_add_f32 v[96:97], v[96:97], v[132:133]
	v_mfma_f32_16x16x32_bf16 v[28:31], v[148:151], v[80:83], v[28:31]
	v_add_f32_e64 v94, v94, v130
	v_add_f32_e64 v95, v95, v131
	v_mov_b64_e32 v[134:135], v[122:123]
	v_mov_b64_e32 v[132:133], v[124:125]
	v_mfma_f32_16x16x32_bf16 v[20:23], v[148:151], v[76:79], v[20:23]
	v_mov_b64_e32 v[130:131], v[126:127]
	v_mfma_f32_16x16x32_bf16 v[24:27], v[148:151], v[72:75], v[24:27]
	v_mfma_f32_16x16x32_bf16 v[16:19], v[68:71], v[0:3], v[16:19]
	v_mov_b64_e32 v[0:1], v[128:129]
	v_mfma_f32_16x16x32_bf16 v[12:15], v[68:71], v[80:83], v[12:15]
	v_mfma_f32_16x16x32_bf16 v[8:11], v[68:71], v[76:79], v[8:11]
	v_mfma_f32_16x16x32_bf16 v[4:7], v[68:71], v[72:75], v[4:7]
	s_cbranch_scc0 .LBB0_692

; __device__ __forceinline__ void ph_lru_c(const Frame& F) {
;     ...
;     for (int task = gw; task < NBAT * LRU_NT * 16; task += nw) {
;         const int kb = task & 15, nt = (task >> 4) % LRU_NT, b = (task >> 4) / LRU_NT;
;         const int row = lru_row(b, nt, tk);
;         u32x4 gx[2][4]; f32x4 hf[4], hb[4]; u32x2 yw[4];
; #pragma unroll
;         for (int d = 0; d < 2; ++d)
; #pragma unroll
;             for (int et = 0; et < 4; ++et) gx[d][et] = *(const u32x4*)(GX + (((size_t)row * 2 + d) * 1024 + kb * 64 + et * 16 + 4 * g) * 2);
; #pragma unroll
;         for (int et = 0; et < 4; ++et) { const int ch = kb * 64 + et * 16 + 4 * g;
;             hf[et] = *(const f32x4*)(HST + ((size_t)(b * 2 + 0) * LRU_NT + nt) * 1024 + ch);
;             hb[et] = *(const f32x4*)(HST + ((size_t)(b * 2 + 1) * LRU_NT + nt) * 1024 + ch);
;             yw[et] = *(const u32x2*)(P + (size_t)row * 2048 + ch); }
;         float av[2][4][4], xv[2][4][4];
; #pragma unroll
;         for (int d = 0; d < 2; ++d)
; #pragma unroll
;             for (int et = 0; et < 4; ++et) { const unsigned ww[4] = {gx[d][et].x, gx[d][et].y, gx[d][et].z, gx[d][et].w};
; #pragma unroll
;                 for (int i = 0; i < 4; ++i) { av[d][et][i] = __expf(__uint_as_float(ww[i] << 16)); xv[d][et][i] = __uint_as_float(ww[i] & 0xffff0000u); } }
.LBB0_1153:
	s_waitcnt vmcnt(0)
	v_or_b32_e32 v4, s8, v3
	v_ashrrev_i32_e32 v5, 31, v4
	s_and_b32 s64, s2, 0x3c0
	v_lshlrev_b64 v[70:71], 11, v[4:5]
	v_lshl_add_u64 v[6:7], s[64:65], 0, v[0:1]
	v_lshl_add_u64 v[6:7], v[6:7], 0, v[70:71]
	v_lshl_add_u64 v[6:7], v[6:7], 2, s[10:11]
	global_load_dwordx4 v[64:67], v[6:7], off
	global_load_dwordx4 v[60:63], v[6:7], off offset:64
	global_load_dwordx4 v[56:59], v[6:7], off offset:128
	global_load_dwordx4 v[52:55], v[6:7], off offset:192
	v_add_co_u32_e32 v6, vcc, s97, v6
	s_mulk_i32 s6, 0x420
	s_nop 0
	v_addc_co_u32_e32 v7, vcc, 0, v7, vcc
	global_load_dwordx4 v[48:51], v[6:7], off
	global_load_dwordx4 v[44:47], v[6:7], off offset:64
	global_load_dwordx4 v[40:43], v[6:7], off offset:128
	global_load_dwordx4 v[36:39], v[6:7], off offset:192
	s_add_i32 s0, s6, s5
	s_ashr_i32 s1, s0, 31
	s_ashr_i32 s7, s5, 31
	s_lshl_b64 s[0:1], s[0:1], 12
	s_add_u32 s0, s23, s0
	v_readlane_b32 s9, v251, 48
	s_addc_u32 s1, s9, s1
	s_addk_i32 s6, 0x210
	s_ashr_i32 s8, s6, 31
	s_add_u32 s6, s6, s5
	s_addc_u32 s7, s8, s7
	v_add_u32_e32 v6, s64, v0
	s_lshl_b64 s[6:7], s[6:7], 12
	s_add_u32 s6, s23, s6
	v_ashrrev_i32_e32 v7, 31, v6
	s_addc_u32 s7, s9, s7
	v_lshlrev_b64 v[8:9], 2, v[6:7]
	v_lshl_add_u64 v[10:11], s[0:1], 0, v[8:9]
	v_lshl_add_u64 v[8:9], s[6:7], 0, v[8:9]
	global_load_dwordx4 v[28:31], v[10:11], off
	global_load_dwordx4 v[32:35], v[8:9], off
	v_lshlrev_b64 v[4:5], 12, v[4:5]
	v_lshl_add_u64 v[4:5], s[82:83], 0, v[4:5]
	v_lshlrev_b64 v[74:75], 1, v[6:7]
	v_lshl_add_u64 v[68:69], v[4:5], 0, v[74:75]
	global_load_dwordx2 v[108:109], v[68:69], off
	global_load_dwordx4 v[20:23], v[10:11], off offset:64
	global_load_dwordx4 v[24:27], v[8:9], off offset:64
	global_load_dwordx2 v[76:77], v[68:69], off offset:32
	global_load_dwordx4 v[12:15], v[10:11], off offset:128
	global_load_dwordx4 v[16:19], v[8:9], off offset:128
	global_load_dwordx2 v[72:73], v[68:69], off offset:64
	global_load_dwordx4 v[4:7], v[10:11], off offset:192
	s_nop 0
	global_load_dwordx4 v[8:11], v[8:9], off offset:192
	s_nop 0
	global_load_dwordx2 v[68:69], v[68:69], off offset:96
	v_readlane_b32 s0, v251, 53
	s_add_i32 s4, s4, s80
	s_add_i32 s2, s2, s0
	s_cmp_lt_i32 s4, 0x8400
	s_waitcnt vmcnt(0)
	v_lshlrev_b32_e32 v78, 16, v64
	v_and_b32_e32 v118, 0xffff0000, v64
	v_lshlrev_b32_e32 v64, 16, v65
	v_mul_f32_e32 v64, 0x3fb8aa3b, v64
	v_exp_f32_e32 v114, v64
	v_lshlrev_b32_e32 v64, 16, v66
	v_mul_f32_e32 v64, 0x3fb8aa3b, v64
	v_exp_f32_e32 v116, v64
	v_lshlrev_b32_e32 v64, 16, v67
	v_mul_f32_e32 v64, 0x3fb8aa3b, v64
	v_exp_f32_e32 v122, v64
	v_lshlrev_b32_e32 v64, 16, v60
	v_and_b32_e32 v100, 0xffff0000, v60
	v_lshlrev_b32_e32 v60, 16, v61
	v_mul_f32_e32 v60, 0x3fb8aa3b, v60
	v_exp_f32_e32 v96, v60
	v_lshlrev_b32_e32 v60, 16, v62
	v_mul_f32_e32 v60, 0x3fb8aa3b, v60
	v_exp_f32_e32 v98, v60
	v_lshlrev_b32_e32 v60, 16, v63
	v_mul_f32_e32 v60, 0x3fb8aa3b, v60
	v_exp_f32_e32 v104, v60
	v_lshlrev_b32_e32 v60, 16, v56
	v_and_b32_e32 v92, 0xffff0000, v56
	v_lshlrev_b32_e32 v56, 16, v57
	v_mul_f32_e32 v56, 0x3fb8aa3b, v56
	v_exp_f32_e32 v86, v56
	v_lshlrev_b32_e32 v56, 16, v58
	v_mul_f32_e32 v78, 0x3fb8aa3b, v78
	v_mul_f32_e32 v56, 0x3fb8aa3b, v56
	v_exp_f32_e32 v112, v78
	v_exp_f32_e32 v78, v56
	v_lshlrev_b32_e32 v56, 16, v59
	v_mul_f32_e32 v56, 0x3fb8aa3b, v56
	v_and_b32_e32 v124, 0xffff0000, v66
	v_and_b32_e32 v106, 0xffff0000, v62
	v_exp_f32_e32 v80, v56
	v_lshlrev_b32_e32 v56, 16, v52
	v_and_b32_e32 v66, 0xffff0000, v52
	v_lshlrev_b32_e32 v52, 16, v53
	v_and_b32_e32 v62, 0xffff0000, v53
	v_lshlrev_b32_e32 v53, 16, v55
	v_mul_f32_e32 v64, 0x3fb8aa3b, v64
	v_mul_f32_e32 v60, 0x3fb8aa3b, v60
	v_mul_f32_e32 v56, 0x3fb8aa3b, v56
	v_mul_f32_e32 v52, 0x3fb8aa3b, v52
	v_mul_f32_e32 v53, 0x3fb8aa3b, v53
	v_exp_f32_e32 v94, v64
	v_exp_f32_e32 v90, v60
	v_exp_f32_e32 v64, v56
	v_exp_f32_e32 v60, v52
	v_lshlrev_b32_e32 v52, 16, v54
	v_and_b32_e32 v56, 0xffff0000, v54
	v_exp_f32_e32 v54, v53
	v_lshlrev_b32_e32 v53, 16, v48
	v_and_b32_e32 v119, 0xffff0000, v48
	v_lshlrev_b32_e32 v48, 16, v49
	v_mul_f32_e32 v48, 0x3fb8aa3b, v48
	v_exp_f32_e32 v115, v48
	v_lshlrev_b32_e32 v48, 16, v50
	v_mul_f32_e32 v48, 0x3fb8aa3b, v48
	v_exp_f32_e32 v117, v48
	v_lshlrev_b32_e32 v48, 16, v51
	v_mul_f32_e32 v48, 0x3fb8aa3b, v48
	v_exp_f32_e32 v123, v48
	v_lshlrev_b32_e32 v48, 16, v44
	v_and_b32_e32 v101, 0xffff0000, v44
	v_lshlrev_b32_e32 v44, 16, v45
	v_mul_f32_e32 v44, 0x3fb8aa3b, v44
	v_exp_f32_e32 v97, v44
	v_lshlrev_b32_e32 v44, 16, v46
	v_mul_f32_e32 v44, 0x3fb8aa3b, v44
	v_exp_f32_e32 v99, v44
	v_lshlrev_b32_e32 v44, 16, v47
	v_mul_f32_e32 v44, 0x3fb8aa3b, v44
	v_exp_f32_e32 v105, v44
	v_lshlrev_b32_e32 v44, 16, v40
	v_and_b32_e32 v93, 0xffff0000, v40
	v_lshlrev_b32_e32 v40, 16, v41
	v_mul_f32_e32 v40, 0x3fb8aa3b, v40
	v_exp_f32_e32 v87, v40
	v_lshlrev_b32_e32 v40, 16, v42
	v_mul_f32_e32 v40, 0x3fb8aa3b, v40
	v_exp_f32_e32 v79, v40
	v_lshlrev_b32_e32 v40, 16, v43
	v_mul_f32_e32 v40, 0x3fb8aa3b, v40
	v_and_b32_e32 v126, 0xffff0000, v67
	v_exp_f32_e32 v81, v40
	v_lshlrev_b32_e32 v40, 16, v36
	v_and_b32_e32 v67, 0xffff0000, v36
	v_lshlrev_b32_e32 v36, 16, v37
	v_mul_f32_e32 v36, 0x3fb8aa3b, v36
	v_and_b32_e32 v102, 0xffff0000, v61
	v_exp_f32_e32 v61, v36
	v_lshlrev_b32_e32 v36, 16, v38
	v_mul_f32_e32 v53, 0x3fb8aa3b, v53
	v_mul_f32_e32 v36, 0x3fb8aa3b, v36
	v_exp_f32_e32 v113, v53
	v_exp_f32_e32 v53, v36
	v_lshlrev_b32_e32 v36, 16, v39
	v_and_b32_e32 v120, 0xffff0000, v65
	v_mul_f32_e32 v52, 0x3fb8aa3b, v52
	v_and_b32_e32 v121, 0xffff0000, v49
	s_waitcnt lgkmcnt(0)
; __device__ __forceinline__ void ph_lru_c(const Frame& F) {
;     ...
;         float av[2][4][4], xv[2][4][4];
; #pragma unroll
;         for (int d = 0; d < 2; ++d)
; #pragma unroll
;             for (int et = 0; et < 4; ++et) { const unsigned ww[4] = {gx[d][et].x, gx[d][et].y, gx[d][et].z, gx[d][et].w};
; #pragma unroll
;                 for (int i = 0; i < 4; ++i) { av[d][et][i] = __expf(__uint_as_float(ww[i] << 16)); xv[d][et][i] = __uint_as_float(ww[i] & 0xffff0000u); } }
;         LRU_SCANS(av, xv);
	v_and_b32_e32 v125, 0xffff0000, v50
	v_and_b32_e32 v127, 0xffff0000, v51
	v_mul_f32_e32 v48, 0x3fb8aa3b, v48
	v_mul_f32_e32 v44, 0x3fb8aa3b, v44
	v_mul_f32_e32 v40, 0x3fb8aa3b, v40
	v_mul_f32_e32 v36, 0x3fb8aa3b, v36
	v_and_b32_e32 v110, 0xffff0000, v63
	v_and_b32_e32 v88, 0xffff0000, v57
	v_and_b32_e32 v82, 0xffff0000, v58
	v_and_b32_e32 v84, 0xffff0000, v59
	v_exp_f32_e32 v52, v52
	v_and_b32_e32 v58, 0xffff0000, v55
	v_exp_f32_e32 v95, v48
	v_and_b32_e32 v103, 0xffff0000, v45
	v_and_b32_e32 v107, 0xffff0000, v46
	v_and_b32_e32 v111, 0xffff0000, v47
	v_exp_f32_e32 v91, v44
	v_and_b32_e32 v89, 0xffff0000, v41
	v_and_b32_e32 v83, 0xffff0000, v42
	v_and_b32_e32 v85, 0xffff0000, v43
	v_exp_f32_e32 v65, v40
	v_and_b32_e32 v63, 0xffff0000, v37
	v_and_b32_e32 v57, 0xffff0000, v38
	v_exp_f32_e32 v55, v36
	v_and_b32_e32 v59, 0xffff0000, v39
	v_fmac_f32_dpp v118, v118, v112 row_shr:1 row_mask:0xf bank_mask:0xf
	v_fmac_f32_dpp v120, v120, v114 row_shr:1 row_mask:0xf bank_mask:0xf
	v_fmac_f32_dpp v124, v124, v116 row_shr:1 row_mask:0xf bank_mask:0xf
	v_fmac_f32_dpp v126, v126, v122 row_shr:1 row_mask:0xf bank_mask:0xf
	v_mul_f32_dpp v112, v112, v112 row_shr:1 row_mask:0xf bank_mask:0xf
	v_mul_f32_dpp v114, v114, v114 row_shr:1 row_mask:0xf bank_mask:0xf
	v_mul_f32_dpp v116, v116, v116 row_shr:1 row_mask:0xf bank_mask:0xf
	v_mul_f32_dpp v122, v122, v122 row_shr:1 row_mask:0xf bank_mask:0xf
	v_fmac_f32_dpp v119, v119, v113 row_shl:1 row_mask:0xf bank_mask:0xf
	v_fmac_f32_dpp v121, v121, v115 row_shl:1 row_mask:0xf bank_mask:0xf
	v_fmac_f32_dpp v125, v125, v117 row_shl:1 row_mask:0xf bank_mask:0xf
	v_fmac_f32_dpp v127, v127, v123 row_shl:1 row_mask:0xf bank_mask:0xf
	v_mul_f32_dpp v113, v113, v113 row_shl:1 row_mask:0xf bank_mask:0xf
	v_mul_f32_dpp v115, v115, v115 row_shl:1 row_mask:0xf bank_mask:0xf
	v_mul_f32_dpp v117, v117, v117 row_shl:1 row_mask:0xf bank_mask:0xf
	v_mul_f32_dpp v123, v123, v123 row_shl:1 row_mask:0xf bank_mask:0xf
	v_fmac_f32_dpp v100, v100, v94 row_shr:1 row_mask:0xf bank_mask:0xf
	v_fmac_f32_dpp v102, v102, v96 row_shr:1 row_mask:0xf bank_mask:0xf
	v_fmac_f32_dpp v106, v106, v98 row_shr:1 row_mask:0xf bank_mask:0xf
	v_fmac_f32_dpp v110, v110, v104 row_shr:1 row_mask:0xf bank_mask:0xf
	v_mul_f32_dpp v94, v94, v94 row_shr:1 row_mask:0xf bank_mask:0xf
	v_mul_f32_dpp v96, v96, v96 row_shr:1 row_mask:0xf bank_mask:0xf
	v_mul_f32_dpp v98, v98, v98 row_shr:1 row_mask:0xf bank_mask:0xf
	v_mul_f32_dpp v104, v104, v104 row_shr:1 row_mask:0xf bank_mask:0xf
	v_fmac_f32_dpp v101, v101, v95 row_shl:1 row_mask:0xf bank_mask:0xf
	v_fmac_f32_dpp v103, v103, v97 row_shl:1 row_mask:0xf bank_mask:0xf
	v_fmac_f32_dpp v107, v107, v99 row_shl:1 row_mask:0xf bank_mask:0xf
	v_fmac_f32_dpp v111, v111, v105 row_shl:1 row_mask:0xf bank_mask:0xf
	v_mul_f32_dpp v95, v95, v95 row_shl:1 row_mask:0xf bank_mask:0xf
	v_mul_f32_dpp v97, v97, v97 row_shl:1 row_mask:0xf bank_mask:0xf
	v_mul_f32_dpp v99, v99, v99 row_shl:1 row_mask:0xf bank_mask:0xf
	v_mul_f32_dpp v105, v105, v105 row_shl:1 row_mask:0xf bank_mask:0xf
	v_fmac_f32_dpp v92, v92, v90 row_shr:1 row_mask:0xf bank_mask:0xf
	v_fmac_f32_dpp v88, v88, v86 row_shr:1 row_mask:0xf bank_mask:0xf
	v_fmac_f32_dpp v82, v82, v78 row_shr:1 row_mask:0xf bank_mask:0xf
	v_fmac_f32_dpp v84, v84, v80 row_shr:1 row_mask:0xf bank_mask:0xf
	v_mul_f32_dpp v90, v90, v90 row_shr:1 row_mask:0xf bank_mask:0xf
	v_mul_f32_dpp v86, v86, v86 row_shr:1 row_mask:0xf bank_mask:0xf
	v_mul_f32_dpp v78, v78, v78 row_shr:1 row_mask:0xf bank_mask:0xf
	v_mul_f32_dpp v80, v80, v80 row_shr:1 row_mask:0xf bank_mask:0xf
	v_fmac_f32_dpp v93, v93, v91 row_shl:1 row_mask:0xf bank_mask:0xf
	v_fmac_f32_dpp v89, v89, v87 row_shl:1 row_mask:0xf bank_mask:0xf
	v_fmac_f32_dpp v83, v83, v79 row_shl:1 row_mask:0xf bank_mask:0xf
	v_fmac_f32_dpp v85, v85, v81 row_shl:1 row_mask:0xf bank_mask:0xf
	v_mul_f32_dpp v91, v91, v91 row_shl:1 row_mask:0xf bank_mask:0xf
	v_mul_f32_dpp v87, v87, v87 row_shl:1 row_mask:0xf bank_mask:0xf
	v_mul_f32_dpp v79, v79, v79 row_shl:1 row_mask:0xf bank_mask:0xf
	v_mul_f32_dpp v81, v81, v81 row_shl:1 row_mask:0xf bank_mask:0xf
	v_fmac_f32_dpp v66, v66, v64 row_shr:1 row_mask:0xf bank_mask:0xf
	v_fmac_f32_dpp v62, v62, v60 row_shr:1 row_mask:0xf bank_mask:0xf
	v_fmac_f32_dpp v56, v56, v52 row_shr:1 row_mask:0xf bank_mask:0xf
	v_fmac_f32_dpp v58, v58, v54 row_shr:1 row_mask:0xf bank_mask:0xf
	v_mul_f32_dpp v64, v64, v64 row_shr:1 row_mask:0xf bank_mask:0xf
	v_mul_f32_dpp v60, v60, v60 row_shr:1 row_mask:0xf bank_mask:0xf
	v_mul_f32_dpp v52, v52, v52 row_shr:1 row_mask:0xf bank_mask:0xf
	v_mul_f32_dpp v54, v54, v54 row_shr:1 row_mask:0xf bank_mask:0xf
	v_fmac_f32_dpp v67, v67, v65 row_shl:1 row_mask:0xf bank_mask:0xf
	v_fmac_f32_dpp v63, v63, v61 row_shl:1 row_mask:0xf bank_mask:0xf
	v_fmac_f32_dpp v57, v57, v53 row_shl:1 row_mask:0xf bank_mask:0xf
	v_fmac_f32_dpp v59, v59, v55 row_shl:1 row_mask:0xf bank_mask:0xf
	v_mul_f32_dpp v65, v65, v65 row_shl:1 row_mask:0xf bank_mask:0xf
	v_mul_f32_dpp v61, v61, v61 row_shl:1 row_mask:0xf bank_mask:0xf
	v_mul_f32_dpp v53, v53, v53 row_shl:1 row_mask:0xf bank_mask:0xf
	v_mul_f32_dpp v55, v55, v55 row_shl:1 row_mask:0xf bank_mask:0xf
	s_nop 0
	v_fmac_f32_dpp v118, v118, v112 row_shr:2 row_mask:0xf bank_mask:0xf
	v_fmac_f32_dpp v120, v120, v114 row_shr:2 row_mask:0xf bank_mask:0xf
	v_fmac_f32_dpp v124, v124, v116 row_shr:2 row_mask:0xf bank_mask:0xf
	v_fmac_f32_dpp v126, v126, v122 row_shr:2 row_mask:0xf bank_mask:0xf
	v_mul_f32_dpp v112, v112, v112 row_shr:2 row_mask:0xf bank_mask:0xf
	v_mul_f32_dpp v114, v114, v114 row_shr:2 row_mask:0xf bank_mask:0xf
	v_mul_f32_dpp v116, v116, v116 row_shr:2 row_mask:0xf bank_mask:0xf
	v_mul_f32_dpp v122, v122, v122 row_shr:2 row_mask:0xf bank_mask:0xf
	v_fmac_f32_dpp v119, v119, v113 row_shl:2 row_mask:0xf bank_mask:0xf
	v_fmac_f32_dpp v121, v121, v115 row_shl:2 row_mask:0xf bank_mask:0xf
	v_fmac_f32_dpp v125, v125, v117 row_shl:2 row_mask:0xf bank_mask:0xf
	v_fmac_f32_dpp v127, v127, v123 row_shl:2 row_mask:0xf bank_mask:0xf
	v_mul_f32_dpp v113, v113, v113 row_shl:2 row_mask:0xf bank_mask:0xf
	v_mul_f32_dpp v115, v115, v115 row_shl:2 row_mask:0xf bank_mask:0xf
	v_mul_f32_dpp v117, v117, v117 row_shl:2 row_mask:0xf bank_mask:0xf
	v_mul_f32_dpp v123, v123, v123 row_shl:2 row_mask:0xf bank_mask:0xf
	v_fmac_f32_dpp v100, v100, v94 row_shr:2 row_mask:0xf bank_mask:0xf
	v_fmac_f32_dpp v102, v102, v96 row_shr:2 row_mask:0xf bank_mask:0xf
	v_fmac_f32_dpp v106, v106, v98 row_shr:2 row_mask:0xf bank_mask:0xf
	v_fmac_f32_dpp v110, v110, v104 row_shr:2 row_mask:0xf bank_mask:0xf
	v_mul_f32_dpp v94, v94, v94 row_shr:2 row_mask:0xf bank_mask:0xf
	v_mul_f32_dpp v96, v96, v96 row_shr:2 row_mask:0xf bank_mask:0xf
	v_mul_f32_dpp v98, v98, v98 row_shr:2 row_mask:0xf bank_mask:0xf
	v_mul_f32_dpp v104, v104, v104 row_shr:2 row_mask:0xf bank_mask:0xf
	v_fmac_f32_dpp v101, v101, v95 row_shl:2 row_mask:0xf bank_mask:0xf
	v_fmac_f32_dpp v103, v103, v97 row_shl:2 row_mask:0xf bank_mask:0xf
	v_fmac_f32_dpp v107, v107, v99 row_shl:2 row_mask:0xf bank_mask:0xf
	v_fmac_f32_dpp v111, v111, v105 row_shl:2 row_mask:0xf bank_mask:0xf
	v_mul_f32_dpp v95, v95, v95 row_shl:2 row_mask:0xf bank_mask:0xf
	v_mul_f32_dpp v97, v97, v97 row_shl:2 row_mask:0xf bank_mask:0xf
	v_mul_f32_dpp v99, v99, v99 row_shl:2 row_mask:0xf bank_mask:0xf
	v_mul_f32_dpp v105, v105, v105 row_shl:2 row_mask:0xf bank_mask:0xf
	v_fmac_f32_dpp v92, v92, v90 row_shr:2 row_mask:0xf bank_mask:0xf
	v_fmac_f32_dpp v88, v88, v86 row_shr:2 row_mask:0xf bank_mask:0xf
	v_fmac_f32_dpp v82, v82, v78 row_shr:2 row_mask:0xf bank_mask:0xf
	v_fmac_f32_dpp v84, v84, v80 row_shr:2 row_mask:0xf bank_mask:0xf
	v_mul_f32_dpp v90, v90, v90 row_shr:2 row_mask:0xf bank_mask:0xf
	v_mul_f32_dpp v86, v86, v86 row_shr:2 row_mask:0xf bank_mask:0xf
	v_mul_f32_dpp v78, v78, v78 row_shr:2 row_mask:0xf bank_mask:0xf
	v_mul_f32_dpp v80, v80, v80 row_shr:2 row_mask:0xf bank_mask:0xf
	v_fmac_f32_dpp v93, v93, v91 row_shl:2 row_mask:0xf bank_mask:0xf
	v_fmac_f32_dpp v89, v89, v87 row_shl:2 row_mask:0xf bank_mask:0xf
	v_fmac_f32_dpp v83, v83, v79 row_shl:2 row_mask:0xf bank_mask:0xf
	v_fmac_f32_dpp v85, v85, v81 row_shl:2 row_mask:0xf bank_mask:0xf
	v_mul_f32_dpp v91, v91, v91 row_shl:2 row_mask:0xf bank_mask:0xf
	v_mul_f32_dpp v87, v87, v87 row_shl:2 row_mask:0xf bank_mask:0xf
	v_mul_f32_dpp v79, v79, v79 row_shl:2 row_mask:0xf bank_mask:0xf
	v_mul_f32_dpp v81, v81, v81 row_shl:2 row_mask:0xf bank_mask:0xf
	v_fmac_f32_dpp v66, v66, v64 row_shr:2 row_mask:0xf bank_mask:0xf
	v_fmac_f32_dpp v62, v62, v60 row_shr:2 row_mask:0xf bank_mask:0xf
	v_fmac_f32_dpp v56, v56, v52 row_shr:2 row_mask:0xf bank_mask:0xf
	v_fmac_f32_dpp v58, v58, v54 row_shr:2 row_mask:0xf bank_mask:0xf
	v_mul_f32_dpp v64, v64, v64 row_shr:2 row_mask:0xf bank_mask:0xf
	v_mul_f32_dpp v60, v60, v60 row_shr:2 row_mask:0xf bank_mask:0xf
	v_mul_f32_dpp v52, v52, v52 row_shr:2 row_mask:0xf bank_mask:0xf
	v_mul_f32_dpp v54, v54, v54 row_shr:2 row_mask:0xf bank_mask:0xf
	v_fmac_f32_dpp v67, v67, v65 row_shl:2 row_mask:0xf bank_mask:0xf
	v_fmac_f32_dpp v63, v63, v61 row_shl:2 row_mask:0xf bank_mask:0xf
	v_fmac_f32_dpp v57, v57, v53 row_shl:2 row_mask:0xf bank_mask:0xf
	v_fmac_f32_dpp v59, v59, v55 row_shl:2 row_mask:0xf bank_mask:0xf
	v_mul_f32_dpp v65, v65, v65 row_shl:2 row_mask:0xf bank_mask:0xf
	v_mul_f32_dpp v61, v61, v61 row_shl:2 row_mask:0xf bank_mask:0xf
	v_mul_f32_dpp v53, v53, v53 row_shl:2 row_mask:0xf bank_mask:0xf
	v_mul_f32_dpp v55, v55, v55 row_shl:2 row_mask:0xf bank_mask:0xf
	s_nop 0
	v_fmac_f32_dpp v118, v118, v112 row_shr:4 row_mask:0xf bank_mask:0xf
	v_fmac_f32_dpp v120, v120, v114 row_shr:4 row_mask:0xf bank_mask:0xf
	v_fmac_f32_dpp v124, v124, v116 row_shr:4 row_mask:0xf bank_mask:0xf
	v_fmac_f32_dpp v126, v126, v122 row_shr:4 row_mask:0xf bank_mask:0xf
	v_mul_f32_dpp v112, v112, v112 row_shr:4 row_mask:0xf bank_mask:0xf
	v_mul_f32_dpp v114, v114, v114 row_shr:4 row_mask:0xf bank_mask:0xf
	v_mul_f32_dpp v116, v116, v116 row_shr:4 row_mask:0xf bank_mask:0xf
	v_mul_f32_dpp v122, v122, v122 row_shr:4 row_mask:0xf bank_mask:0xf
	v_fmac_f32_dpp v119, v119, v113 row_shl:4 row_mask:0xf bank_mask:0xf
	v_fmac_f32_dpp v121, v121, v115 row_shl:4 row_mask:0xf bank_mask:0xf
	v_fmac_f32_dpp v125, v125, v117 row_shl:4 row_mask:0xf bank_mask:0xf
	v_fmac_f32_dpp v127, v127, v123 row_shl:4 row_mask:0xf bank_mask:0xf
	v_mul_f32_dpp v113, v113, v113 row_shl:4 row_mask:0xf bank_mask:0xf
	v_mul_f32_dpp v115, v115, v115 row_shl:4 row_mask:0xf bank_mask:0xf
	v_mul_f32_dpp v117, v117, v117 row_shl:4 row_mask:0xf bank_mask:0xf
	v_mul_f32_dpp v123, v123, v123 row_shl:4 row_mask:0xf bank_mask:0xf
	v_mov_b32_e32 v37, v32
	v_mov_b32_e32 v32, v29
	v_fmac_f32_dpp v100, v100, v94 row_shr:4 row_mask:0xf bank_mask:0xf
	v_fmac_f32_dpp v102, v102, v96 row_shr:4 row_mask:0xf bank_mask:0xf
	v_fmac_f32_dpp v106, v106, v98 row_shr:4 row_mask:0xf bank_mask:0xf
	v_fmac_f32_dpp v110, v110, v104 row_shr:4 row_mask:0xf bank_mask:0xf
	v_mul_f32_dpp v94, v94, v94 row_shr:4 row_mask:0xf bank_mask:0xf
	v_mul_f32_dpp v96, v96, v96 row_shr:4 row_mask:0xf bank_mask:0xf
	v_mul_f32_dpp v98, v98, v98 row_shr:4 row_mask:0xf bank_mask:0xf
	v_mul_f32_dpp v104, v104, v104 row_shr:4 row_mask:0xf bank_mask:0xf
	v_fmac_f32_dpp v101, v101, v95 row_shl:4 row_mask:0xf bank_mask:0xf
; __device__ __forceinline__ unsigned cvt_pk_bf16(float lo, float hi) { unsigned r; asm volatile("v_cvt_pk_bf16_f32 %0, %1, %2" : "=v"(r) : "v"(lo), "v"(hi)); return r; }
; __device__ __forceinline__ float gelu_tanh_(float x) { return x * sigmoidf_(1.5957691216057308f * (x + 0.044715f * x * x * x)); }
; __device__ __forceinline__ void ph_lru_c(const Frame& F) {
;     ...
;         for (int et = 0; et < 4; ++et) {
;             const int ch = kb * 64 + et * 16 + 4 * g;
;             const float y0 = __uint_as_float(yw[et].x << 16), y1 = __uint_as_float(yw[et].x & 0xffff0000u), y2 = __uint_as_float(yw[et].y << 16), y3 = __uint_as_float(yw[et].y & 0xffff0000u);
;             float o[4];
; #pragma unroll
;             for (int i = 0; i < 4; ++i) o[i] = fmaf(av[0][et][i], hf[et][i], xv[0][et][i]) + fmaf(av[1][et][i], hb[et][i], xv[1][et][i]);
;             o[0] *= gelu_tanh_(y0); o[1] *= gelu_tanh_(y1); o[2] *= gelu_tanh_(y2); o[3] *= gelu_tanh_(y3);
;             u32x2 w; w.x = cvt_pk_bf16(o[0], o[1]); w.y = cvt_pk_bf16(o[2], o[3]);
;             *(u32x2*)(F.MIX + (size_t)row * DM + ch) = w;
	v_fmac_f32_dpp v103, v103, v97 row_shl:4 row_mask:0xf bank_mask:0xf
	v_fmac_f32_dpp v107, v107, v99 row_shl:4 row_mask:0xf bank_mask:0xf
	v_fmac_f32_dpp v111, v111, v105 row_shl:4 row_mask:0xf bank_mask:0xf
	v_mul_f32_dpp v95, v95, v95 row_shl:4 row_mask:0xf bank_mask:0xf
	v_mul_f32_dpp v97, v97, v97 row_shl:4 row_mask:0xf bank_mask:0xf
	v_mul_f32_dpp v99, v99, v99 row_shl:4 row_mask:0xf bank_mask:0xf
	v_mul_f32_dpp v105, v105, v105 row_shl:4 row_mask:0xf bank_mask:0xf
	v_fmac_f32_dpp v92, v92, v90 row_shr:4 row_mask:0xf bank_mask:0xf
	v_fmac_f32_dpp v88, v88, v86 row_shr:4 row_mask:0xf bank_mask:0xf
	v_fmac_f32_dpp v82, v82, v78 row_shr:4 row_mask:0xf bank_mask:0xf
	v_fmac_f32_dpp v84, v84, v80 row_shr:4 row_mask:0xf bank_mask:0xf
	v_mul_f32_dpp v90, v90, v90 row_shr:4 row_mask:0xf bank_mask:0xf
	v_mul_f32_dpp v86, v86, v86 row_shr:4 row_mask:0xf bank_mask:0xf
	v_mul_f32_dpp v78, v78, v78 row_shr:4 row_mask:0xf bank_mask:0xf
	v_mul_f32_dpp v80, v80, v80 row_shr:4 row_mask:0xf bank_mask:0xf
	v_fmac_f32_dpp v93, v93, v91 row_shl:4 row_mask:0xf bank_mask:0xf
	v_fmac_f32_dpp v89, v89, v87 row_shl:4 row_mask:0xf bank_mask:0xf
	v_fmac_f32_dpp v83, v83, v79 row_shl:4 row_mask:0xf bank_mask:0xf
	v_fmac_f32_dpp v85, v85, v81 row_shl:4 row_mask:0xf bank_mask:0xf
	v_mul_f32_dpp v91, v91, v91 row_shl:4 row_mask:0xf bank_mask:0xf
	v_mul_f32_dpp v87, v87, v87 row_shl:4 row_mask:0xf bank_mask:0xf
	v_mul_f32_dpp v79, v79, v79 row_shl:4 row_mask:0xf bank_mask:0xf
	v_mul_f32_dpp v81, v81, v81 row_shl:4 row_mask:0xf bank_mask:0xf
	v_fmac_f32_dpp v66, v66, v64 row_shr:4 row_mask:0xf bank_mask:0xf
	v_fmac_f32_dpp v62, v62, v60 row_shr:4 row_mask:0xf bank_mask:0xf
	v_fmac_f32_dpp v56, v56, v52 row_shr:4 row_mask:0xf bank_mask:0xf
	v_fmac_f32_dpp v58, v58, v54 row_shr:4 row_mask:0xf bank_mask:0xf
	v_mul_f32_dpp v64, v64, v64 row_shr:4 row_mask:0xf bank_mask:0xf
	v_mul_f32_dpp v60, v60, v60 row_shr:4 row_mask:0xf bank_mask:0xf
	v_mul_f32_dpp v52, v52, v52 row_shr:4 row_mask:0xf bank_mask:0xf
	v_mul_f32_dpp v54, v54, v54 row_shr:4 row_mask:0xf bank_mask:0xf
	v_fmac_f32_dpp v67, v67, v65 row_shl:4 row_mask:0xf bank_mask:0xf
	v_fmac_f32_dpp v63, v63, v61 row_shl:4 row_mask:0xf bank_mask:0xf
	v_fmac_f32_dpp v57, v57, v53 row_shl:4 row_mask:0xf bank_mask:0xf
	v_fmac_f32_dpp v59, v59, v55 row_shl:4 row_mask:0xf bank_mask:0xf
	v_mul_f32_dpp v65, v65, v65 row_shl:4 row_mask:0xf bank_mask:0xf
	v_mul_f32_dpp v61, v61, v61 row_shl:4 row_mask:0xf bank_mask:0xf
	v_mul_f32_dpp v53, v53, v53 row_shl:4 row_mask:0xf bank_mask:0xf
	v_mul_f32_dpp v55, v55, v55 row_shl:4 row_mask:0xf bank_mask:0xf
	v_fmac_f32_dpp v118, v118, v112 row_shr:8 row_mask:0xf bank_mask:0xf
	v_fmac_f32_dpp v120, v120, v114 row_shr:8 row_mask:0xf bank_mask:0xf
	v_fmac_f32_dpp v124, v124, v116 row_shr:8 row_mask:0xf bank_mask:0xf
	v_fmac_f32_dpp v126, v126, v122 row_shr:8 row_mask:0xf bank_mask:0xf
	v_mul_f32_dpp v112, v112, v112 row_shr:8 row_mask:0xf bank_mask:0xf
	v_mul_f32_dpp v114, v114, v114 row_shr:8 row_mask:0xf bank_mask:0xf
	v_mul_f32_dpp v116, v116, v116 row_shr:8 row_mask:0xf bank_mask:0xf
	v_mul_f32_dpp v122, v122, v122 row_shr:8 row_mask:0xf bank_mask:0xf
	v_fmac_f32_dpp v119, v119, v113 row_shl:8 row_mask:0xf bank_mask:0xf
	v_fmac_f32_dpp v121, v121, v115 row_shl:8 row_mask:0xf bank_mask:0xf
	v_fmac_f32_dpp v125, v125, v117 row_shl:8 row_mask:0xf bank_mask:0xf
	v_fmac_f32_dpp v127, v127, v123 row_shl:8 row_mask:0xf bank_mask:0xf
	v_mul_f32_dpp v113, v113, v113 row_shl:8 row_mask:0xf bank_mask:0xf
	v_mul_f32_dpp v115, v115, v115 row_shl:8 row_mask:0xf bank_mask:0xf
	v_mul_f32_dpp v117, v117, v117 row_shl:8 row_mask:0xf bank_mask:0xf
	v_mul_f32_dpp v123, v123, v123 row_shl:8 row_mask:0xf bank_mask:0xf
	v_and_b32_e32 v39, 0xffff0000, v108
	v_mov_b32_e32 v36, v28
	v_pk_fma_f32 v[28:29], v[114:115], v[32:33], v[120:121]
	v_lshlrev_b32_e32 v40, 16, v109
	v_add_f32_e32 v32, v28, v29
	v_mov_b32_e32 v29, v34
	v_mov_b32_e32 v34, v31
	v_mul_f32_e32 v31, 0x3d372713, v39
	v_mul_f32_e32 v31, v31, v39
	v_fma_f32 v31, v31, v39, v39
	v_mul_f32_e32 v31, 0x3fcc422a, v31
	v_mul_f32_e32 v31, 0xbfb8aa3b, v31
	v_exp_f32_e32 v31, v31
	v_mov_b32_e32 v28, v30
	v_pk_fma_f32 v[28:29], v[116:117], v[28:29], v[124:125]
	v_lshlrev_b32_e32 v38, 16, v108
	v_add_f32_e32 v31, 1.0, v31
	v_rcp_f32_e32 v31, v31
	v_and_b32_e32 v41, 0xffff0000, v109
	v_add_f32_e32 v30, v28, v29
	v_pk_fma_f32 v[28:29], v[122:123], v[34:35], v[126:127]
	v_mul_f32_e32 v31, v31, v39
	v_mul_f32_e32 v31, v31, v32
	v_mul_f32_e32 v32, 0x3d372713, v40
	v_mul_f32_e32 v32, v32, v40
	v_fma_f32 v32, v32, v40, v40
	v_mul_f32_e32 v32, 0x3fcc422a, v32
	v_mul_f32_e32 v32, 0xbfb8aa3b, v32
	v_exp_f32_e32 v32, v32
	v_add_f32_e32 v28, v28, v29
	v_mul_f32_e32 v29, 0x3d372713, v38
	v_mul_f32_e32 v29, v29, v38
	v_add_f32_e32 v32, 1.0, v32
	v_rcp_f32_e32 v32, v32
	v_fma_f32 v29, v29, v38, v38
	v_mul_f32_e32 v29, 0x3fcc422a, v29
	v_mul_f32_e32 v29, 0xbfb8aa3b, v29
	v_mul_f32_e32 v32, v32, v40
	v_mul_f32_e32 v32, v32, v30
	v_mul_f32_e32 v30, 0x3d372713, v41
	v_mul_f32_e32 v30, v30, v41
	v_fma_f32 v30, v30, v41, v41
	v_mul_f32_e32 v30, 0x3fcc422a, v30
	v_mul_f32_e32 v30, 0xbfb8aa3b, v30
	v_exp_f32_e32 v29, v29
	v_exp_f32_e32 v30, v30
	v_pk_fma_f32 v[36:37], v[112:113], v[36:37], v[118:119]
	v_fmac_f32_dpp v100, v100, v94 row_shr:8 row_mask:0xf bank_mask:0xf
	v_fmac_f32_dpp v102, v102, v96 row_shr:8 row_mask:0xf bank_mask:0xf
	v_fmac_f32_dpp v106, v106, v98 row_shr:8 row_mask:0xf bank_mask:0xf
	v_fmac_f32_dpp v110, v110, v104 row_shr:8 row_mask:0xf bank_mask:0xf
	v_mul_f32_dpp v94, v94, v94 row_shr:8 row_mask:0xf bank_mask:0xf
	v_mul_f32_dpp v96, v96, v96 row_shr:8 row_mask:0xf bank_mask:0xf
; __device__ __forceinline__ unsigned cvt_pk_bf16(float lo, float hi) { unsigned r; asm volatile("v_cvt_pk_bf16_f32 %0, %1, %2" : "=v"(r) : "v"(lo), "v"(hi)); return r; }
; __device__ __forceinline__ float gelu_tanh_(float x) { return x * sigmoidf_(1.5957691216057308f * (x + 0.044715f * x * x * x)); }
; __device__ __forceinline__ void ph_lru_c(const Frame& F) {
;     ...
;         for (int et = 0; et < 4; ++et) {
;             const int ch = kb * 64 + et * 16 + 4 * g;
;             const float y0 = __uint_as_float(yw[et].x << 16), y1 = __uint_as_float(yw[et].x & 0xffff0000u), y2 = __uint_as_float(yw[et].y << 16), y3 = __uint_as_float(yw[et].y & 0xffff0000u);
;             float o[4];
; #pragma unroll
;             for (int i = 0; i < 4; ++i) o[i] = fmaf(av[0][et][i], hf[et][i], xv[0][et][i]) + fmaf(av[1][et][i], hb[et][i], xv[1][et][i]);
;             o[0] *= gelu_tanh_(y0); o[1] *= gelu_tanh_(y1); o[2] *= gelu_tanh_(y2); o[3] *= gelu_tanh_(y3);
;             u32x2 w; w.x = cvt_pk_bf16(o[0], o[1]); w.y = cvt_pk_bf16(o[2], o[3]);
;             *(u32x2*)(F.MIX + (size_t)row * DM + ch) = w;
;         }
	v_mul_f32_dpp v98, v98, v98 row_shr:8 row_mask:0xf bank_mask:0xf
	v_mul_f32_dpp v104, v104, v104 row_shr:8 row_mask:0xf bank_mask:0xf
	v_add_f32_e32 v29, 1.0, v29
	v_add_f32_e32 v30, 1.0, v30
	v_rcp_f32_e32 v29, v29
	v_rcp_f32_e32 v30, v30
	v_add_f32_e32 v36, v36, v37
	v_fmac_f32_dpp v101, v101, v95 row_shl:8 row_mask:0xf bank_mask:0xf
	v_fmac_f32_dpp v103, v103, v97 row_shl:8 row_mask:0xf bank_mask:0xf
	v_fmac_f32_dpp v107, v107, v99 row_shl:8 row_mask:0xf bank_mask:0xf
	v_fmac_f32_dpp v111, v111, v105 row_shl:8 row_mask:0xf bank_mask:0xf
	v_mul_f32_dpp v95, v95, v95 row_shl:8 row_mask:0xf bank_mask:0xf
	v_mul_f32_dpp v97, v97, v97 row_shl:8 row_mask:0xf bank_mask:0xf
	v_mul_f32_dpp v99, v99, v99 row_shl:8 row_mask:0xf bank_mask:0xf
	v_mul_f32_dpp v105, v105, v105 row_shl:8 row_mask:0xf bank_mask:0xf
	v_mul_f32_e32 v29, v29, v38
	v_mul_f32_e32 v30, v30, v41
	v_mul_f32_e32 v29, v29, v36
	v_mul_f32_e32 v28, v30, v28
	v_fmac_f32_dpp v92, v92, v90 row_shr:8 row_mask:0xf bank_mask:0xf
	v_fmac_f32_dpp v88, v88, v86 row_shr:8 row_mask:0xf bank_mask:0xf
	v_fmac_f32_dpp v82, v82, v78 row_shr:8 row_mask:0xf bank_mask:0xf
	v_fmac_f32_dpp v84, v84, v80 row_shr:8 row_mask:0xf bank_mask:0xf
	v_mul_f32_dpp v90, v90, v90 row_shr:8 row_mask:0xf bank_mask:0xf
	v_mul_f32_dpp v86, v86, v86 row_shr:8 row_mask:0xf bank_mask:0xf
	v_mul_f32_dpp v78, v78, v78 row_shr:8 row_mask:0xf bank_mask:0xf
	v_mul_f32_dpp v80, v80, v80 row_shr:8 row_mask:0xf bank_mask:0xf
	v_fmac_f32_dpp v93, v93, v91 row_shl:8 row_mask:0xf bank_mask:0xf
	v_fmac_f32_dpp v89, v89, v87 row_shl:8 row_mask:0xf bank_mask:0xf
	v_fmac_f32_dpp v83, v83, v79 row_shl:8 row_mask:0xf bank_mask:0xf
	v_fmac_f32_dpp v85, v85, v81 row_shl:8 row_mask:0xf bank_mask:0xf
	v_mul_f32_dpp v91, v91, v91 row_shl:8 row_mask:0xf bank_mask:0xf
	v_mul_f32_dpp v87, v87, v87 row_shl:8 row_mask:0xf bank_mask:0xf
	v_mul_f32_dpp v79, v79, v79 row_shl:8 row_mask:0xf bank_mask:0xf
	v_mul_f32_dpp v81, v81, v81 row_shl:8 row_mask:0xf bank_mask:0xf
	v_fmac_f32_dpp v66, v66, v64 row_shr:8 row_mask:0xf bank_mask:0xf
	v_fmac_f32_dpp v62, v62, v60 row_shr:8 row_mask:0xf bank_mask:0xf
	v_fmac_f32_dpp v56, v56, v52 row_shr:8 row_mask:0xf bank_mask:0xf
	v_fmac_f32_dpp v58, v58, v54 row_shr:8 row_mask:0xf bank_mask:0xf
	v_mul_f32_dpp v64, v64, v64 row_shr:8 row_mask:0xf bank_mask:0xf
	v_mul_f32_dpp v60, v60, v60 row_shr:8 row_mask:0xf bank_mask:0xf
	v_mul_f32_dpp v52, v52, v52 row_shr:8 row_mask:0xf bank_mask:0xf
	v_mul_f32_dpp v54, v54, v54 row_shr:8 row_mask:0xf bank_mask:0xf
	v_fmac_f32_dpp v67, v67, v65 row_shl:8 row_mask:0xf bank_mask:0xf
	v_fmac_f32_dpp v63, v63, v61 row_shl:8 row_mask:0xf bank_mask:0xf
	v_fmac_f32_dpp v57, v57, v53 row_shl:8 row_mask:0xf bank_mask:0xf
	v_fmac_f32_dpp v59, v59, v55 row_shl:8 row_mask:0xf bank_mask:0xf
	v_mul_f32_dpp v65, v65, v65 row_shl:8 row_mask:0xf bank_mask:0xf
	v_mul_f32_dpp v61, v61, v61 row_shl:8 row_mask:0xf bank_mask:0xf
	v_mul_f32_dpp v53, v53, v53 row_shl:8 row_mask:0xf bank_mask:0xf
	v_mul_f32_dpp v55, v55, v55 row_shl:8 row_mask:0xf bank_mask:0xf
	v_cvt_pk_bf16_f32 v30, v29, v31
	v_cvt_pk_bf16_f32 v31, v32, v28
	v_lshl_add_u64 v[28:29], s[76:77], 0, v[70:71]
	v_lshl_add_u64 v[28:29], v[28:29], 0, v[74:75]
	global_store_dwordx2 v[28:29], v[30:31], off
	v_mov_b32_e32 v31, v24
	v_mov_b32_e32 v24, v21
	v_and_b32_e32 v33, 0xffff0000, v76
	v_mov_b32_e32 v30, v20
	v_pk_fma_f32 v[20:21], v[96:97], v[24:25], v[102:103]
	v_lshlrev_b32_e32 v34, 16, v77
	v_add_f32_e32 v24, v20, v21
	v_mov_b32_e32 v21, v26
	v_mov_b32_e32 v26, v23
	v_mul_f32_e32 v23, 0x3d372713, v33
	v_mul_f32_e32 v23, v23, v33
	v_fma_f32 v23, v23, v33, v33
	v_mul_f32_e32 v23, 0x3fcc422a, v23
	v_mul_f32_e32 v23, 0xbfb8aa3b, v23
	v_exp_f32_e32 v23, v23
	v_mov_b32_e32 v20, v22
	v_pk_fma_f32 v[20:21], v[98:99], v[20:21], v[106:107]
	v_lshlrev_b32_e32 v32, 16, v76
	v_add_f32_e32 v23, 1.0, v23
	v_rcp_f32_e32 v23, v23
	v_add_f32_e32 v22, v20, v21
	v_pk_fma_f32 v[20:21], v[104:105], v[26:27], v[110:111]
	v_and_b32_e32 v35, 0xffff0000, v77
	v_mul_f32_e32 v23, v23, v33
	v_mul_f32_e32 v23, v23, v24
	v_mul_f32_e32 v24, 0x3d372713, v34
	v_mul_f32_e32 v24, v24, v34
	v_fma_f32 v24, v24, v34, v34
	v_mul_f32_e32 v24, 0x3fcc422a, v24
	v_mul_f32_e32 v24, 0xbfb8aa3b, v24
	v_exp_f32_e32 v24, v24
	v_add_f32_e32 v20, v20, v21
	v_mul_f32_e32 v21, 0x3d372713, v32
	v_mul_f32_e32 v21, v21, v32
	v_add_f32_e32 v24, 1.0, v24
	v_rcp_f32_e32 v24, v24
	v_fma_f32 v21, v21, v32, v32
	v_mul_f32_e32 v21, 0x3fcc422a, v21
	v_mul_f32_e32 v21, 0xbfb8aa3b, v21
; __device__ __forceinline__ unsigned cvt_pk_bf16(float lo, float hi) { unsigned r; asm volatile("v_cvt_pk_bf16_f32 %0, %1, %2" : "=v"(r) : "v"(lo), "v"(hi)); return r; }
; __device__ __forceinline__ float gelu_tanh_(float x) { return x * sigmoidf_(1.5957691216057308f * (x + 0.044715f * x * x * x)); }
; __device__ __forceinline__ void ph_lru_c(const Frame& F) {
;     ...
;         for (int et = 0; et < 4; ++et) {
;             const int ch = kb * 64 + et * 16 + 4 * g;
;             const float y0 = __uint_as_float(yw[et].x << 16), y1 = __uint_as_float(yw[et].x & 0xffff0000u), y2 = __uint_as_float(yw[et].y << 16), y3 = __uint_as_float(yw[et].y & 0xffff0000u);
;             float o[4];
; #pragma unroll
;             for (int i = 0; i < 4; ++i) o[i] = fmaf(av[0][et][i], hf[et][i], xv[0][et][i]) + fmaf(av[1][et][i], hb[et][i], xv[1][et][i]);
;             o[0] *= gelu_tanh_(y0); o[1] *= gelu_tanh_(y1); o[2] *= gelu_tanh_(y2); o[3] *= gelu_tanh_(y3);
;             u32x2 w; w.x = cvt_pk_bf16(o[0], o[1]); w.y = cvt_pk_bf16(o[2], o[3]);
;             *(u32x2*)(F.MIX + (size_t)row * DM + ch) = w;
;         }
;     }
	v_mul_f32_e32 v24, v24, v34
	v_mul_f32_e32 v22, v24, v22
	v_mul_f32_e32 v24, 0x3d372713, v35
	v_mul_f32_e32 v24, v24, v35
	v_fma_f32 v24, v24, v35, v35
	v_mul_f32_e32 v24, 0x3fcc422a, v24
	v_exp_f32_e32 v21, v21
	v_mul_f32_e32 v24, 0xbfb8aa3b, v24
	v_exp_f32_e32 v24, v24
	v_pk_fma_f32 v[30:31], v[94:95], v[30:31], v[100:101]
	v_add_f32_e32 v21, 1.0, v21
	v_rcp_f32_e32 v21, v21
	v_add_f32_e32 v24, 1.0, v24
	v_rcp_f32_e32 v24, v24
	v_add_f32_e32 v30, v30, v31
	v_mul_f32_e32 v21, v21, v32
	v_mul_f32_e32 v21, v21, v30
	v_mul_f32_e32 v24, v24, v35
	v_mul_f32_e32 v24, v24, v20
	v_cvt_pk_bf16_f32 v20, v21, v23
	v_cvt_pk_bf16_f32 v21, v22, v24
	global_store_dwordx2 v[28:29], v[20:21], off offset:32
	v_mov_b32_e32 v21, v16
	v_mov_b32_e32 v16, v13
	v_and_b32_e32 v23, 0xffff0000, v72
	v_mov_b32_e32 v20, v12
	v_pk_fma_f32 v[12:13], v[86:87], v[16:17], v[88:89]
	v_lshlrev_b32_e32 v24, 16, v73
	v_add_f32_e32 v16, v12, v13
	v_mov_b32_e32 v13, v18
	v_mov_b32_e32 v18, v15
	v_mul_f32_e32 v15, 0x3d372713, v23
	v_mul_f32_e32 v15, v15, v23
	v_fma_f32 v15, v15, v23, v23
	v_mul_f32_e32 v15, 0x3fcc422a, v15
	v_mul_f32_e32 v15, 0xbfb8aa3b, v15
	v_exp_f32_e32 v15, v15
	v_mov_b32_e32 v12, v14
	v_pk_fma_f32 v[12:13], v[78:79], v[12:13], v[82:83]
	v_lshlrev_b32_e32 v22, 16, v72
	v_add_f32_e32 v15, 1.0, v15
	v_rcp_f32_e32 v15, v15
	v_add_f32_e32 v14, v12, v13
	v_pk_fma_f32 v[12:13], v[80:81], v[18:19], v[84:85]
	v_and_b32_e32 v25, 0xffff0000, v73
	v_mul_f32_e32 v15, v15, v23
	v_mul_f32_e32 v15, v15, v16
	v_mul_f32_e32 v16, 0x3d372713, v24
	v_mul_f32_e32 v16, v16, v24
	v_fma_f32 v16, v16, v24, v24
	v_mul_f32_e32 v16, 0x3fcc422a, v16
	v_mul_f32_e32 v16, 0xbfb8aa3b, v16
	v_exp_f32_e32 v16, v16
	v_add_f32_e32 v12, v12, v13
	v_mul_f32_e32 v13, 0x3d372713, v22
	v_mul_f32_e32 v13, v13, v22
	v_add_f32_e32 v16, 1.0, v16
	v_rcp_f32_e32 v16, v16
	v_fma_f32 v13, v13, v22, v22
	v_mul_f32_e32 v13, 0x3fcc422a, v13
	v_mul_f32_e32 v13, 0xbfb8aa3b, v13
	v_mul_f32_e32 v16, v16, v24
	v_mul_f32_e32 v14, v16, v14
	v_mul_f32_e32 v16, 0x3d372713, v25
	v_mul_f32_e32 v16, v16, v25
	v_fma_f32 v16, v16, v25, v25
	v_mul_f32_e32 v16, 0x3fcc422a, v16
	v_exp_f32_e32 v13, v13
	v_mul_f32_e32 v16, 0xbfb8aa3b, v16
	v_exp_f32_e32 v16, v16
	v_pk_fma_f32 v[20:21], v[90:91], v[20:21], v[92:93]
	v_add_f32_e32 v13, 1.0, v13
	v_rcp_f32_e32 v13, v13
	v_add_f32_e32 v16, 1.0, v16
	v_rcp_f32_e32 v16, v16
	v_add_f32_e32 v20, v20, v21
	v_mul_f32_e32 v13, v13, v22
	v_mul_f32_e32 v13, v13, v20
	v_mul_f32_e32 v16, v16, v25
	v_mul_f32_e32 v16, v16, v12
	v_cvt_pk_bf16_f32 v12, v13, v15
	v_cvt_pk_bf16_f32 v13, v14, v16
	global_store_dwordx2 v[28:29], v[12:13], off offset:64
	v_mov_b32_e32 v13, v8
	v_mov_b32_e32 v8, v5
	v_and_b32_e32 v15, 0xffff0000, v68
	v_mov_b32_e32 v12, v4
	v_pk_fma_f32 v[4:5], v[60:61], v[8:9], v[62:63]
	v_lshlrev_b32_e32 v16, 16, v69
	v_add_f32_e32 v8, v4, v5
	v_mov_b32_e32 v5, v10
	v_mov_b32_e32 v10, v7
	v_mul_f32_e32 v7, 0x3d372713, v15
	v_mul_f32_e32 v7, v7, v15
	v_fma_f32 v7, v7, v15, v15
	v_mul_f32_e32 v7, 0x3fcc422a, v7
	v_mul_f32_e32 v7, 0xbfb8aa3b, v7
	v_exp_f32_e32 v7, v7
	v_mov_b32_e32 v4, v6
	v_pk_fma_f32 v[4:5], v[52:53], v[4:5], v[56:57]
	v_lshlrev_b32_e32 v14, 16, v68
	v_add_f32_e32 v7, 1.0, v7
	v_rcp_f32_e32 v7, v7
	v_add_f32_e32 v6, v4, v5
	v_pk_fma_f32 v[4:5], v[54:55], v[10:11], v[58:59]
	v_and_b32_e32 v17, 0xffff0000, v69
	v_mul_f32_e32 v7, v7, v15
	v_mul_f32_e32 v7, v7, v8
	v_mul_f32_e32 v8, 0x3d372713, v16
	v_mul_f32_e32 v8, v8, v16
	v_fma_f32 v8, v8, v16, v16
	v_mul_f32_e32 v8, 0x3fcc422a, v8
	v_mul_f32_e32 v8, 0xbfb8aa3b, v8
	v_exp_f32_e32 v8, v8
	v_add_f32_e32 v4, v4, v5
	v_mul_f32_e32 v5, 0x3d372713, v14
	v_mul_f32_e32 v5, v5, v14
	v_add_f32_e32 v8, 1.0, v8
	v_rcp_f32_e32 v8, v8
	v_fma_f32 v5, v5, v14, v14
	v_mul_f32_e32 v5, 0x3fcc422a, v5
	v_mul_f32_e32 v5, 0xbfb8aa3b, v5
	v_mul_f32_e32 v8, v8, v16
	v_mul_f32_e32 v6, v8, v6
	v_mul_f32_e32 v8, 0x3d372713, v17
	v_mul_f32_e32 v8, v8, v17
	v_fma_f32 v8, v8, v17, v17
	v_mul_f32_e32 v8, 0x3fcc422a, v8
	v_exp_f32_e32 v5, v5
	v_mul_f32_e32 v8, 0xbfb8aa3b, v8
	v_exp_f32_e32 v8, v8
	v_pk_fma_f32 v[12:13], v[64:65], v[12:13], v[66:67]
	v_add_f32_e32 v5, 1.0, v5
	v_rcp_f32_e32 v5, v5
	v_add_f32_e32 v8, 1.0, v8
	v_rcp_f32_e32 v8, v8
	v_add_f32_e32 v12, v12, v13
	v_mul_f32_e32 v5, v5, v14
	v_mul_f32_e32 v5, v5, v12
	v_mul_f32_e32 v8, v8, v17
	v_mul_f32_e32 v8, v8, v4
	v_cvt_pk_bf16_f32 v4, v5, v7
	v_cvt_pk_bf16_f32 v5, v6, v8
	global_store_dwordx2 v[28:29], v[4:5], off offset:96
	s_cbranch_scc0 .LBB0_1158

; #define LAS __attribute__((address_space(3)))
; __device__ __forceinline__ float sigmoidf_(float x) { return __builtin_amdgcn_rcpf(1.0f + __expf(-x)); }
; template <int CTRL> __device__ __forceinline__ float dpp_add0(float x) { return x + dppf<CTRL>(0.0f, x); }
; template <bool WITHO, bool RAW = false>
; __device__ __forceinline__ void hg_pass(const Frame& F, const bf16_t* P, const float* lbh, int b, int h, int nb, int dir, f32x4 (&S)[4][4], float (&Gsum)[16],
;                                         LAS bf16_t* Vl, LAS bf16_t* Kl, float* OF, const float* ngp) {
;     ...
;         for (int m = 0; m < 4; ++m) { const float z0 = __uint_as_float(zr[m].x << 16), z1 = __uint_as_float(zr[m].x & 0xffff0000u), z2 = __uint_as_float(zr[m].y << 16), z3 = __uint_as_float(zr[m].y & 0xffff0000u);
;             const float zz[4] = {z0, z1, z2, z3};
;             const f32x4 lb4 = *(const f32x4*)(lbh + 16 * m + 4 * g);
; #pragma unroll
;             for (int i = 0; i < 4; ++i) { const float lb = lb4[i]; const float f = fmaxf(lb + (1.0f - lb) * sigmoidf_(zz[i]), 1e-30f); kk[m * 4 + i] = 1.0f - f; c[m * 4 + i] = __logf(f); }
;             *(LAS u32x2*)(Vl + tau * 64 + 16 * m + 4 * g) = vr[m];
;  }
;         if (ci + 1 < HG_U / 16) { const int pos = (ci + 1) * 16 + tau, t = dir ? (HG_U - 1 - pos) : pos; const bf16_t* pr = P + (size_t)hg_row(b, nb, t) * 4096 + h * 64 + 4 * g;
; #pragma unroll
;             for (int m = 0; m < 4; ++m) { zr[m] = *(const u32x2*)(pr + (dir ? 2560 : 2048) + 16 * m); vr[m] = *(const u32x2*)(pr + 3072 + 16 * m); } }
;         float G[16];
; #pragma unroll
;         for (int q = 0; q < 16; ++q) G[q] = c[q];
; #pragma unroll
;         for (int q = 0; q < 16; q += 4) ROW_ALLREDUCE4(G[q], G[q + 1], G[q + 2], G[q + 3]);
; #pragma unroll
;         for (int q = 0; q < 16; ++q) { c[q] = dpp_add0<0x111>(c[q]); c[q] = dpp_add0<0x112>(c[q]); c[q] = dpp_add0<0x114>(c[q]); c[q] = dpp_add0<0x118>(c[q]); }
.LBB0_1172:
	v_lshlrev_b32_e32 v3, 16, v90
	v_mul_f32_e32 v3, 0xbfb8aa3b, v3
	v_exp_f32_e32 v3, v3
	s_waitcnt vmcnt(0)
	v_sub_f32_e32 v93, 1.0, v80
	v_and_b32_e32 v90, 0xffff0000, v90
	v_mul_f32_e32 v90, 0xbfb8aa3b, v90
	v_add_f32_e32 v3, 1.0, v3
	v_rcp_f32_e32 v3, v3
	v_exp_f32_e32 v90, v90
	v_lshlrev_b32_e32 v92, 16, v91
	v_and_b32_e32 v91, 0xffff0000, v91
	v_fma_f32 v3, v3, v93, v80
	v_max_f32_e32 v3, 0xda24260, v3
	v_add_f32_e32 v90, 1.0, v90
	v_sub_f32_e32 v100, 1.0, v3
	v_log_f32_e32 v80, v3
	v_rcp_f32_e32 v90, v90
	v_mul_f32_e32 v91, 0xbfb8aa3b, v91
	v_exp_f32_e32 v91, v91
	v_mul_f32_e32 v3, 0x3f317217, v80
	v_fma_f32 v3, v80, s93, -v3
	v_fmac_f32_e32 v3, 0x3377d1cf, v80
	v_fmac_f32_e32 v3, 0x3f317217, v80
	v_add_f32_e32 v91, 1.0, v91
	v_rcp_f32_e32 v91, v91
	v_sub_f32_e32 v80, 1.0, v81
	v_fma_f32 v80, v90, v80, v81
	v_max_f32_e32 v80, 0xda24260, v80
	v_mul_f32_e32 v90, 0xbfb8aa3b, v92
	v_log_f32_e32 v81, v80
	v_exp_f32_e32 v90, v90
	v_sub_f32_e32 v101, 1.0, v80
	v_lshlrev_b32_e32 v92, 16, v88
	v_mul_f32_e32 v80, 0x3f317217, v81
	v_add_f32_e32 v90, 1.0, v90
	v_fma_f32 v80, v81, s93, -v80
	v_rcp_f32_e32 v90, v90
	v_fmac_f32_e32 v80, 0x3377d1cf, v81
	v_fmac_f32_e32 v80, 0x3f317217, v81
	v_mul_f32_e32 v92, 0xbfb8aa3b, v92
	v_exp_f32_e32 v92, v92
	v_sub_f32_e32 v81, 1.0, v82
	v_fma_f32 v81, v90, v81, v82
	v_max_f32_e32 v81, 0xda24260, v81
	v_cmp_gt_f32_e32 vcc, s92, v81
	v_add_f32_e32 v92, 1.0, v92
	v_rcp_f32_e32 v92, v92
	v_cndmask_b32_e64 v82, 0, 32, vcc
	v_ldexp_f32 v82, v81, v82
	v_log_f32_e32 v90, v82
	v_sub_f32_e32 v82, 1.0, v81
	v_mul_f32_e32 v81, 0x3f317217, v90
	v_fma_f32 v81, v90, s93, -v81
	v_fmac_f32_e32 v81, 0x3377d1cf, v90
	v_fmac_f32_e32 v81, 0x3f317217, v90
	v_cmp_lt_f32_e64 s[48:49], |v90|, s90
	v_and_b32_e32 v88, 0xffff0000, v88
	v_mul_f32_e32 v88, 0xbfb8aa3b, v88
	v_cndmask_b32_e64 v81, v90, v81, s[48:49]
	v_sub_f32_e32 v90, 1.0, v83
	v_fmac_f32_e32 v83, v91, v90
	v_max_f32_e32 v83, 0xda24260, v83
	v_cndmask_b32_e32 v91, 0, v179, vcc
	v_sub_f32_e32 v81, v81, v91
	v_log_f32_e32 v90, v83
	v_exp_f32_e32 v88, v88
	v_mov_b32_e32 v227, v3
	v_add_f32_dpp v3, v3, v3 row_shr:1 row_mask:0xf bank_mask:0xf bound_ctrl:1
	v_mul_f32_e32 v91, 0x3f317217, v90
	v_fma_f32 v91, v90, s93, -v91
	v_fmac_f32_e32 v91, 0x3377d1cf, v90
	v_fmac_f32_e32 v91, 0x3f317217, v90
	v_add_f32_e32 v88, 1.0, v88
	v_rcp_f32_e32 v88, v88
	v_mov_b32_e32 v90, v91
	v_sub_f32_e32 v91, 1.0, v76
	v_fma_f32 v76, v92, v91, v76
	v_max_f32_e32 v76, 0xda24260, v76
	v_sub_f32_e32 v102, 1.0, v76
	v_lshlrev_b32_e32 v92, 16, v89
	v_log_f32_e32 v91, v76
	v_and_b32_e32 v89, 0xffff0000, v89
	v_mul_f32_e32 v89, 0xbfb8aa3b, v89
	v_exp_f32_e32 v89, v89
	v_mul_f32_e32 v76, 0x3f317217, v91
	v_fma_f32 v76, v91, s93, -v76
	v_fmac_f32_e32 v76, 0x3377d1cf, v91
	v_fmac_f32_e32 v76, 0x3f317217, v91
	v_add_f32_e32 v89, 1.0, v89
	v_rcp_f32_e32 v89, v89
	v_sub_f32_e32 v91, 1.0, v77
	v_fma_f32 v77, v88, v91, v77
	v_max_f32_e32 v77, 0xda24260, v77
	v_mul_f32_e32 v91, 0xbfb8aa3b, v92
	v_log_f32_e32 v88, v77
	v_exp_f32_e32 v91, v91
	v_sub_f32_e32 v103, 1.0, v77
	v_lshlrev_b32_e32 v92, 16, v84
	v_mul_f32_e32 v77, 0x3f317217, v88
	v_add_f32_e32 v91, 1.0, v91
	v_fma_f32 v77, v88, s93, -v77
	v_rcp_f32_e32 v91, v91
	v_fmac_f32_e32 v77, 0x3377d1cf, v88
	v_fmac_f32_e32 v77, 0x3f317217, v88
	v_mul_f32_e32 v92, 0xbfb8aa3b, v92
	v_exp_f32_e32 v92, v92
	v_sub_f32_e32 v88, 1.0, v78
	v_fma_f32 v78, v91, v88, v78
	v_max_f32_e32 v78, 0xda24260, v78
	v_sub_f32_e32 v104, 1.0, v78
	v_log_f32_e32 v88, v78
	v_lshlrev_b32_e32 v91, 16, v87
	v_mul_f32_e32 v91, 0xbfb8aa3b, v91
	v_mul_f32_e32 v78, 0x3f317217, v88
	v_fma_f32 v78, v88, s93, -v78
	v_fmac_f32_e32 v78, 0x3377d1cf, v88
	v_fmac_f32_e32 v78, 0x3f317217, v88
	v_exp_f32_e32 v91, v91
	v_and_b32_e32 v87, 0xffff0000, v87
	v_sub_f32_e32 v88, 1.0, v79
	v_fmac_f32_e32 v79, v89, v88
	v_max_f32_e32 v79, 0xda24260, v79
	v_sub_f32_e32 v105, 1.0, v79
	v_mov_b32_e32 v88, v79
	v_lshlrev_b32_e32 v79, 16, v86
	v_log_f32_e32 v88, v88
	v_mul_f32_e32 v79, 0xbfb8aa3b, v79
	v_exp_f32_e32 v79, v79
	v_mov_b32_e32 v89, v78
	v_mul_f32_e32 v78, 0x3f317217, v88
	v_fma_f32 v78, v88, s93, -v78
	v_add_f32_e32 v79, 1.0, v79
	v_fmac_f32_e32 v78, 0x3377d1cf, v88
	v_rcp_f32_e32 v79, v79
	v_fmac_f32_e32 v78, 0x3f317217, v88
	v_and_b32_e32 v86, 0xffff0000, v86
	v_mul_f32_e32 v86, 0xbfb8aa3b, v86
	v_mov_b32_e32 v88, v78
	v_sub_f32_e32 v78, 1.0, v72
	v_fma_f32 v72, v79, v78, v72
	v_max_f32_e32 v72, 0xda24260, v72
	v_cmp_gt_f32_e32 vcc, s92, v72
	v_exp_f32_e32 v86, v86
	v_add_f32_e32 v91, 1.0, v91
	v_cndmask_b32_e64 v78, 0, 32, vcc
	v_ldexp_f32 v78, v72, v78
	v_log_f32_e32 v79, v78
	v_sub_f32_e32 v78, 1.0, v72
	v_add_f32_e32 v86, 1.0, v86
	v_rcp_f32_e32 v86, v86
	v_mul_f32_e32 v72, 0x3f317217, v79
	v_fma_f32 v72, v79, s93, -v72
	v_fmac_f32_e32 v72, 0x3377d1cf, v79
	v_fmac_f32_e32 v72, 0x3f317217, v79
	v_cmp_lt_f32_e64 s[48:49], |v79|, s90
	v_rcp_f32_e32 v91, v91
	v_mul_f32_e32 v87, 0xbfb8aa3b, v87
	v_cndmask_b32_e64 v72, v79, v72, s[48:49]
	v_sub_f32_e32 v79, 1.0, v73
	v_fma_f32 v73, v86, v79, v73
	v_max_f32_e32 v73, 0xda24260, v73
	v_cmp_gt_f32_e64 s[48:49], s92, v73
	v_exp_f32_e32 v87, v87
	v_add_f32_e32 v92, 1.0, v92
	v_cndmask_b32_e64 v79, 0, 32, s[48:49]
	v_ldexp_f32 v79, v73, v79
	v_log_f32_e32 v86, v79
	v_cndmask_b32_e32 v79, 0, v179, vcc
	v_sub_f32_e32 v72, v72, v79
	v_sub_f32_e32 v79, 1.0, v73
	v_mul_f32_e32 v73, 0x3f317217, v86
	v_fma_f32 v73, v86, s93, -v73
	v_fmac_f32_e32 v73, 0x3377d1cf, v86
	v_fmac_f32_e32 v73, 0x3f317217, v86
	v_cmp_lt_f32_e64 vcc, |v86|, s90
	v_add_f32_e32 v87, 1.0, v87
	v_rcp_f32_e32 v87, v87
	v_cndmask_b32_e32 v73, v86, v73, vcc
	v_sub_f32_e32 v86, 1.0, v74
; #define LAS __attribute__((address_space(3)))
; __device__ __forceinline__ float sigmoidf_(float x) { return __builtin_amdgcn_rcpf(1.0f + __expf(-x)); }
; template <int CTRL> __device__ __forceinline__ float dpp_add0(float x) { return x + dppf<CTRL>(0.0f, x); }
; template <bool WITHO, bool RAW = false>
; __device__ __forceinline__ void hg_pass(const Frame& F, const bf16_t* P, const float* lbh, int b, int h, int nb, int dir, f32x4 (&S)[4][4], float (&Gsum)[16],
;                                         LAS bf16_t* Vl, LAS bf16_t* Kl, float* OF, const float* ngp) {
;     ...
;         for (int m = 0; m < 4; ++m) { const float z0 = __uint_as_float(zr[m].x << 16), z1 = __uint_as_float(zr[m].x & 0xffff0000u), z2 = __uint_as_float(zr[m].y << 16), z3 = __uint_as_float(zr[m].y & 0xffff0000u);
;             const float zz[4] = {z0, z1, z2, z3};
;             const f32x4 lb4 = *(const f32x4*)(lbh + 16 * m + 4 * g);
; #pragma unroll
;             for (int i = 0; i < 4; ++i) { const float lb = lb4[i]; const float f = fmaxf(lb + (1.0f - lb) * sigmoidf_(zz[i]), 1e-30f); kk[m * 4 + i] = 1.0f - f; c[m * 4 + i] = __logf(f); }
;             *(LAS u32x2*)(Vl + tau * 64 + 16 * m + 4 * g) = vr[m];
;  }
;         if (ci + 1 < HG_U / 16) { const int pos = (ci + 1) * 16 + tau, t = dir ? (HG_U - 1 - pos) : pos; const bf16_t* pr = P + (size_t)hg_row(b, nb, t) * 4096 + h * 64 + 4 * g;
; #pragma unroll
;             for (int m = 0; m < 4; ++m) { zr[m] = *(const u32x2*)(pr + (dir ? 2560 : 2048) + 16 * m); vr[m] = *(const u32x2*)(pr + 3072 + 16 * m); } }
;         float G[16];
; #pragma unroll
;         for (int q = 0; q < 16; ++q) G[q] = c[q];
; #pragma unroll
;         for (int q = 0; q < 16; q += 4) ROW_ALLREDUCE4(G[q], G[q + 1], G[q + 2], G[q + 3]);
; #pragma unroll
;         for (int q = 0; q < 16; ++q) { c[q] = dpp_add0<0x111>(c[q]); c[q] = dpp_add0<0x112>(c[q]); c[q] = dpp_add0<0x114>(c[q]); c[q] = dpp_add0<0x118>(c[q]); }
	v_fma_f32 v74, v91, v86, v74
	v_max_f32_e32 v74, 0xda24260, v74
	v_cndmask_b32_e64 v91, 0, v179, s[48:49]
	v_sub_f32_e32 v73, v73, v91
	v_log_f32_e32 v86, v74
	v_rcp_f32_e32 v92, v92
	v_and_b32_e32 v84, 0xffff0000, v84
	v_mul_f32_e32 v84, 0xbfb8aa3b, v84
	v_mul_f32_e32 v91, 0x3f317217, v86
	v_fma_f32 v91, v86, s93, -v91
	v_fmac_f32_e32 v91, 0x3377d1cf, v86
	v_fmac_f32_e32 v91, 0x3f317217, v86
	v_exp_f32_e32 v84, v84
	v_add_f32_dpp v3, v3, v3 row_shr:2 row_mask:0xf bank_mask:0xf bound_ctrl:1
	v_mov_b32_e32 v86, v91
	v_sub_f32_e32 v91, 1.0, v75
	v_fmac_f32_e32 v75, v87, v91
	v_max_f32_e32 v75, 0xda24260, v75
	v_log_f32_e32 v87, v75
	v_add_f32_e32 v84, 1.0, v84
	v_rcp_f32_e32 v84, v84
	v_add_f32_dpp v3, v3, v3 row_shr:4 row_mask:0xf bank_mask:0xf bound_ctrl:1
	v_mul_f32_e32 v91, 0x3f317217, v87
	v_fma_f32 v91, v87, s93, -v91
	v_fmac_f32_e32 v91, 0x3377d1cf, v87
	v_fmac_f32_e32 v91, 0x3f317217, v87
	v_add_f32_dpp v244, v3, v3 row_shr:8 row_mask:0xf bank_mask:0xf bound_ctrl:1
	v_add_f32_dpp v3, v80, v80 row_shr:1 row_mask:0xf bank_mask:0xf bound_ctrl:1
	v_mov_b32_e32 v87, v91
	v_sub_f32_e32 v91, 1.0, v68
	v_fma_f32 v68, v92, v91, v68
	v_max_f32_e32 v68, 0xda24260, v68
	v_sub_f32_e32 v229, 1.0, v68
	v_add_f32_dpp v3, v3, v3 row_shr:2 row_mask:0xf bank_mask:0xf bound_ctrl:1
	v_log_f32_e32 v91, v68
	v_lshlrev_b32_e32 v92, 16, v85
	v_add_f32_dpp v3, v3, v3 row_shr:4 row_mask:0xf bank_mask:0xf bound_ctrl:1
	v_and_b32_e32 v85, 0xffff0000, v85
	v_mul_f32_e32 v68, 0x3f317217, v91
	v_fma_f32 v68, v91, s93, -v68
	v_fmac_f32_e32 v68, 0x3377d1cf, v91
	v_fmac_f32_e32 v68, 0x3f317217, v91
	v_add_f32_dpp v243, v3, v3 row_shr:8 row_mask:0xf bank_mask:0xf bound_ctrl:1
	v_add_f32_dpp v3, v81, v81 row_shr:1 row_mask:0xf bank_mask:0xf bound_ctrl:1
	v_sub_f32_e32 v91, 1.0, v69
	v_fma_f32 v69, v84, v91, v69
	v_max_f32_e32 v69, 0xda24260, v69
	v_mul_f32_e32 v91, 0xbfb8aa3b, v92
	v_log_f32_e32 v84, v69
	v_exp_f32_e32 v91, v91
	v_add_f32_dpp v3, v3, v3 row_shr:2 row_mask:0xf bank_mask:0xf bound_ctrl:1
	v_sub_f32_e32 v230, 1.0, v69
	v_mul_f32_e32 v69, 0x3f317217, v84
	v_add_f32_dpp v3, v3, v3 row_shr:4 row_mask:0xf bank_mask:0xf bound_ctrl:1
	v_add_f32_e32 v91, 1.0, v91
	v_fma_f32 v69, v84, s93, -v69
	v_add_f32_dpp v242, v3, v3 row_shr:8 row_mask:0xf bank_mask:0xf bound_ctrl:1
	v_add_f32_dpp v3, v90, v90 row_shr:1 row_mask:0xf bank_mask:0xf bound_ctrl:1
	v_rcp_f32_e32 v91, v91
	v_fmac_f32_e32 v69, 0x3377d1cf, v84
	v_add_f32_dpp v3, v3, v3 row_shr:2 row_mask:0xf bank_mask:0xf bound_ctrl:1
	v_fmac_f32_e32 v69, 0x3f317217, v84
	s_nop 0
	v_add_f32_dpp v3, v3, v3 row_shr:4 row_mask:0xf bank_mask:0xf bound_ctrl:1
	v_mul_f32_e32 v85, 0xbfb8aa3b, v85
	s_nop 0
	v_add_f32_dpp v241, v3, v3 row_shr:8 row_mask:0xf bank_mask:0xf bound_ctrl:1
	v_add_f32_dpp v3, v76, v76 row_shr:1 row_mask:0xf bank_mask:0xf bound_ctrl:1
	v_sub_f32_e32 v84, 1.0, v70
	v_fma_f32 v70, v91, v84, v70
	v_add_f32_dpp v3, v3, v3 row_shr:2 row_mask:0xf bank_mask:0xf bound_ctrl:1
	v_max_f32_e32 v70, 0xda24260, v70
	s_nop 0
	v_add_f32_dpp v3, v3, v3 row_shr:4 row_mask:0xf bank_mask:0xf bound_ctrl:1
	v_exp_f32_e32 v85, v85
	s_nop 0
	v_add_f32_dpp v109, v3, v3 row_shr:8 row_mask:0xf bank_mask:0xf bound_ctrl:1
	v_add_f32_dpp v3, v77, v77 row_shr:1 row_mask:0xf bank_mask:0xf bound_ctrl:1
	v_log_f32_e32 v84, v70
	s_nop 0
	v_add_f32_dpp v3, v3, v3 row_shr:2 row_mask:0xf bank_mask:0xf bound_ctrl:1
	v_sub_f32_e32 v231, 1.0, v70
	v_add_f32_e32 v85, 1.0, v85
	v_add_f32_dpp v3, v3, v3 row_shr:4 row_mask:0xf bank_mask:0xf bound_ctrl:1
	v_mul_f32_e32 v70, 0x3f317217, v84
	v_fma_f32 v70, v84, s93, -v70
	v_add_f32_dpp v108, v3, v3 row_shr:8 row_mask:0xf bank_mask:0xf bound_ctrl:1
	v_add_f32_dpp v3, v89, v89 row_shr:1 row_mask:0xf bank_mask:0xf bound_ctrl:1
	v_rcp_f32_e32 v85, v85
	v_fmac_f32_e32 v70, 0x3377d1cf, v84
	v_add_f32_dpp v3, v3, v3 row_shr:2 row_mask:0xf bank_mask:0xf bound_ctrl:1
	v_fmac_f32_e32 v70, 0x3f317217, v84
	s_nop 0
	v_add_f32_dpp v3, v3, v3 row_shr:4 row_mask:0xf bank_mask:0xf bound_ctrl:1
	s_nop 1
	v_add_f32_dpp v107, v3, v3 row_shr:8 row_mask:0xf bank_mask:0xf bound_ctrl:1
	v_add_f32_dpp v3, v88, v88 row_shr:1 row_mask:0xf bank_mask:0xf bound_ctrl:1
	v_sub_f32_e32 v84, 1.0, v71
	s_nop 0
	v_add_f32_dpp v3, v3, v3 row_shr:2 row_mask:0xf bank_mask:0xf bound_ctrl:1
	v_fmac_f32_e32 v71, v85, v84
	v_max_f32_e32 v71, 0xda24260, v71
	v_add_f32_dpp v3, v3, v3 row_shr:4 row_mask:0xf bank_mask:0xf bound_ctrl:1
	v_sub_f32_e32 v232, 1.0, v71
	s_nop 0
	v_add_f32_dpp v106, v3, v3 row_shr:8 row_mask:0xf bank_mask:0xf bound_ctrl:1
	v_add_f32_dpp v3, v72, v72 row_shr:1 row_mask:0xf bank_mask:0xf bound_ctrl:1
	s_nop 1
	v_add_f32_dpp v3, v3, v3 row_shr:2 row_mask:0xf bank_mask:0xf bound_ctrl:1
	v_log_f32_e32 v84, v71
	s_nop 0
	v_add_f32_dpp v3, v3, v3 row_shr:4 row_mask:0xf bank_mask:0xf bound_ctrl:1
	v_mul_f32_e32 v71, 0x3f317217, v84
	s_nop 0
	v_add_f32_dpp v240, v3, v3 row_shr:8 row_mask:0xf bank_mask:0xf bound_ctrl:1
	v_add_f32_dpp v3, v73, v73 row_shr:1 row_mask:0xf bank_mask:0xf bound_ctrl:1
	v_fma_f32 v71, v84, s93, -v71
	v_fmac_f32_e32 v71, 0x3377d1cf, v84
	v_add_f32_dpp v3, v3, v3 row_shr:2 row_mask:0xf bank_mask:0xf bound_ctrl:1
	v_fmac_f32_e32 v71, 0x3f317217, v84
	s_nop 0
	v_add_f32_dpp v3, v3, v3 row_shr:4 row_mask:0xf bank_mask:0xf bound_ctrl:1
	v_mov_b32_e32 v225, v90
	s_nop 0
	v_add_f32_dpp v239, v3, v3 row_shr:8 row_mask:0xf bank_mask:0xf bound_ctrl:1
	v_add_f32_dpp v3, v86, v86 row_shr:1 row_mask:0xf bank_mask:0xf bound_ctrl:1
	s_nop 1
	v_add_f32_dpp v3, v3, v3 row_shr:2 row_mask:0xf bank_mask:0xf bound_ctrl:1
	v_mov_b32_e32 v226, v81
	v_mov_b32_e32 v228, v80
	v_add_f32_dpp v3, v3, v3 row_shr:4 row_mask:0xf bank_mask:0xf bound_ctrl:1
; #define LAS __attribute__((address_space(3)))
; __device__ __forceinline__ unsigned cvt_pk_bf16(float lo, float hi) { unsigned r; asm volatile("v_cvt_pk_bf16_f32 %0, %1, %2" : "=v"(r) : "v"(lo), "v"(hi)); return r; }
; template <int CTRL> __device__ __forceinline__ float dpp_add0(float x) { return x + dppf<CTRL>(0.0f, x); }
; template <bool WITHO, bool RAW = false>
; __device__ __forceinline__ void hg_pass(const Frame& F, const bf16_t* P, const float* lbh, int b, int h, int nb, int dir, f32x4 (&S)[4][4], float (&Gsum)[16],
;                                         LAS bf16_t* Vl, LAS bf16_t* Kl, float* OF, const float* ngp) {
;     ...
;         float G[16];
; #pragma unroll
;         for (int q = 0; q < 16; ++q) G[q] = c[q];
; #pragma unroll
;         for (int q = 0; q < 16; q += 4) ROW_ALLREDUCE4(G[q], G[q + 1], G[q + 2], G[q + 3]);
; #pragma unroll
;         for (int q = 0; q < 16; ++q) { c[q] = dpp_add0<0x111>(c[q]); c[q] = dpp_add0<0x112>(c[q]); c[q] = dpp_add0<0x114>(c[q]); c[q] = dpp_add0<0x118>(c[q]); }
; #pragma unroll
;         for (int q = 0; q < 16; ++q) Gsum[q] += G[q];
; #pragma unroll
;         for (int m = 0; m < 4; ++m) { float kh[4];
; #pragma unroll
;             for (int i = 0; i < 4; ++i) kh[i] = kk[m * 4 + i] * __expf(G[m * 4 + i] - c[m * 4 + i]);
;             u32x2 w; w.x = cvt_pk_bf16(kh[0], kh[1]); w.y = cvt_pk_bf16(kh[2], kh[3]);
;             *(LAS u32x2*)(Kl + tau * 64 + 16 * m + 4 * g) = w; }
	s_nop 1
	v_add_f32_dpp v227, v227, v227 quad_perm:[1,0,3,2] row_mask:0xf bank_mask:0xf
	v_add_f32_dpp v228, v228, v228 quad_perm:[1,0,3,2] row_mask:0xf bank_mask:0xf
	v_add_f32_dpp v226, v226, v226 quad_perm:[1,0,3,2] row_mask:0xf bank_mask:0xf
	v_add_f32_dpp v225, v225, v225 quad_perm:[1,0,3,2] row_mask:0xf bank_mask:0xf
	v_add_f32_dpp v227, v227, v227 quad_perm:[2,3,0,1] row_mask:0xf bank_mask:0xf
	v_add_f32_dpp v228, v228, v228 quad_perm:[2,3,0,1] row_mask:0xf bank_mask:0xf
	v_add_f32_dpp v226, v226, v226 quad_perm:[2,3,0,1] row_mask:0xf bank_mask:0xf
	v_add_f32_dpp v225, v225, v225 quad_perm:[2,3,0,1] row_mask:0xf bank_mask:0xf
	v_add_f32_dpp v227, v227, v227 row_half_mirror row_mask:0xf bank_mask:0xf
	v_add_f32_dpp v228, v228, v228 row_half_mirror row_mask:0xf bank_mask:0xf
	v_add_f32_dpp v226, v226, v226 row_half_mirror row_mask:0xf bank_mask:0xf
	v_add_f32_dpp v225, v225, v225 row_half_mirror row_mask:0xf bank_mask:0xf
	v_add_f32_dpp v227, v227, v227 row_mirror row_mask:0xf bank_mask:0xf
	v_add_f32_dpp v228, v228, v228 row_mirror row_mask:0xf bank_mask:0xf
	v_add_f32_dpp v226, v226, v226 row_mirror row_mask:0xf bank_mask:0xf
	v_add_f32_dpp v225, v225, v225 row_mirror row_mask:0xf bank_mask:0xf
	v_mov_b32_e32 v215, v68
	v_mov_b32_e32 v216, v69
	v_add_f32_dpp v238, v3, v3 row_shr:8 row_mask:0xf bank_mask:0xf bound_ctrl:1
	v_add_f32_dpp v3, v87, v87 row_shr:1 row_mask:0xf bank_mask:0xf bound_ctrl:1
	v_mov_b32_e32 v213, v70
	v_mov_b32_e32 v221, v89
	v_add_f32_dpp v3, v3, v3 row_shr:2 row_mask:0xf bank_mask:0xf bound_ctrl:1
	v_mov_b32_e32 v223, v77
	v_mov_b32_e32 v222, v88
	v_add_f32_dpp v3, v3, v3 row_shr:4 row_mask:0xf bank_mask:0xf bound_ctrl:1
	v_mov_b32_e32 v224, v76
	v_mov_b32_e32 v218, v73
	v_add_f32_dpp v237, v3, v3 row_shr:8 row_mask:0xf bank_mask:0xf bound_ctrl:1
	v_add_f32_dpp v3, v68, v68 row_shr:1 row_mask:0xf bank_mask:0xf bound_ctrl:1
	v_sub_f32_e32 v68, v228, v243
	v_mul_f32_e32 v68, 0x3fb8aa3b, v68
	v_add_f32_dpp v3, v3, v3 row_shr:2 row_mask:0xf bank_mask:0xf bound_ctrl:1
	v_exp_f32_e32 v68, v68
	v_mov_b32_e32 v217, v87
	v_add_f32_dpp v3, v3, v3 row_shr:4 row_mask:0xf bank_mask:0xf bound_ctrl:1
	v_mov_b32_e32 v220, v72
	v_mov_b32_e32 v219, v86
	v_add_f32_dpp v236, v3, v3 row_shr:8 row_mask:0xf bank_mask:0xf bound_ctrl:1
	v_add_f32_dpp v3, v69, v69 row_shr:1 row_mask:0xf bank_mask:0xf bound_ctrl:1
	v_sub_f32_e32 v69, v226, v242
	v_mul_f32_e32 v69, 0x3fb8aa3b, v69
	v_add_f32_dpp v3, v3, v3 row_shr:2 row_mask:0xf bank_mask:0xf bound_ctrl:1
	v_exp_f32_e32 v69, v69
	v_mov_b32_e32 v214, v71
	v_add_f32_dpp v3, v3, v3 row_shr:4 row_mask:0xf bank_mask:0xf bound_ctrl:1
	v_mul_f32_e32 v68, v101, v68
	v_sub_f32_e32 v83, 1.0, v83
	v_add_f32_dpp v235, v3, v3 row_shr:8 row_mask:0xf bank_mask:0xf bound_ctrl:1
	v_add_f32_dpp v3, v70, v70 row_shr:1 row_mask:0xf bank_mask:0xf bound_ctrl:1
	v_sub_f32_e32 v70, v225, v241
	v_mul_f32_e32 v70, 0x3fb8aa3b, v70
	v_add_f32_dpp v3, v3, v3 row_shr:2 row_mask:0xf bank_mask:0xf bound_ctrl:1
	v_exp_f32_e32 v70, v70
	s_nop 1
	v_add_f32_dpp v224, v224, v224 quad_perm:[1,0,3,2] row_mask:0xf bank_mask:0xf
	v_add_f32_dpp v223, v223, v223 quad_perm:[1,0,3,2] row_mask:0xf bank_mask:0xf
	v_add_f32_dpp v221, v221, v221 quad_perm:[1,0,3,2] row_mask:0xf bank_mask:0xf
	v_add_f32_dpp v222, v222, v222 quad_perm:[1,0,3,2] row_mask:0xf bank_mask:0xf
	v_add_f32_dpp v224, v224, v224 quad_perm:[2,3,0,1] row_mask:0xf bank_mask:0xf
	v_add_f32_dpp v223, v223, v223 quad_perm:[2,3,0,1] row_mask:0xf bank_mask:0xf
	v_add_f32_dpp v221, v221, v221 quad_perm:[2,3,0,1] row_mask:0xf bank_mask:0xf
	v_add_f32_dpp v222, v222, v222 quad_perm:[2,3,0,1] row_mask:0xf bank_mask:0xf
	v_add_f32_dpp v224, v224, v224 row_half_mirror row_mask:0xf bank_mask:0xf
	v_add_f32_dpp v223, v223, v223 row_half_mirror row_mask:0xf bank_mask:0xf
	v_add_f32_dpp v221, v221, v221 row_half_mirror row_mask:0xf bank_mask:0xf
	v_add_f32_dpp v222, v222, v222 row_half_mirror row_mask:0xf bank_mask:0xf
	v_add_f32_dpp v224, v224, v224 row_mirror row_mask:0xf bank_mask:0xf
	v_add_f32_dpp v223, v223, v223 row_mirror row_mask:0xf bank_mask:0xf
	v_add_f32_dpp v221, v221, v221 row_mirror row_mask:0xf bank_mask:0xf
	v_add_f32_dpp v222, v222, v222 row_mirror row_mask:0xf bank_mask:0xf
	s_nop 1
	v_add_f32_dpp v220, v220, v220 quad_perm:[1,0,3,2] row_mask:0xf bank_mask:0xf
	v_add_f32_dpp v218, v218, v218 quad_perm:[1,0,3,2] row_mask:0xf bank_mask:0xf
	v_add_f32_dpp v219, v219, v219 quad_perm:[1,0,3,2] row_mask:0xf bank_mask:0xf
	v_add_f32_dpp v217, v217, v217 quad_perm:[1,0,3,2] row_mask:0xf bank_mask:0xf
	v_add_f32_dpp v220, v220, v220 quad_perm:[2,3,0,1] row_mask:0xf bank_mask:0xf
	v_add_f32_dpp v218, v218, v218 quad_perm:[2,3,0,1] row_mask:0xf bank_mask:0xf
	v_add_f32_dpp v219, v219, v219 quad_perm:[2,3,0,1] row_mask:0xf bank_mask:0xf
	v_add_f32_dpp v217, v217, v217 quad_perm:[2,3,0,1] row_mask:0xf bank_mask:0xf
	v_add_f32_dpp v220, v220, v220 row_half_mirror row_mask:0xf bank_mask:0xf
	v_add_f32_dpp v218, v218, v218 row_half_mirror row_mask:0xf bank_mask:0xf
	v_add_f32_dpp v219, v219, v219 row_half_mirror row_mask:0xf bank_mask:0xf
	v_add_f32_dpp v217, v217, v217 row_half_mirror row_mask:0xf bank_mask:0xf
	v_add_f32_dpp v220, v220, v220 row_mirror row_mask:0xf bank_mask:0xf
	v_add_f32_dpp v218, v218, v218 row_mirror row_mask:0xf bank_mask:0xf
	v_add_f32_dpp v219, v219, v219 row_mirror row_mask:0xf bank_mask:0xf
	v_add_f32_dpp v217, v217, v217 row_mirror row_mask:0xf bank_mask:0xf
	s_nop 1
	v_add_f32_dpp v215, v215, v215 quad_perm:[1,0,3,2] row_mask:0xf bank_mask:0xf
	v_add_f32_dpp v216, v216, v216 quad_perm:[1,0,3,2] row_mask:0xf bank_mask:0xf
; #define LAS __attribute__((address_space(3)))
; __device__ __forceinline__ unsigned cvt_pk_bf16(float lo, float hi) { unsigned r; asm volatile("v_cvt_pk_bf16_f32 %0, %1, %2" : "=v"(r) : "v"(lo), "v"(hi)); return r; }
; template <int CTRL> __device__ __forceinline__ float dpp_add0(float x) { return x + dppf<CTRL>(0.0f, x); }
; template <bool WITHO, bool RAW = false>
; __device__ __forceinline__ void hg_pass(const Frame& F, const bf16_t* P, const float* lbh, int b, int h, int nb, int dir, f32x4 (&S)[4][4], float (&Gsum)[16],
;                                         LAS bf16_t* Vl, LAS bf16_t* Kl, float* OF, const float* ngp) {
;     ...
;         for (int q = 0; q < 16; q += 4) ROW_ALLREDUCE4(G[q], G[q + 1], G[q + 2], G[q + 3]);
; #pragma unroll
;         for (int q = 0; q < 16; ++q) { c[q] = dpp_add0<0x111>(c[q]); c[q] = dpp_add0<0x112>(c[q]); c[q] = dpp_add0<0x114>(c[q]); c[q] = dpp_add0<0x118>(c[q]); }
; #pragma unroll
;         for (int q = 0; q < 16; ++q) Gsum[q] += G[q];
; #pragma unroll
;         for (int m = 0; m < 4; ++m) { float kh[4];
; #pragma unroll
;             for (int i = 0; i < 4; ++i) kh[i] = kk[m * 4 + i] * __expf(G[m * 4 + i] - c[m * 4 + i]);
;             u32x2 w; w.x = cvt_pk_bf16(kh[0], kh[1]); w.y = cvt_pk_bf16(kh[2], kh[3]);
;             *(LAS u32x2*)(Kl + tau * 64 + 16 * m + 4 * g) = w; }
;         float ofv[4][4], gtv[4][4]; int orow[4];
;         if (WITHO) {
; #pragma unroll
;             for (int i = 0; i < 4; ++i) { const int p2 = ci * 16 + 4 * g + i, t2 = dir ? (HG_U - 1 - p2) : p2; orow[i] = hg_row(b, nb, t2); }
	v_add_f32_dpp v213, v213, v213 quad_perm:[1,0,3,2] row_mask:0xf bank_mask:0xf
	v_add_f32_dpp v214, v214, v214 quad_perm:[1,0,3,2] row_mask:0xf bank_mask:0xf
	v_add_f32_dpp v215, v215, v215 quad_perm:[2,3,0,1] row_mask:0xf bank_mask:0xf
	v_add_f32_dpp v216, v216, v216 quad_perm:[2,3,0,1] row_mask:0xf bank_mask:0xf
	v_add_f32_dpp v213, v213, v213 quad_perm:[2,3,0,1] row_mask:0xf bank_mask:0xf
	v_add_f32_dpp v214, v214, v214 quad_perm:[2,3,0,1] row_mask:0xf bank_mask:0xf
	v_add_f32_dpp v215, v215, v215 row_half_mirror row_mask:0xf bank_mask:0xf
	v_add_f32_dpp v216, v216, v216 row_half_mirror row_mask:0xf bank_mask:0xf
	v_add_f32_dpp v213, v213, v213 row_half_mirror row_mask:0xf bank_mask:0xf
	v_add_f32_dpp v214, v214, v214 row_half_mirror row_mask:0xf bank_mask:0xf
	v_add_f32_dpp v215, v215, v215 row_mirror row_mask:0xf bank_mask:0xf
	v_add_f32_dpp v216, v216, v216 row_mirror row_mask:0xf bank_mask:0xf
	v_add_f32_dpp v213, v213, v213 row_mirror row_mask:0xf bank_mask:0xf
	v_add_f32_dpp v214, v214, v214 row_mirror row_mask:0xf bank_mask:0xf
	v_mul_f32_e32 v69, v82, v69
	v_add_f32_dpp v3, v3, v3 row_shr:4 row_mask:0xf bank_mask:0xf bound_ctrl:1
	v_mul_f32_e32 v70, v83, v70
	v_sub_f32_e32 v74, 1.0, v74
	v_add_f32_dpp v234, v3, v3 row_shr:8 row_mask:0xf bank_mask:0xf bound_ctrl:1
	v_add_f32_dpp v3, v71, v71 row_shr:1 row_mask:0xf bank_mask:0xf bound_ctrl:1
	v_sub_f32_e32 v75, 1.0, v75
	s_andn2_b64 vcc, exec, s[4:5]
	v_add_f32_dpp v3, v3, v3 row_shr:2 row_mask:0xf bank_mask:0xf bound_ctrl:1
	s_nop 1
	v_add_f32_dpp v3, v3, v3 row_shr:4 row_mask:0xf bank_mask:0xf bound_ctrl:1
	s_nop 1
	v_add_f32_dpp v233, v3, v3 row_shr:8 row_mask:0xf bank_mask:0xf bound_ctrl:1
	v_sub_f32_e32 v3, v227, v244
	v_mul_f32_e32 v3, 0x3fb8aa3b, v3
	v_exp_f32_e32 v3, v3
	s_nop 0
	v_mul_f32_e32 v3, v100, v3
	v_cvt_pk_bf16_f32 v68, v3, v68
	v_cvt_pk_bf16_f32 v69, v69, v70
	ds_write_b64 v191, v[68:69] offset:34816
	v_sub_f32_e32 v68, v223, v108
	v_sub_f32_e32 v3, v224, v109
	v_mul_f32_e32 v68, 0x3fb8aa3b, v68
	v_sub_f32_e32 v69, v221, v107
	v_mul_f32_e32 v3, 0x3fb8aa3b, v3
	v_exp_f32_e32 v68, v68
	v_mul_f32_e32 v69, 0x3fb8aa3b, v69
	v_sub_f32_e32 v70, v222, v106
	v_exp_f32_e32 v3, v3
	v_exp_f32_e32 v69, v69
	v_mul_f32_e32 v70, 0x3fb8aa3b, v70
	v_exp_f32_e32 v70, v70
	v_mul_f32_e32 v68, v103, v68
	v_mul_f32_e32 v3, v102, v3
	v_mul_f32_e32 v69, v104, v69
	v_cvt_pk_bf16_f32 v68, v3, v68
	v_mul_f32_e32 v70, v105, v70
	v_cvt_pk_bf16_f32 v69, v69, v70
	ds_write_b64 v191, v[68:69] offset:34848
	v_sub_f32_e32 v68, v218, v239
	v_sub_f32_e32 v3, v220, v240
	v_mul_f32_e32 v68, 0x3fb8aa3b, v68
	v_sub_f32_e32 v69, v219, v238
	v_mul_f32_e32 v3, 0x3fb8aa3b, v3
	v_exp_f32_e32 v68, v68
	v_mul_f32_e32 v69, 0x3fb8aa3b, v69
	v_sub_f32_e32 v70, v217, v237
	v_exp_f32_e32 v3, v3
	v_exp_f32_e32 v69, v69
	v_mul_f32_e32 v70, 0x3fb8aa3b, v70
	v_exp_f32_e32 v70, v70
	v_mul_f32_e32 v68, v79, v68
	v_mul_f32_e32 v3, v78, v3
	v_mul_f32_e32 v69, v74, v69
	v_cvt_pk_bf16_f32 v68, v3, v68
	v_mul_f32_e32 v70, v75, v70
	v_cvt_pk_bf16_f32 v69, v69, v70
	ds_write_b64 v191, v[68:69] offset:34880
	v_sub_f32_e32 v68, v216, v235
	v_sub_f32_e32 v3, v215, v236
	v_mul_f32_e32 v68, 0x3fb8aa3b, v68
	v_sub_f32_e32 v69, v213, v234
	v_mul_f32_e32 v3, 0x3fb8aa3b, v3
	v_exp_f32_e32 v68, v68
	v_mul_f32_e32 v69, 0x3fb8aa3b, v69
	v_sub_f32_e32 v70, v214, v233
	v_exp_f32_e32 v3, v3
	v_exp_f32_e32 v69, v69
	v_mul_f32_e32 v70, 0x3fb8aa3b, v70
	v_exp_f32_e32 v70, v70
	v_mul_f32_e32 v68, v230, v68
	v_mul_f32_e32 v3, v229, v3
	v_mul_f32_e32 v69, v231, v69
	v_cvt_pk_bf16_f32 v68, v3, v68
	v_mul_f32_e32 v70, v232, v70
	v_cvt_pk_bf16_f32 v69, v69, v70
	ds_write_b64 v191, v[68:69] offset:34912
	v_add_u32_e32 v68, s26, v193
	v_add_u32_e32 v3, s27, v114
	v_add_u32_e32 v69, 0x7f, v68
	v_cndmask_b32_e64 v69, v69, v3, s[0:1]
	v_add_u32_e32 v172, s25, v69
	v_add_u32_e32 v69, 1, v3
	v_add_u32_e32 v70, 0x7e, v68
	v_cndmask_b32_e64 v69, v70, v69, s[0:1]
	v_add_u32_e32 v90, s25, v69
	v_add_u32_e32 v69, 2, v3
	v_add_u32_e32 v70, 0x7d, v68
	v_add_u32_e32 v3, 3, v3
	v_add_u32_e32 v68, 0x7c, v68
	v_cndmask_b32_e64 v69, v70, v69, s[0:1]
	v_cndmask_b32_e64 v3, v68, v3, s[0:1]
	v_add_u32_e32 v86, s25, v69
	v_add_u32_e32 v70, s25, v3
	v_ashrrev_i32_e32 v173, 31, v172
	v_ashrrev_i32_e32 v91, 31, v90
	v_ashrrev_i32_e32 v87, 31, v86
	v_ashrrev_i32_e32 v71, 31, v70
	s_cbranch_vccnz .LBB0_1174
; __device__ __forceinline__ float bf2f(unsigned short b) { return __uint_as_float(((unsigned)b) << 16); }
; template <bool WITHO, bool RAW = false>
; __device__ __forceinline__ void hg_pass(const Frame& F, const bf16_t* P, const float* lbh, int b, int h, int nb, int dir, f32x4 (&S)[4][4], float (&Gsum)[16],
;                                         LAS bf16_t* Vl, LAS bf16_t* Kl, float* OF, const float* ngp) {
;     ...
;             if (dir && !RAW) {
; #pragma unroll
;                 for (int i = 0; i < 4; ++i)
; #pragma unroll
;                     for (int vt = 0; vt < 4; ++vt) { ofv[i][vt] = OF[(size_t)orow[i] * 512 + h * 64 + 16 * vt + tau]; gtv[i][vt] = bf2f(P[(size_t)orow[i] * 4096 + 3584 + h * 64 + 16 * vt + tau]); }
;             }
	v_lshlrev_b64 v[72:73], 13, v[172:173]
	v_lshl_add_u64 v[72:73], v[132:133], 0, v[72:73]
	v_add_co_u32_e32 v72, vcc, 0x1000, v72
	v_lshlrev_b64 v[80:81], 13, v[90:91]
	s_nop 0
	v_addc_co_u32_e32 v73, vcc, 0, v73, vcc
	v_lshl_add_u64 v[80:81], v[132:133], 0, v[80:81]
	v_lshlrev_b64 v[76:77], 11, v[90:91]
	v_add_co_u32_e32 v80, vcc, s97, v80
	v_lshl_add_u64 v[76:77], v[130:131], 0, v[76:77]
	s_nop 0
	v_addc_co_u32_e32 v81, vcc, 0, v81, vcc
	global_load_dword v197, v[76:77], off
	global_load_dword v198, v[76:77], off offset:64
	global_load_ushort v3, v[80:81], off offset:3104
	global_load_ushort v84, v[80:81], off offset:3168
	global_load_ushort v85, v[80:81], off offset:3136
	global_load_ushort v88, v[80:81], off offset:3072
	global_load_dword v199, v[76:77], off offset:128
	global_load_dword v200, v[76:77], off offset:192
	v_lshlrev_b64 v[80:81], 13, v[86:87]
	v_lshl_add_u64 v[80:81], v[132:133], 0, v[80:81]
	v_lshlrev_b64 v[76:77], 11, v[86:87]
	v_add_co_u32_e32 v80, vcc, s97, v80
	v_lshl_add_u64 v[76:77], v[130:131], 0, v[76:77]
	s_nop 0
	v_addc_co_u32_e32 v81, vcc, 0, v81, vcc
	global_load_dword v201, v[76:77], off
	global_load_dword v202, v[76:77], off offset:64
	global_load_ushort v89, v[80:81], off offset:3104
	global_load_ushort v92, v[80:81], off offset:3136
	global_load_ushort v93, v[80:81], off offset:3168
	global_load_ushort v160, v[80:81], off offset:3072
	global_load_dword v203, v[76:77], off offset:128
	global_load_dword v204, v[76:77], off offset:192
	v_lshlrev_b64 v[80:81], 13, v[70:71]
	v_lshl_add_u64 v[80:81], v[132:133], 0, v[80:81]
	v_lshlrev_b64 v[76:77], 11, v[70:71]
	v_add_co_u32_e32 v80, vcc, s97, v80
	v_lshlrev_b64 v[68:69], 11, v[172:173]
	v_lshl_add_u64 v[76:77], v[130:131], 0, v[76:77]
	v_addc_co_u32_e32 v81, vcc, 0, v81, vcc
	v_lshl_add_u64 v[68:69], v[130:131], 0, v[68:69]
	global_load_dword v205, v[76:77], off
	global_load_dword v206, v[76:77], off offset:64
	global_load_ushort v164, v[80:81], off offset:3072
	global_load_ushort v165, v[80:81], off offset:3104
	global_load_dword v209, v[76:77], off offset:128
	global_load_ushort v170, v[80:81], off offset:3136
	s_nop 0
	global_load_ushort v80, v[80:81], off offset:3168
	s_nop 0
	global_load_dword v212, v[76:77], off offset:192
	s_nop 0
	global_load_ushort v76, v[72:73], off offset:3136
	global_load_ushort v77, v[72:73], off offset:3168
	global_load_ushort v81, v[72:73], off offset:3072
	s_nop 0
	global_load_ushort v72, v[72:73], off offset:3104
	s_nop 0
	global_load_dword v207, v[68:69], off
	global_load_dword v208, v[68:69], off offset:64
	global_load_dword v210, v[68:69], off offset:128
	global_load_dword v211, v[68:69], off offset:192
	s_waitcnt vmcnt(0)
	v_lshlrev_b32_e32 v156, 16, v3
	v_lshlrev_b32_e32 v158, 16, v84
	v_lshlrev_b32_e32 v159, 16, v85
	v_lshlrev_b32_e32 v157, 16, v88
	v_lshlrev_b32_e32 v162, 16, v92
	v_lshlrev_b32_e32 v163, 16, v93
	v_lshlrev_b32_e32 v161, 16, v160
	v_lshlrev_b32_e32 v160, 16, v89
	v_lshlrev_b32_e32 v165, 16, v165
	v_lshlrev_b32_e32 v164, 16, v164
	v_lshlrev_b32_e32 v171, 16, v80
	v_lshlrev_b32_e32 v170, 16, v170
	v_lshlrev_b32_e32 v169, 16, v76
	v_lshlrev_b32_e32 v168, 16, v77
	v_lshlrev_b32_e32 v167, 16, v81
	v_lshlrev_b32_e32 v166, 16, v72
